# hand-written weight converter (register transpose, row-contiguous item order, 4 slots in flight)
# baseline (speedup 1.0000x reference)
.LBB0_6:
	s_cmp_gt_i32 s12, 0
	s_cbranch_scc1 .LBB0_225
	v_readlane_b32 s0, v254, 0
	s_lshl_b32 s0, s0, 3
	v_readlane_b32 s2, v254, 41
	v_mbcnt_lo_u32_b32 v0, -1, 0
	s_add_i32 s6, s2, s0
	s_mov_b32 s1, 0
	v_mbcnt_hi_u32_b32 v14, -1, v0
	s_cmpk_gt_i32 s6, 0x6a7f
	s_branch .Lcvt_site_102
.Lcvt_site_102:
	s_waitcnt vmcnt(0) lgkmcnt(0)
	v_readlane_b32 s0, v254, 42
	v_readlane_b32 s1, v254, 43
	v_readlane_b32 s60, v254, 0
	v_readlane_b32 s61, v254, 41
	s_nop 3
	s_sub_u32 s0, s0, 0xd0
	s_subb_u32 s1, s1, 0
	s_lshl_b32 s9, s60, 3
	s_add_u32 s9, s9, s61
	s_min_u32 s20, s74, 0x100
	s_lshl_b32 s20, s20, 3
	s_load_dwordx2 s[10:11], s[0:1], 0x10
	s_load_dwordx2 s[12:13], s[0:1], 0x18
	s_load_dwordx2 s[14:15], s[0:1], 0x88
	s_load_dwordx2 s[28:29], s[0:1], 0x90
	s_load_dwordx2 s[38:39], s[0:1], 0x98
	s_load_dwordx2 s[44:45], s[0:1], 0xa0
	s_load_dwordx2 s[46:47], s[0:1], 0xa8
	s_load_dwordx2 s[48:49], s[0:1], 0xb8
	v_mbcnt_lo_u32_b32 v100, -1, 0
	v_mbcnt_hi_u32_b32 v100, -1, v100
	v_and_b32_e32 v96, 7, v100
	v_lshrrev_b32_e32 v97, 3, v100
	v_mov_b32_e32 v98, 0x43e00000
	s_mov_b32 s64, 0xc3e00000
	s_waitcnt lgkmcnt(0)
	s_lshl_b32 s32, s9, 2
	s_lshl_b32 s20, s20, 2
	s_mov_b32 s41, 0
	s_cmp_lt_u32 s32, 0x6a80
	s_cbranch_scc0 .Lcv102_drain0
	s_add_u32 s43, s32, 0
	s_cmp_lt_u32 s43, 0x600
	s_cbranch_scc0 .Lcv102_d0_b
	s_mul_i32 s58, s43, 0xaaab
	s_lshr_b32 s58, s58, 22
	s_mul_i32 s59, s58, 96
	s_sub_u32 s59, s43, s59
	s_mul_i32 s60, s58, 0xc0000
	s_mul_i32 s81, s59, 0x80
	s_add_u32 s60, s60, s81
	s_add_u32 s2, s10, s60
	s_addc_u32 s3, s11, 0
	s_mov_b32 s63, 0x3000
	s_mul_i32 s61, s59, 0x8000
	s_mul_i32 s81, s58, 0x40
	s_add_u32 s61, s61, s81
	s_add_u32 s61, s61, 0x800000
	s_add_u32 s50, s48, s61
	s_addc_u32 s51, s49, 0
	s_mov_b32 s65, 0x400
	s_mov_b32 s71, 0x44000000
	s_branch .Lcv102_d0_ld
.Lcv102_d0_b:
	s_sub_u32 s43, s43, 0x600
	s_cmp_lt_u32 s43, 0x200
	s_cbranch_scc0 .Lcv102_d0_c
	s_lshr_b32 s58, s43, 5
	s_and_b32 s59, s43, 31
	s_mul_i32 s60, s58, 0x40000
	s_mul_i32 s81, s59, 0x80
	s_add_u32 s60, s60, s81
	s_add_u32 s2, s12, s60
	s_addc_u32 s3, s13, 0
	s_mov_b32 s63, 0x1000
	s_mul_i32 s61, s59, 0x8000
	s_mul_i32 s81, s58, 0x40
	s_add_u32 s61, s61, s81
	s_add_u32 s61, s61, 0xe00000
	s_add_u32 s50, s48, s61
	s_addc_u32 s51, s49, 0
	s_mov_b32 s65, 0x400
	s_mov_b32 s71, 0x44800000
	s_branch .Lcv102_d0_ld
.Lcv102_d0_c:
	s_sub_u32 s43, s43, 0x200
	s_cmp_lt_u32 s43, 0x2000
	s_cbranch_scc0 .Lcv102_d0_dd
	s_lshr_b32 s80, s43, 8
	s_and_b32 s59, s43, 15
	s_bfe_u32 s58, s43, 0x40004
	s_lshr_b32 s81, s59, 2
	s_mul_i32 s61, s81, 0x40000
	s_and_b32 s81, s59, 3
	s_mul_i32 s81, s81, 0x8000
	s_add_u32 s61, s61, s81
	s_mul_i32 s81, s80, 0x100000
	s_add_u32 s61, s61, s81
	s_lshl_b32 s81, s58, 6
	s_add_u32 s61, s61, s81
	s_add_u32 s61, s61, 0x1000000
	s_add_u32 s50, s48, s61
	s_addc_u32 s51, s49, 0
	s_mul_i32 s60, s80, 0x200000
	s_mul_i32 s81, s58, 0x20000
	s_add_u32 s60, s60, s81
	s_lshl_b32 s81, s59, 7
	s_add_u32 s60, s60, s81
	s_add_u32 s2, s14, s60
	s_addc_u32 s3, s15, 0
	s_mov_b32 s63, 0x800
	s_mov_b32 s65, 0x400
	s_mov_b32 s71, 0x44000000
	s_branch .Lcv102_d0_ld
.Lcv102_d0_dd:
	s_sub_u32 s43, s43, 0x2000
	s_cmp_lt_u32 s43, 0x2000
	s_cbranch_scc0 .Lcv102_d0_e
	s_lshr_b32 s80, s43, 8
	s_and_b32 s59, s43, 15
	s_bfe_u32 s58, s43, 0x40004
	s_lshr_b32 s81, s59, 2
	s_mul_i32 s61, s81, 0x40000
	s_and_b32 s81, s59, 3
	s_mul_i32 s81, s81, 0x8000
	s_add_u32 s61, s61, s81
	s_mul_i32 s81, s80, 0x100000
	s_add_u32 s61, s61, s81
	s_lshl_b32 s81, s58, 6
	s_add_u32 s61, s61, s81
	s_add_u32 s61, s61, 0x1020000
	s_add_u32 s50, s48, s61
	s_addc_u32 s51, s49, 0
	s_mul_i32 s60, s80, 0x200000
	s_mul_i32 s81, s58, 0x20000
	s_add_u32 s60, s60, s81
	s_lshl_b32 s81, s59, 7
	s_add_u32 s60, s60, s81
	s_add_u32 s2, s28, s60
	s_addc_u32 s3, s29, 0
	s_mov_b32 s63, 0x800
	s_mov_b32 s65, 0x400
	s_mov_b32 s71, 0x44000000
	s_branch .Lcv102_d0_ld
.Lcv102_d0_e:
	s_sub_u32 s43, s43, 0x2000
	s_cmp_lt_u32 s43, 0x2000
	s_cbranch_scc0 .Lcv102_d0_f
	s_lshr_b32 s80, s43, 8
	s_and_b32 s59, s43, 31
	s_bfe_u32 s58, s43, 0x30005
	s_mul_i32 s60, s80, 0x200000
	s_mul_i32 s81, s58, 0x40000
	s_add_u32 s60, s60, s81
	s_mul_i32 s81, s59, 0x80
	s_add_u32 s60, s60, s81
	s_add_u32 s2, s38, s60
	s_addc_u32 s3, s39, 0
	s_mov_b32 s63, 0x1000
	s_mul_i32 s61, s80, 0x80000
	s_mul_i32 s81, s59, 0x4000
	s_add_u32 s61, s61, s81
	s_mul_i32 s81, s58, 0x40
	s_add_u32 s61, s61, s81
	s_add_u32 s61, s61, 0x5000000
	s_add_u32 s50, s48, s61
	s_addc_u32 s51, s49, 0
	s_mov_b32 s65, 0x200
	s_mov_b32 s71, 0x44800000
	s_branch .Lcv102_d0_ld
.Lcv102_d0_f:
	s_sub_u32 s43, s43, 0x2000
	s_cmp_lt_u32 s43, 0x200
	s_cbranch_scc0 .Lcv102_d0_g
	s_lshr_b32 s58, s43, 5
	s_and_b32 s59, s43, 31
	s_mul_i32 s60, s58, 0x40000
	s_mul_i32 s81, s59, 0x80
	s_add_u32 s60, s60, s81
	s_add_u32 s2, s44, s60
	s_addc_u32 s3, s45, 0
	s_mov_b32 s63, 0x1000
	s_mul_i32 s61, s59, 0x10000
	s_mul_i32 s81, s58, 0x80
	s_add_u32 s61, s61, s81
	s_add_u32 s61, s61, 0x7000000
	s_add_u32 s50, s48, s61
	s_addc_u32 s51, s49, 0
	s_mov_b32 s65, 0x800
	s_mov_b32 s71, 0x0
	s_branch .Lcv102_d0_ld
.Lcv102_d0_g:
	s_sub_u32 s43, s43, 0x200
	s_lshr_b32 s58, s43, 5
	s_and_b32 s59, s43, 31
	s_mul_i32 s60, s58, 0x40000
	s_mul_i32 s81, s59, 0x80
	s_add_u32 s60, s60, s81
	s_add_u32 s2, s46, s60
	s_addc_u32 s3, s47, 0
	s_mov_b32 s63, 0x1000
	s_mul_i32 s61, s59, 0x4000
	s_mul_i32 s81, s58, 0x80
	s_add_u32 s61, s61, s81
	s_add_u32 s61, s61, 0x7200000
	s_add_u32 s50, s48, s61
	s_addc_u32 s51, s49, 0
	s_mov_b32 s65, 0x200
	s_mov_b32 s71, 0x0
	s_branch .Lcv102_d0_ld
.Lcv102_d0_ld:
	s_lshl_b32 s60, s63, 3
	v_mul_lo_u32 v0, v96, s60
	v_lshl_add_u32 v0, v97, 4, v0
	v_add_u32_e32 v4, s63, v0
	v_add_u32_e32 v10, s63, v4
	v_add_u32_e32 v11, s63, v10
	v_add_u32_e32 v12, s63, v11
	v_add_u32_e32 v19, s63, v12
	v_add_u32_e32 v24, s63, v19
	v_add_u32_e32 v25, s63, v24
	global_load_dwordx4 v[34:37], v0, s[2:3] nt
	global_load_dwordx4 v[38:41], v4, s[2:3] nt
	global_load_dwordx4 v[42:45], v10, s[2:3] nt
	global_load_dwordx4 v[46:49], v11, s[2:3] nt
	global_load_dwordx4 v[50:53], v12, s[2:3] nt
	global_load_dwordx4 v[54:57], v19, s[2:3] nt
	global_load_dwordx4 v[58:61], v24, s[2:3] nt
	global_load_dwordx4 v[62:65], v25, s[2:3] nt
	s_mov_b32 s41, 1
	s_cmp_lt_u32 s32, 0x6a80
	s_cbranch_scc0 .Lcv102_drain0
	s_add_u32 s43, s32, 1
	s_cmp_lt_u32 s43, 0x600
	s_cbranch_scc0 .Lcv102_d1_b
	s_mul_i32 s58, s43, 0xaaab
	s_lshr_b32 s58, s58, 22
	s_mul_i32 s59, s58, 96
	s_sub_u32 s59, s43, s59
	s_mul_i32 s60, s58, 0xc0000
	s_mul_i32 s81, s59, 0x80
	s_add_u32 s60, s60, s81
	s_add_u32 s2, s10, s60
	s_addc_u32 s3, s11, 0
	s_mov_b32 s63, 0x3000
	s_mul_i32 s61, s59, 0x8000
	s_mul_i32 s81, s58, 0x40
	s_add_u32 s61, s61, s81
	s_add_u32 s61, s61, 0x800000
	s_add_u32 s52, s48, s61
	s_addc_u32 s53, s49, 0
	s_mov_b32 s66, 0x400
	s_mov_b32 s75, 0x44000000
	s_branch .Lcv102_d1_ld
.Lcv102_d1_b:
	s_sub_u32 s43, s43, 0x600
	s_cmp_lt_u32 s43, 0x200
	s_cbranch_scc0 .Lcv102_d1_c
	s_lshr_b32 s58, s43, 5
	s_and_b32 s59, s43, 31
	s_mul_i32 s60, s58, 0x40000
	s_mul_i32 s81, s59, 0x80
	s_add_u32 s60, s60, s81
	s_add_u32 s2, s12, s60
	s_addc_u32 s3, s13, 0
	s_mov_b32 s63, 0x1000
	s_mul_i32 s61, s59, 0x8000
	s_mul_i32 s81, s58, 0x40
	s_add_u32 s61, s61, s81
	s_add_u32 s61, s61, 0xe00000
	s_add_u32 s52, s48, s61
	s_addc_u32 s53, s49, 0
	s_mov_b32 s66, 0x400
	s_mov_b32 s75, 0x44800000
	s_branch .Lcv102_d1_ld
.Lcv102_d1_c:
	s_sub_u32 s43, s43, 0x200
	s_cmp_lt_u32 s43, 0x2000
	s_cbranch_scc0 .Lcv102_d1_dd
	s_lshr_b32 s80, s43, 8
	s_and_b32 s59, s43, 15
	s_bfe_u32 s58, s43, 0x40004
	s_lshr_b32 s81, s59, 2
	s_mul_i32 s61, s81, 0x40000
	s_and_b32 s81, s59, 3
	s_mul_i32 s81, s81, 0x8000
	s_add_u32 s61, s61, s81
	s_mul_i32 s81, s80, 0x100000
	s_add_u32 s61, s61, s81
	s_lshl_b32 s81, s58, 6
	s_add_u32 s61, s61, s81
	s_add_u32 s61, s61, 0x1000000
	s_add_u32 s52, s48, s61
	s_addc_u32 s53, s49, 0
	s_mul_i32 s60, s80, 0x200000
	s_mul_i32 s81, s58, 0x20000
	s_add_u32 s60, s60, s81
	s_lshl_b32 s81, s59, 7
	s_add_u32 s60, s60, s81
	s_add_u32 s2, s14, s60
	s_addc_u32 s3, s15, 0
	s_mov_b32 s63, 0x800
	s_mov_b32 s66, 0x400
	s_mov_b32 s75, 0x44000000
	s_branch .Lcv102_d1_ld
.Lcv102_d1_dd:
	s_sub_u32 s43, s43, 0x2000
	s_cmp_lt_u32 s43, 0x2000
	s_cbranch_scc0 .Lcv102_d1_e
	s_lshr_b32 s80, s43, 8
	s_and_b32 s59, s43, 15
	s_bfe_u32 s58, s43, 0x40004
	s_lshr_b32 s81, s59, 2
	s_mul_i32 s61, s81, 0x40000
	s_and_b32 s81, s59, 3
	s_mul_i32 s81, s81, 0x8000
	s_add_u32 s61, s61, s81
	s_mul_i32 s81, s80, 0x100000
	s_add_u32 s61, s61, s81
	s_lshl_b32 s81, s58, 6
	s_add_u32 s61, s61, s81
	s_add_u32 s61, s61, 0x1020000
	s_add_u32 s52, s48, s61
	s_addc_u32 s53, s49, 0
	s_mul_i32 s60, s80, 0x200000
	s_mul_i32 s81, s58, 0x20000
	s_add_u32 s60, s60, s81
	s_lshl_b32 s81, s59, 7
	s_add_u32 s60, s60, s81
	s_add_u32 s2, s28, s60
	s_addc_u32 s3, s29, 0
	s_mov_b32 s63, 0x800
	s_mov_b32 s66, 0x400
	s_mov_b32 s75, 0x44000000
	s_branch .Lcv102_d1_ld
.Lcv102_d1_e:
	s_sub_u32 s43, s43, 0x2000
	s_cmp_lt_u32 s43, 0x2000
	s_cbranch_scc0 .Lcv102_d1_f
	s_lshr_b32 s80, s43, 8
	s_and_b32 s59, s43, 31
	s_bfe_u32 s58, s43, 0x30005
	s_mul_i32 s60, s80, 0x200000
	s_mul_i32 s81, s58, 0x40000
	s_add_u32 s60, s60, s81
	s_mul_i32 s81, s59, 0x80
	s_add_u32 s60, s60, s81
	s_add_u32 s2, s38, s60
	s_addc_u32 s3, s39, 0
	s_mov_b32 s63, 0x1000
	s_mul_i32 s61, s80, 0x80000
	s_mul_i32 s81, s59, 0x4000
	s_add_u32 s61, s61, s81
	s_mul_i32 s81, s58, 0x40
	s_add_u32 s61, s61, s81
	s_add_u32 s61, s61, 0x5000000
	s_add_u32 s52, s48, s61
	s_addc_u32 s53, s49, 0
	s_mov_b32 s66, 0x200
	s_mov_b32 s75, 0x44800000
	s_branch .Lcv102_d1_ld
.Lcv102_d1_f:
	s_sub_u32 s43, s43, 0x2000
	s_cmp_lt_u32 s43, 0x200
	s_cbranch_scc0 .Lcv102_d1_g
	s_lshr_b32 s58, s43, 5
	s_and_b32 s59, s43, 31
	s_mul_i32 s60, s58, 0x40000
	s_mul_i32 s81, s59, 0x80
	s_add_u32 s60, s60, s81
	s_add_u32 s2, s44, s60
	s_addc_u32 s3, s45, 0
	s_mov_b32 s63, 0x1000
	s_mul_i32 s61, s59, 0x10000
	s_mul_i32 s81, s58, 0x80
	s_add_u32 s61, s61, s81
	s_add_u32 s61, s61, 0x7000000
	s_add_u32 s52, s48, s61
	s_addc_u32 s53, s49, 0
	s_mov_b32 s66, 0x800
	s_mov_b32 s75, 0x0
	s_branch .Lcv102_d1_ld
.Lcv102_d1_g:
	s_sub_u32 s43, s43, 0x200
	s_lshr_b32 s58, s43, 5
	s_and_b32 s59, s43, 31
	s_mul_i32 s60, s58, 0x40000
	s_mul_i32 s81, s59, 0x80
	s_add_u32 s60, s60, s81
	s_add_u32 s2, s46, s60
	s_addc_u32 s3, s47, 0
	s_mov_b32 s63, 0x1000
	s_mul_i32 s61, s59, 0x4000
	s_mul_i32 s81, s58, 0x80
	s_add_u32 s61, s61, s81
	s_add_u32 s61, s61, 0x7200000
	s_add_u32 s52, s48, s61
	s_addc_u32 s53, s49, 0
	s_mov_b32 s66, 0x200
	s_mov_b32 s75, 0x0
	s_branch .Lcv102_d1_ld
.Lcv102_d1_ld:
	s_lshl_b32 s60, s63, 3
	v_mul_lo_u32 v0, v96, s60
	v_lshl_add_u32 v0, v97, 4, v0
	v_add_u32_e32 v4, s63, v0
	v_add_u32_e32 v10, s63, v4
	v_add_u32_e32 v11, s63, v10
	v_add_u32_e32 v12, s63, v11
	v_add_u32_e32 v19, s63, v12
	v_add_u32_e32 v24, s63, v19
	v_add_u32_e32 v25, s63, v24
	global_load_dwordx4 v[66:69], v0, s[2:3] nt
	global_load_dwordx4 v[70:73], v4, s[2:3] nt
	global_load_dwordx4 v[74:77], v10, s[2:3] nt
	global_load_dwordx4 v[78:81], v11, s[2:3] nt
	global_load_dwordx4 v[82:85], v12, s[2:3] nt
	global_load_dwordx4 v[86:89], v19, s[2:3] nt
	global_load_dwordx4 v[102:105], v24, s[2:3] nt
	global_load_dwordx4 v[106:109], v25, s[2:3] nt
	s_mov_b32 s41, 2
	s_cmp_lt_u32 s32, 0x6a80
	s_cbranch_scc0 .Lcv102_drain0
	s_add_u32 s43, s32, 2
	s_cmp_lt_u32 s43, 0x600
	s_cbranch_scc0 .Lcv102_d2_b
	s_mul_i32 s58, s43, 0xaaab
	s_lshr_b32 s58, s58, 22
	s_mul_i32 s59, s58, 96
	s_sub_u32 s59, s43, s59
	s_mul_i32 s60, s58, 0xc0000
	s_mul_i32 s81, s59, 0x80
	s_add_u32 s60, s60, s81
	s_add_u32 s2, s10, s60
	s_addc_u32 s3, s11, 0
	s_mov_b32 s63, 0x3000
	s_mul_i32 s61, s59, 0x8000
	s_mul_i32 s81, s58, 0x40
	s_add_u32 s61, s61, s81
	s_add_u32 s61, s61, 0x800000
	s_add_u32 s54, s48, s61
	s_addc_u32 s55, s49, 0
	s_mov_b32 s67, 0x400
	s_mov_b32 s78, 0x44000000
	s_branch .Lcv102_d2_ld
.Lcv102_d2_b:
	s_sub_u32 s43, s43, 0x600
	s_cmp_lt_u32 s43, 0x200
	s_cbranch_scc0 .Lcv102_d2_c
	s_lshr_b32 s58, s43, 5
	s_and_b32 s59, s43, 31
	s_mul_i32 s60, s58, 0x40000
	s_mul_i32 s81, s59, 0x80
	s_add_u32 s60, s60, s81
	s_add_u32 s2, s12, s60
	s_addc_u32 s3, s13, 0
	s_mov_b32 s63, 0x1000
	s_mul_i32 s61, s59, 0x8000
	s_mul_i32 s81, s58, 0x40
	s_add_u32 s61, s61, s81
	s_add_u32 s61, s61, 0xe00000
	s_add_u32 s54, s48, s61
	s_addc_u32 s55, s49, 0
	s_mov_b32 s67, 0x400
	s_mov_b32 s78, 0x44800000
	s_branch .Lcv102_d2_ld
.Lcv102_d2_c:
	s_sub_u32 s43, s43, 0x200
	s_cmp_lt_u32 s43, 0x2000
	s_cbranch_scc0 .Lcv102_d2_dd
	s_lshr_b32 s80, s43, 8
	s_and_b32 s59, s43, 15
	s_bfe_u32 s58, s43, 0x40004
	s_lshr_b32 s81, s59, 2
	s_mul_i32 s61, s81, 0x40000
	s_and_b32 s81, s59, 3
	s_mul_i32 s81, s81, 0x8000
	s_add_u32 s61, s61, s81
	s_mul_i32 s81, s80, 0x100000
	s_add_u32 s61, s61, s81
	s_lshl_b32 s81, s58, 6
	s_add_u32 s61, s61, s81
	s_add_u32 s61, s61, 0x1000000
	s_add_u32 s54, s48, s61
	s_addc_u32 s55, s49, 0
	s_mul_i32 s60, s80, 0x200000
	s_mul_i32 s81, s58, 0x20000
	s_add_u32 s60, s60, s81
	s_lshl_b32 s81, s59, 7
	s_add_u32 s60, s60, s81
	s_add_u32 s2, s14, s60
	s_addc_u32 s3, s15, 0
	s_mov_b32 s63, 0x800
	s_mov_b32 s67, 0x400
	s_mov_b32 s78, 0x44000000
	s_branch .Lcv102_d2_ld
.Lcv102_d2_dd:
	s_sub_u32 s43, s43, 0x2000
	s_cmp_lt_u32 s43, 0x2000
	s_cbranch_scc0 .Lcv102_d2_e
	s_lshr_b32 s80, s43, 8
	s_and_b32 s59, s43, 15
	s_bfe_u32 s58, s43, 0x40004
	s_lshr_b32 s81, s59, 2
	s_mul_i32 s61, s81, 0x40000
	s_and_b32 s81, s59, 3
	s_mul_i32 s81, s81, 0x8000
	s_add_u32 s61, s61, s81
	s_mul_i32 s81, s80, 0x100000
	s_add_u32 s61, s61, s81
	s_lshl_b32 s81, s58, 6
	s_add_u32 s61, s61, s81
	s_add_u32 s61, s61, 0x1020000
	s_add_u32 s54, s48, s61
	s_addc_u32 s55, s49, 0
	s_mul_i32 s60, s80, 0x200000
	s_mul_i32 s81, s58, 0x20000
	s_add_u32 s60, s60, s81
	s_lshl_b32 s81, s59, 7
	s_add_u32 s60, s60, s81
	s_add_u32 s2, s28, s60
	s_addc_u32 s3, s29, 0
	s_mov_b32 s63, 0x800
	s_mov_b32 s67, 0x400
	s_mov_b32 s78, 0x44000000
	s_branch .Lcv102_d2_ld
.Lcv102_d2_e:
	s_sub_u32 s43, s43, 0x2000
	s_cmp_lt_u32 s43, 0x2000
	s_cbranch_scc0 .Lcv102_d2_f
	s_lshr_b32 s80, s43, 8
	s_and_b32 s59, s43, 31
	s_bfe_u32 s58, s43, 0x30005
	s_mul_i32 s60, s80, 0x200000
	s_mul_i32 s81, s58, 0x40000
	s_add_u32 s60, s60, s81
	s_mul_i32 s81, s59, 0x80
	s_add_u32 s60, s60, s81
	s_add_u32 s2, s38, s60
	s_addc_u32 s3, s39, 0
	s_mov_b32 s63, 0x1000
	s_mul_i32 s61, s80, 0x80000
	s_mul_i32 s81, s59, 0x4000
	s_add_u32 s61, s61, s81
	s_mul_i32 s81, s58, 0x40
	s_add_u32 s61, s61, s81
	s_add_u32 s61, s61, 0x5000000
	s_add_u32 s54, s48, s61
	s_addc_u32 s55, s49, 0
	s_mov_b32 s67, 0x200
	s_mov_b32 s78, 0x44800000
	s_branch .Lcv102_d2_ld
.Lcv102_d2_f:
	s_sub_u32 s43, s43, 0x2000
	s_cmp_lt_u32 s43, 0x200
	s_cbranch_scc0 .Lcv102_d2_g
	s_lshr_b32 s58, s43, 5
	s_and_b32 s59, s43, 31
	s_mul_i32 s60, s58, 0x40000
	s_mul_i32 s81, s59, 0x80
	s_add_u32 s60, s60, s81
	s_add_u32 s2, s44, s60
	s_addc_u32 s3, s45, 0
	s_mov_b32 s63, 0x1000
	s_mul_i32 s61, s59, 0x10000
	s_mul_i32 s81, s58, 0x80
	s_add_u32 s61, s61, s81
	s_add_u32 s61, s61, 0x7000000
	s_add_u32 s54, s48, s61
	s_addc_u32 s55, s49, 0
	s_mov_b32 s67, 0x800
	s_mov_b32 s78, 0x0
	s_branch .Lcv102_d2_ld
.Lcv102_d2_g:
	s_sub_u32 s43, s43, 0x200
	s_lshr_b32 s58, s43, 5
	s_and_b32 s59, s43, 31
	s_mul_i32 s60, s58, 0x40000
	s_mul_i32 s81, s59, 0x80
	s_add_u32 s60, s60, s81
	s_add_u32 s2, s46, s60
	s_addc_u32 s3, s47, 0
	s_mov_b32 s63, 0x1000
	s_mul_i32 s61, s59, 0x4000
	s_mul_i32 s81, s58, 0x80
	s_add_u32 s61, s61, s81
	s_add_u32 s61, s61, 0x7200000
	s_add_u32 s54, s48, s61
	s_addc_u32 s55, s49, 0
	s_mov_b32 s67, 0x200
	s_mov_b32 s78, 0x0
	s_branch .Lcv102_d2_ld
.Lcv102_d2_ld:
	s_lshl_b32 s60, s63, 3
	v_mul_lo_u32 v0, v96, s60
	v_lshl_add_u32 v0, v97, 4, v0
	v_add_u32_e32 v4, s63, v0
	v_add_u32_e32 v10, s63, v4
	v_add_u32_e32 v11, s63, v10
	v_add_u32_e32 v12, s63, v11
	v_add_u32_e32 v19, s63, v12
	v_add_u32_e32 v24, s63, v19
	v_add_u32_e32 v25, s63, v24
	global_load_dwordx4 v[110:113], v0, s[2:3] nt
	global_load_dwordx4 v[114:117], v4, s[2:3] nt
	global_load_dwordx4 v[118:121], v10, s[2:3] nt
	global_load_dwordx4 v[122:125], v11, s[2:3] nt
	global_load_dwordx4 v[126:129], v12, s[2:3] nt
	global_load_dwordx4 v[130:133], v19, s[2:3] nt
	global_load_dwordx4 v[134:137], v24, s[2:3] nt
	global_load_dwordx4 v[138:141], v25, s[2:3] nt
	s_mov_b32 s41, 3
	s_cmp_lt_u32 s32, 0x6a80
	s_cbranch_scc0 .Lcv102_drain0
	s_add_u32 s43, s32, 3
	s_cmp_lt_u32 s43, 0x600
	s_cbranch_scc0 .Lcv102_d3_b
	s_mul_i32 s58, s43, 0xaaab
	s_lshr_b32 s58, s58, 22
	s_mul_i32 s59, s58, 96
	s_sub_u32 s59, s43, s59
	s_mul_i32 s60, s58, 0xc0000
	s_mul_i32 s81, s59, 0x80
	s_add_u32 s60, s60, s81
	s_add_u32 s2, s10, s60
	s_addc_u32 s3, s11, 0
	s_mov_b32 s63, 0x3000
	s_mul_i32 s61, s59, 0x8000
	s_mul_i32 s81, s58, 0x40
	s_add_u32 s61, s61, s81
	s_add_u32 s61, s61, 0x800000
	s_add_u32 s56, s48, s61
	s_addc_u32 s57, s49, 0
	s_mov_b32 s69, 0x400
	s_mov_b32 s79, 0x44000000
	s_branch .Lcv102_d3_ld
.Lcv102_d3_b:
	s_sub_u32 s43, s43, 0x600
	s_cmp_lt_u32 s43, 0x200
	s_cbranch_scc0 .Lcv102_d3_c
	s_lshr_b32 s58, s43, 5
	s_and_b32 s59, s43, 31
	s_mul_i32 s60, s58, 0x40000
	s_mul_i32 s81, s59, 0x80
	s_add_u32 s60, s60, s81
	s_add_u32 s2, s12, s60
	s_addc_u32 s3, s13, 0
	s_mov_b32 s63, 0x1000
	s_mul_i32 s61, s59, 0x8000
	s_mul_i32 s81, s58, 0x40
	s_add_u32 s61, s61, s81
	s_add_u32 s61, s61, 0xe00000
	s_add_u32 s56, s48, s61
	s_addc_u32 s57, s49, 0
	s_mov_b32 s69, 0x400
	s_mov_b32 s79, 0x44800000
	s_branch .Lcv102_d3_ld
.Lcv102_d3_c:
	s_sub_u32 s43, s43, 0x200
	s_cmp_lt_u32 s43, 0x2000
	s_cbranch_scc0 .Lcv102_d3_dd
	s_lshr_b32 s80, s43, 8
	s_and_b32 s59, s43, 15
	s_bfe_u32 s58, s43, 0x40004
	s_lshr_b32 s81, s59, 2
	s_mul_i32 s61, s81, 0x40000
	s_and_b32 s81, s59, 3
	s_mul_i32 s81, s81, 0x8000
	s_add_u32 s61, s61, s81
	s_mul_i32 s81, s80, 0x100000
	s_add_u32 s61, s61, s81
	s_lshl_b32 s81, s58, 6
	s_add_u32 s61, s61, s81
	s_add_u32 s61, s61, 0x1000000
	s_add_u32 s56, s48, s61
	s_addc_u32 s57, s49, 0
	s_mul_i32 s60, s80, 0x200000
	s_mul_i32 s81, s58, 0x20000
	s_add_u32 s60, s60, s81
	s_lshl_b32 s81, s59, 7
	s_add_u32 s60, s60, s81
	s_add_u32 s2, s14, s60
	s_addc_u32 s3, s15, 0
	s_mov_b32 s63, 0x800
	s_mov_b32 s69, 0x400
	s_mov_b32 s79, 0x44000000
	s_branch .Lcv102_d3_ld
.Lcv102_d3_dd:
	s_sub_u32 s43, s43, 0x2000
	s_cmp_lt_u32 s43, 0x2000
	s_cbranch_scc0 .Lcv102_d3_e
	s_lshr_b32 s80, s43, 8
	s_and_b32 s59, s43, 15
	s_bfe_u32 s58, s43, 0x40004
	s_lshr_b32 s81, s59, 2
	s_mul_i32 s61, s81, 0x40000
	s_and_b32 s81, s59, 3
	s_mul_i32 s81, s81, 0x8000
	s_add_u32 s61, s61, s81
	s_mul_i32 s81, s80, 0x100000
	s_add_u32 s61, s61, s81
	s_lshl_b32 s81, s58, 6
	s_add_u32 s61, s61, s81
	s_add_u32 s61, s61, 0x1020000
	s_add_u32 s56, s48, s61
	s_addc_u32 s57, s49, 0
	s_mul_i32 s60, s80, 0x200000
	s_mul_i32 s81, s58, 0x20000
	s_add_u32 s60, s60, s81
	s_lshl_b32 s81, s59, 7
	s_add_u32 s60, s60, s81
	s_add_u32 s2, s28, s60
	s_addc_u32 s3, s29, 0
	s_mov_b32 s63, 0x800
	s_mov_b32 s69, 0x400
	s_mov_b32 s79, 0x44000000
	s_branch .Lcv102_d3_ld
.Lcv102_d3_e:
	s_sub_u32 s43, s43, 0x2000
	s_cmp_lt_u32 s43, 0x2000
	s_cbranch_scc0 .Lcv102_d3_f
	s_lshr_b32 s80, s43, 8
	s_and_b32 s59, s43, 31
	s_bfe_u32 s58, s43, 0x30005
	s_mul_i32 s60, s80, 0x200000
	s_mul_i32 s81, s58, 0x40000
	s_add_u32 s60, s60, s81
	s_mul_i32 s81, s59, 0x80
	s_add_u32 s60, s60, s81
	s_add_u32 s2, s38, s60
	s_addc_u32 s3, s39, 0
	s_mov_b32 s63, 0x1000
	s_mul_i32 s61, s80, 0x80000
	s_mul_i32 s81, s59, 0x4000
	s_add_u32 s61, s61, s81
	s_mul_i32 s81, s58, 0x40
	s_add_u32 s61, s61, s81
	s_add_u32 s61, s61, 0x5000000
	s_add_u32 s56, s48, s61
	s_addc_u32 s57, s49, 0
	s_mov_b32 s69, 0x200
	s_mov_b32 s79, 0x44800000
	s_branch .Lcv102_d3_ld
.Lcv102_d3_f:
	s_sub_u32 s43, s43, 0x2000
	s_cmp_lt_u32 s43, 0x200
	s_cbranch_scc0 .Lcv102_d3_g
	s_lshr_b32 s58, s43, 5
	s_and_b32 s59, s43, 31
	s_mul_i32 s60, s58, 0x40000
	s_mul_i32 s81, s59, 0x80
	s_add_u32 s60, s60, s81
	s_add_u32 s2, s44, s60
	s_addc_u32 s3, s45, 0
	s_mov_b32 s63, 0x1000
	s_mul_i32 s61, s59, 0x10000
	s_mul_i32 s81, s58, 0x80
	s_add_u32 s61, s61, s81
	s_add_u32 s61, s61, 0x7000000
	s_add_u32 s56, s48, s61
	s_addc_u32 s57, s49, 0
	s_mov_b32 s69, 0x800
	s_mov_b32 s79, 0x0
	s_branch .Lcv102_d3_ld
.Lcv102_d3_g:
	s_sub_u32 s43, s43, 0x200
	s_lshr_b32 s58, s43, 5
	s_and_b32 s59, s43, 31
	s_mul_i32 s60, s58, 0x40000
	s_mul_i32 s81, s59, 0x80
	s_add_u32 s60, s60, s81
	s_add_u32 s2, s46, s60
	s_addc_u32 s3, s47, 0
	s_mov_b32 s63, 0x1000
	s_mul_i32 s61, s59, 0x4000
	s_mul_i32 s81, s58, 0x80
	s_add_u32 s61, s61, s81
	s_add_u32 s61, s61, 0x7200000
	s_add_u32 s56, s48, s61
	s_addc_u32 s57, s49, 0
	s_mov_b32 s69, 0x200
	s_mov_b32 s79, 0x0
	s_branch .Lcv102_d3_ld
.Lcv102_d3_ld:
	s_lshl_b32 s60, s63, 3
	v_mul_lo_u32 v0, v96, s60
	v_lshl_add_u32 v0, v97, 4, v0
	v_add_u32_e32 v4, s63, v0
	v_add_u32_e32 v10, s63, v4
	v_add_u32_e32 v11, s63, v10
	v_add_u32_e32 v12, s63, v11
	v_add_u32_e32 v19, s63, v12
	v_add_u32_e32 v24, s63, v19
	v_add_u32_e32 v25, s63, v24
	global_load_dwordx4 v[142:145], v0, s[2:3] nt
	global_load_dwordx4 v[172:175], v4, s[2:3] nt
	global_load_dwordx4 v[176:179], v10, s[2:3] nt
	global_load_dwordx4 v[180:183], v11, s[2:3] nt
	global_load_dwordx4 v[184:187], v12, s[2:3] nt
	global_load_dwordx4 v[188:191], v19, s[2:3] nt
	global_load_dwordx4 v[162:165], v24, s[2:3] nt
	global_load_dwordx4 v[6:9], v25, s[2:3] nt
	s_add_u32 s32, s32, s20
	s_mov_b32 s41, 4
.Lcv102_loop:
	s_cmp_lt_u32 s32, 0x6a80
	s_cbranch_scc0 .Lcv102_drain0
	s_waitcnt vmcnt(24)
	s_lshl_b32 s60, s65, 2
	v_mul_lo_u32 v27, v97, s60
	s_cmp_eq_u32 s71, 0
	s_cbranch_scc1 .Lcv102_p4_bf
	v_lshl_add_u32 v27, v96, 3, v27
	v_add_u32_e32 v32, s65, v27
	v_add_u32_e32 v92, s65, v32
	v_add_u32_e32 v94, s65, v92
	v_mul_f32_e32 v34, s71, v34
	v_mul_f32_e32 v35, s71, v35
	v_mul_f32_e32 v36, s71, v36
	v_mul_f32_e32 v37, s71, v37
	v_mul_f32_e32 v38, s71, v38
	v_mul_f32_e32 v39, s71, v39
	v_mul_f32_e32 v40, s71, v40
	v_mul_f32_e32 v41, s71, v41
	v_mul_f32_e32 v42, s71, v42
	v_mul_f32_e32 v43, s71, v43
	v_mul_f32_e32 v44, s71, v44
	v_mul_f32_e32 v45, s71, v45
	v_mul_f32_e32 v46, s71, v46
	v_mul_f32_e32 v47, s71, v47
	v_mul_f32_e32 v48, s71, v48
	v_mul_f32_e32 v49, s71, v49
	v_mul_f32_e32 v50, s71, v50
	v_mul_f32_e32 v51, s71, v51
	v_mul_f32_e32 v52, s71, v52
	v_mul_f32_e32 v53, s71, v53
	v_mul_f32_e32 v54, s71, v54
	v_mul_f32_e32 v55, s71, v55
	v_mul_f32_e32 v56, s71, v56
	v_mul_f32_e32 v57, s71, v57
	v_mul_f32_e32 v58, s71, v58
	v_mul_f32_e32 v59, s71, v59
	v_mul_f32_e32 v60, s71, v60
	v_mul_f32_e32 v61, s71, v61
	v_mul_f32_e32 v62, s71, v62
	v_mul_f32_e32 v63, s71, v63
	v_mul_f32_e32 v64, s71, v64
	v_mul_f32_e32 v65, s71, v65
	v_med3_f32 v34, v34, s64, v98
	v_med3_f32 v35, v35, s64, v98
	v_med3_f32 v36, v36, s64, v98
	v_med3_f32 v37, v37, s64, v98
	v_med3_f32 v38, v38, s64, v98
	v_med3_f32 v39, v39, s64, v98
	v_med3_f32 v40, v40, s64, v98
	v_med3_f32 v41, v41, s64, v98
	v_med3_f32 v42, v42, s64, v98
	v_med3_f32 v43, v43, s64, v98
	v_med3_f32 v44, v44, s64, v98
	v_med3_f32 v45, v45, s64, v98
	v_med3_f32 v46, v46, s64, v98
	v_med3_f32 v47, v47, s64, v98
	v_med3_f32 v48, v48, s64, v98
	v_med3_f32 v49, v49, s64, v98
	v_med3_f32 v50, v50, s64, v98
	v_med3_f32 v51, v51, s64, v98
	v_med3_f32 v52, v52, s64, v98
	v_med3_f32 v53, v53, s64, v98
	v_med3_f32 v54, v54, s64, v98
	v_med3_f32 v55, v55, s64, v98
	v_med3_f32 v56, v56, s64, v98
	v_med3_f32 v57, v57, s64, v98
	v_med3_f32 v58, v58, s64, v98
	v_med3_f32 v59, v59, s64, v98
	v_med3_f32 v60, v60, s64, v98
	v_med3_f32 v61, v61, s64, v98
	v_med3_f32 v62, v62, s64, v98
	v_med3_f32 v63, v63, s64, v98
	v_med3_f32 v64, v64, s64, v98
	v_med3_f32 v65, v65, s64, v98
	v_cvt_pk_fp8_f32 v148, v34, v38
	v_cvt_pk_fp8_f32 v149, v50, v54
	v_cvt_pk_fp8_f32 v152, v35, v39
	v_cvt_pk_fp8_f32 v153, v51, v55
	v_cvt_pk_fp8_f32 v158, v36, v40
	v_cvt_pk_fp8_f32 v159, v52, v56
	v_cvt_pk_fp8_f32 v196, v37, v41
	v_cvt_pk_fp8_f32 v197, v53, v57
	v_cvt_pk_fp8_f32 v148, v42, v46 op_sel:[0,0,1]
	v_cvt_pk_fp8_f32 v149, v58, v62 op_sel:[0,0,1]
	v_cvt_pk_fp8_f32 v152, v43, v47 op_sel:[0,0,1]
	v_cvt_pk_fp8_f32 v153, v59, v63 op_sel:[0,0,1]
	v_cvt_pk_fp8_f32 v158, v44, v48 op_sel:[0,0,1]
	v_cvt_pk_fp8_f32 v159, v60, v64 op_sel:[0,0,1]
	v_cvt_pk_fp8_f32 v196, v45, v49 op_sel:[0,0,1]
	v_cvt_pk_fp8_f32 v197, v61, v65 op_sel:[0,0,1]
	s_nop 1
	global_store_dwordx2 v27, v[148:149], s[50:51]
	global_store_dwordx2 v32, v[152:153], s[50:51]
	global_store_dwordx2 v92, v[158:159], s[50:51]
	global_store_dwordx2 v94, v[196:197], s[50:51]
	s_branch .Lcv102_p4_end
.Lcv102_p4_bf:
	v_lshl_add_u32 v27, v96, 4, v27
	v_add_u32_e32 v32, s65, v27
	v_add_u32_e32 v92, s65, v32
	v_add_u32_e32 v94, s65, v92
	v_cvt_pk_bf16_f32 v148, v34, v38
	v_cvt_pk_bf16_f32 v149, v42, v46
	v_cvt_pk_bf16_f32 v202, v50, v54
	v_cvt_pk_bf16_f32 v203, v58, v62
	v_cvt_pk_bf16_f32 v152, v35, v39
	v_cvt_pk_bf16_f32 v153, v43, v47
	v_cvt_pk_bf16_f32 v208, v51, v55
	v_cvt_pk_bf16_f32 v209, v59, v63
	v_cvt_pk_bf16_f32 v158, v36, v40
	v_cvt_pk_bf16_f32 v159, v44, v48
	v_cvt_pk_bf16_f32 v220, v52, v56
	v_cvt_pk_bf16_f32 v221, v60, v64
	v_cvt_pk_bf16_f32 v196, v37, v41
	v_cvt_pk_bf16_f32 v197, v45, v49
	v_cvt_pk_bf16_f32 v226, v53, v57
	v_cvt_pk_bf16_f32 v227, v61, v65
	s_nop 1
	global_store_dwordx2 v27, v[148:149], s[50:51]
	global_store_dwordx2 v27, v[202:203], s[50:51] offset:8
	global_store_dwordx2 v32, v[152:153], s[50:51]
	global_store_dwordx2 v32, v[208:209], s[50:51] offset:8
	global_store_dwordx2 v92, v[158:159], s[50:51]
	global_store_dwordx2 v92, v[220:221], s[50:51] offset:8
	global_store_dwordx2 v94, v[196:197], s[50:51]
	global_store_dwordx2 v94, v[226:227], s[50:51] offset:8
.Lcv102_p4_end:
	s_add_u32 s43, s32, 0
	s_cmp_lt_u32 s43, 0x600
	s_cbranch_scc0 .Lcv102_d5_b
	s_mul_i32 s58, s43, 0xaaab
	s_lshr_b32 s58, s58, 22
	s_mul_i32 s59, s58, 96
	s_sub_u32 s59, s43, s59
	s_mul_i32 s60, s58, 0xc0000
	s_mul_i32 s81, s59, 0x80
	s_add_u32 s60, s60, s81
	s_add_u32 s2, s10, s60
	s_addc_u32 s3, s11, 0
	s_mov_b32 s63, 0x3000
	s_mul_i32 s61, s59, 0x8000
	s_mul_i32 s81, s58, 0x40
	s_add_u32 s61, s61, s81
	s_add_u32 s61, s61, 0x800000
	s_add_u32 s50, s48, s61
	s_addc_u32 s51, s49, 0
	s_mov_b32 s65, 0x400
	s_mov_b32 s71, 0x44000000
	s_branch .Lcv102_d5_ld

.Lcv102_d5_ld:
	s_lshl_b32 s60, s63, 3
	v_mul_lo_u32 v0, v96, s60
	v_lshl_add_u32 v0, v97, 4, v0
	v_add_u32_e32 v4, s63, v0
	v_add_u32_e32 v10, s63, v4
	v_add_u32_e32 v11, s63, v10
	v_add_u32_e32 v12, s63, v11
	v_add_u32_e32 v19, s63, v12
	v_add_u32_e32 v24, s63, v19
	v_add_u32_e32 v25, s63, v24
	global_load_dwordx4 v[34:37], v0, s[2:3] nt
	global_load_dwordx4 v[38:41], v4, s[2:3] nt
	global_load_dwordx4 v[42:45], v10, s[2:3] nt
	global_load_dwordx4 v[46:49], v11, s[2:3] nt
	global_load_dwordx4 v[50:53], v12, s[2:3] nt
	global_load_dwordx4 v[54:57], v19, s[2:3] nt
	global_load_dwordx4 v[58:61], v24, s[2:3] nt
	global_load_dwordx4 v[62:65], v25, s[2:3] nt
	s_cmp_lt_u32 s32, 0x6a80
	s_cbranch_scc0 .Lcv102_drain1
	s_waitcnt vmcnt(24)
	s_lshl_b32 s60, s66, 2
	v_mul_lo_u32 v27, v97, s60
	s_cmp_eq_u32 s75, 0
	s_cbranch_scc1 .Lcv102_p6_bf
	v_lshl_add_u32 v27, v96, 3, v27
	v_add_u32_e32 v32, s66, v27
	v_add_u32_e32 v92, s66, v32
	v_add_u32_e32 v94, s66, v92
	v_mul_f32_e32 v66, s75, v66
	v_mul_f32_e32 v67, s75, v67
	v_mul_f32_e32 v68, s75, v68
	v_mul_f32_e32 v69, s75, v69
	v_mul_f32_e32 v70, s75, v70
	v_mul_f32_e32 v71, s75, v71
	v_mul_f32_e32 v72, s75, v72
	v_mul_f32_e32 v73, s75, v73
	v_mul_f32_e32 v74, s75, v74
	v_mul_f32_e32 v75, s75, v75
	v_mul_f32_e32 v76, s75, v76
	v_mul_f32_e32 v77, s75, v77
	v_mul_f32_e32 v78, s75, v78
	v_mul_f32_e32 v79, s75, v79
	v_mul_f32_e32 v80, s75, v80
	v_mul_f32_e32 v81, s75, v81
	v_mul_f32_e32 v82, s75, v82
	v_mul_f32_e32 v83, s75, v83
	v_mul_f32_e32 v84, s75, v84
	v_mul_f32_e32 v85, s75, v85
	v_mul_f32_e32 v86, s75, v86
	v_mul_f32_e32 v87, s75, v87
	v_mul_f32_e32 v88, s75, v88
	v_mul_f32_e32 v89, s75, v89
	v_mul_f32_e32 v102, s75, v102
	v_mul_f32_e32 v103, s75, v103
	v_mul_f32_e32 v104, s75, v104
	v_mul_f32_e32 v105, s75, v105
	v_mul_f32_e32 v106, s75, v106
	v_mul_f32_e32 v107, s75, v107
	v_mul_f32_e32 v108, s75, v108
	v_mul_f32_e32 v109, s75, v109
	v_med3_f32 v66, v66, s64, v98
	v_med3_f32 v67, v67, s64, v98
	v_med3_f32 v68, v68, s64, v98
	v_med3_f32 v69, v69, s64, v98
	v_med3_f32 v70, v70, s64, v98
	v_med3_f32 v71, v71, s64, v98
	v_med3_f32 v72, v72, s64, v98
	v_med3_f32 v73, v73, s64, v98
	v_med3_f32 v74, v74, s64, v98
	v_med3_f32 v75, v75, s64, v98
	v_med3_f32 v76, v76, s64, v98
	v_med3_f32 v77, v77, s64, v98
	v_med3_f32 v78, v78, s64, v98
	v_med3_f32 v79, v79, s64, v98
	v_med3_f32 v80, v80, s64, v98
	v_med3_f32 v81, v81, s64, v98
	v_med3_f32 v82, v82, s64, v98
	v_med3_f32 v83, v83, s64, v98
	v_med3_f32 v84, v84, s64, v98
	v_med3_f32 v85, v85, s64, v98
	v_med3_f32 v86, v86, s64, v98
	v_med3_f32 v87, v87, s64, v98
	v_med3_f32 v88, v88, s64, v98
	v_med3_f32 v89, v89, s64, v98
	v_med3_f32 v102, v102, s64, v98
	v_med3_f32 v103, v103, s64, v98
	v_med3_f32 v104, v104, s64, v98
	v_med3_f32 v105, v105, s64, v98
	v_med3_f32 v106, v106, s64, v98
	v_med3_f32 v107, v107, s64, v98
	v_med3_f32 v108, v108, s64, v98
	v_med3_f32 v109, v109, s64, v98
	v_cvt_pk_fp8_f32 v148, v66, v70
	v_cvt_pk_fp8_f32 v149, v82, v86
	v_cvt_pk_fp8_f32 v152, v67, v71
	v_cvt_pk_fp8_f32 v153, v83, v87
	v_cvt_pk_fp8_f32 v158, v68, v72
	v_cvt_pk_fp8_f32 v159, v84, v88
	v_cvt_pk_fp8_f32 v196, v69, v73
	v_cvt_pk_fp8_f32 v197, v85, v89
	v_cvt_pk_fp8_f32 v148, v74, v78 op_sel:[0,0,1]
	v_cvt_pk_fp8_f32 v149, v102, v106 op_sel:[0,0,1]
	v_cvt_pk_fp8_f32 v152, v75, v79 op_sel:[0,0,1]
	v_cvt_pk_fp8_f32 v153, v103, v107 op_sel:[0,0,1]
	v_cvt_pk_fp8_f32 v158, v76, v80 op_sel:[0,0,1]
	v_cvt_pk_fp8_f32 v159, v104, v108 op_sel:[0,0,1]
	v_cvt_pk_fp8_f32 v196, v77, v81 op_sel:[0,0,1]
	v_cvt_pk_fp8_f32 v197, v105, v109 op_sel:[0,0,1]
	s_nop 1
	global_store_dwordx2 v27, v[148:149], s[52:53]
	global_store_dwordx2 v32, v[152:153], s[52:53]
	global_store_dwordx2 v92, v[158:159], s[52:53]
	global_store_dwordx2 v94, v[196:197], s[52:53]
	s_branch .Lcv102_p6_end
.Lcv102_p6_bf:
	v_lshl_add_u32 v27, v96, 4, v27
	v_add_u32_e32 v32, s66, v27
	v_add_u32_e32 v92, s66, v32
	v_add_u32_e32 v94, s66, v92
	v_cvt_pk_bf16_f32 v148, v66, v70
	v_cvt_pk_bf16_f32 v149, v74, v78
	v_cvt_pk_bf16_f32 v202, v82, v86
	v_cvt_pk_bf16_f32 v203, v102, v106
	v_cvt_pk_bf16_f32 v152, v67, v71
	v_cvt_pk_bf16_f32 v153, v75, v79
	v_cvt_pk_bf16_f32 v208, v83, v87
	v_cvt_pk_bf16_f32 v209, v103, v107
	v_cvt_pk_bf16_f32 v158, v68, v72
	v_cvt_pk_bf16_f32 v159, v76, v80
	v_cvt_pk_bf16_f32 v220, v84, v88
	v_cvt_pk_bf16_f32 v221, v104, v108
	v_cvt_pk_bf16_f32 v196, v69, v73
	v_cvt_pk_bf16_f32 v197, v77, v81
	v_cvt_pk_bf16_f32 v226, v85, v89
	v_cvt_pk_bf16_f32 v227, v105, v109
	s_nop 1
	global_store_dwordx2 v27, v[148:149], s[52:53]
	global_store_dwordx2 v27, v[202:203], s[52:53] offset:8
	global_store_dwordx2 v32, v[152:153], s[52:53]
	global_store_dwordx2 v32, v[208:209], s[52:53] offset:8
	global_store_dwordx2 v92, v[158:159], s[52:53]
	global_store_dwordx2 v92, v[220:221], s[52:53] offset:8
	global_store_dwordx2 v94, v[196:197], s[52:53]
	global_store_dwordx2 v94, v[226:227], s[52:53] offset:8
.Lcv102_p6_end:
	s_add_u32 s43, s32, 1
	s_cmp_lt_u32 s43, 0x600
	s_cbranch_scc0 .Lcv102_d7_b
	s_mul_i32 s58, s43, 0xaaab
	s_lshr_b32 s58, s58, 22
	s_mul_i32 s59, s58, 96
	s_sub_u32 s59, s43, s59
	s_mul_i32 s60, s58, 0xc0000
	s_mul_i32 s81, s59, 0x80
	s_add_u32 s60, s60, s81
	s_add_u32 s2, s10, s60
	s_addc_u32 s3, s11, 0
	s_mov_b32 s63, 0x3000
	s_mul_i32 s61, s59, 0x8000
	s_mul_i32 s81, s58, 0x40
	s_add_u32 s61, s61, s81
	s_add_u32 s61, s61, 0x800000
	s_add_u32 s52, s48, s61
	s_addc_u32 s53, s49, 0
	s_mov_b32 s66, 0x400
	s_mov_b32 s75, 0x44000000
	s_branch .Lcv102_d7_ld

.Lcv102_d7_ld:
	s_lshl_b32 s60, s63, 3
	v_mul_lo_u32 v0, v96, s60
	v_lshl_add_u32 v0, v97, 4, v0
	v_add_u32_e32 v4, s63, v0
	v_add_u32_e32 v10, s63, v4
	v_add_u32_e32 v11, s63, v10
	v_add_u32_e32 v12, s63, v11
	v_add_u32_e32 v19, s63, v12
	v_add_u32_e32 v24, s63, v19
	v_add_u32_e32 v25, s63, v24
	global_load_dwordx4 v[66:69], v0, s[2:3] nt
	global_load_dwordx4 v[70:73], v4, s[2:3] nt
	global_load_dwordx4 v[74:77], v10, s[2:3] nt
	global_load_dwordx4 v[78:81], v11, s[2:3] nt
	global_load_dwordx4 v[82:85], v12, s[2:3] nt
	global_load_dwordx4 v[86:89], v19, s[2:3] nt
	global_load_dwordx4 v[102:105], v24, s[2:3] nt
	global_load_dwordx4 v[106:109], v25, s[2:3] nt
	s_cmp_lt_u32 s32, 0x6a80
	s_cbranch_scc0 .Lcv102_drain2
	s_waitcnt vmcnt(24)
	s_lshl_b32 s60, s67, 2
	v_mul_lo_u32 v27, v97, s60
	s_cmp_eq_u32 s78, 0
	s_cbranch_scc1 .Lcv102_p8_bf
	v_lshl_add_u32 v27, v96, 3, v27
	v_add_u32_e32 v32, s67, v27
	v_add_u32_e32 v92, s67, v32
	v_add_u32_e32 v94, s67, v92
	v_mul_f32_e32 v110, s78, v110
	v_mul_f32_e32 v111, s78, v111
	v_mul_f32_e32 v112, s78, v112
	v_mul_f32_e32 v113, s78, v113
	v_mul_f32_e32 v114, s78, v114
	v_mul_f32_e32 v115, s78, v115
	v_mul_f32_e32 v116, s78, v116
	v_mul_f32_e32 v117, s78, v117
	v_mul_f32_e32 v118, s78, v118
	v_mul_f32_e32 v119, s78, v119
	v_mul_f32_e32 v120, s78, v120
	v_mul_f32_e32 v121, s78, v121
	v_mul_f32_e32 v122, s78, v122
	v_mul_f32_e32 v123, s78, v123
	v_mul_f32_e32 v124, s78, v124
	v_mul_f32_e32 v125, s78, v125
	v_mul_f32_e32 v126, s78, v126
	v_mul_f32_e32 v127, s78, v127
	v_mul_f32_e32 v128, s78, v128
	v_mul_f32_e32 v129, s78, v129
	v_mul_f32_e32 v130, s78, v130
	v_mul_f32_e32 v131, s78, v131
	v_mul_f32_e32 v132, s78, v132
	v_mul_f32_e32 v133, s78, v133
	v_mul_f32_e32 v134, s78, v134
	v_mul_f32_e32 v135, s78, v135
	v_mul_f32_e32 v136, s78, v136
	v_mul_f32_e32 v137, s78, v137
	v_mul_f32_e32 v138, s78, v138
	v_mul_f32_e32 v139, s78, v139
	v_mul_f32_e32 v140, s78, v140
	v_mul_f32_e32 v141, s78, v141
	v_med3_f32 v110, v110, s64, v98
	v_med3_f32 v111, v111, s64, v98
	v_med3_f32 v112, v112, s64, v98
	v_med3_f32 v113, v113, s64, v98
	v_med3_f32 v114, v114, s64, v98
	v_med3_f32 v115, v115, s64, v98
	v_med3_f32 v116, v116, s64, v98
	v_med3_f32 v117, v117, s64, v98
	v_med3_f32 v118, v118, s64, v98
	v_med3_f32 v119, v119, s64, v98
	v_med3_f32 v120, v120, s64, v98
	v_med3_f32 v121, v121, s64, v98
	v_med3_f32 v122, v122, s64, v98
	v_med3_f32 v123, v123, s64, v98
	v_med3_f32 v124, v124, s64, v98
	v_med3_f32 v125, v125, s64, v98
	v_med3_f32 v126, v126, s64, v98
	v_med3_f32 v127, v127, s64, v98
	v_med3_f32 v128, v128, s64, v98
	v_med3_f32 v129, v129, s64, v98
	v_med3_f32 v130, v130, s64, v98
	v_med3_f32 v131, v131, s64, v98
	v_med3_f32 v132, v132, s64, v98
	v_med3_f32 v133, v133, s64, v98
	v_med3_f32 v134, v134, s64, v98
	v_med3_f32 v135, v135, s64, v98
	v_med3_f32 v136, v136, s64, v98
	v_med3_f32 v137, v137, s64, v98
	v_med3_f32 v138, v138, s64, v98
	v_med3_f32 v139, v139, s64, v98
	v_med3_f32 v140, v140, s64, v98
	v_med3_f32 v141, v141, s64, v98
	v_cvt_pk_fp8_f32 v148, v110, v114
	v_cvt_pk_fp8_f32 v149, v126, v130
	v_cvt_pk_fp8_f32 v152, v111, v115
	v_cvt_pk_fp8_f32 v153, v127, v131
	v_cvt_pk_fp8_f32 v158, v112, v116
	v_cvt_pk_fp8_f32 v159, v128, v132
	v_cvt_pk_fp8_f32 v196, v113, v117
	v_cvt_pk_fp8_f32 v197, v129, v133
	v_cvt_pk_fp8_f32 v148, v118, v122 op_sel:[0,0,1]
	v_cvt_pk_fp8_f32 v149, v134, v138 op_sel:[0,0,1]
	v_cvt_pk_fp8_f32 v152, v119, v123 op_sel:[0,0,1]
	v_cvt_pk_fp8_f32 v153, v135, v139 op_sel:[0,0,1]
	v_cvt_pk_fp8_f32 v158, v120, v124 op_sel:[0,0,1]
	v_cvt_pk_fp8_f32 v159, v136, v140 op_sel:[0,0,1]
	v_cvt_pk_fp8_f32 v196, v121, v125 op_sel:[0,0,1]
	v_cvt_pk_fp8_f32 v197, v137, v141 op_sel:[0,0,1]
	s_nop 1
	global_store_dwordx2 v27, v[148:149], s[54:55]
	global_store_dwordx2 v32, v[152:153], s[54:55]
	global_store_dwordx2 v92, v[158:159], s[54:55]
	global_store_dwordx2 v94, v[196:197], s[54:55]
	s_branch .Lcv102_p8_end
.Lcv102_p8_bf:
	v_lshl_add_u32 v27, v96, 4, v27
	v_add_u32_e32 v32, s67, v27
	v_add_u32_e32 v92, s67, v32
	v_add_u32_e32 v94, s67, v92
	v_cvt_pk_bf16_f32 v148, v110, v114
	v_cvt_pk_bf16_f32 v149, v118, v122
	v_cvt_pk_bf16_f32 v202, v126, v130
	v_cvt_pk_bf16_f32 v203, v134, v138
	v_cvt_pk_bf16_f32 v152, v111, v115
	v_cvt_pk_bf16_f32 v153, v119, v123
	v_cvt_pk_bf16_f32 v208, v127, v131
	v_cvt_pk_bf16_f32 v209, v135, v139
	v_cvt_pk_bf16_f32 v158, v112, v116
	v_cvt_pk_bf16_f32 v159, v120, v124
	v_cvt_pk_bf16_f32 v220, v128, v132
	v_cvt_pk_bf16_f32 v221, v136, v140
	v_cvt_pk_bf16_f32 v196, v113, v117
	v_cvt_pk_bf16_f32 v197, v121, v125
	v_cvt_pk_bf16_f32 v226, v129, v133
	v_cvt_pk_bf16_f32 v227, v137, v141
	s_nop 1
	global_store_dwordx2 v27, v[148:149], s[54:55]
	global_store_dwordx2 v27, v[202:203], s[54:55] offset:8
	global_store_dwordx2 v32, v[152:153], s[54:55]
	global_store_dwordx2 v32, v[208:209], s[54:55] offset:8
	global_store_dwordx2 v92, v[158:159], s[54:55]
	global_store_dwordx2 v92, v[220:221], s[54:55] offset:8
	global_store_dwordx2 v94, v[196:197], s[54:55]
	global_store_dwordx2 v94, v[226:227], s[54:55] offset:8
.Lcv102_p8_end:
	s_add_u32 s43, s32, 2
	s_cmp_lt_u32 s43, 0x600
	s_cbranch_scc0 .Lcv102_d9_b
	s_mul_i32 s58, s43, 0xaaab
	s_lshr_b32 s58, s58, 22
	s_mul_i32 s59, s58, 96
	s_sub_u32 s59, s43, s59
	s_mul_i32 s60, s58, 0xc0000
	s_mul_i32 s81, s59, 0x80
	s_add_u32 s60, s60, s81
	s_add_u32 s2, s10, s60
	s_addc_u32 s3, s11, 0
	s_mov_b32 s63, 0x3000
	s_mul_i32 s61, s59, 0x8000
	s_mul_i32 s81, s58, 0x40
	s_add_u32 s61, s61, s81
	s_add_u32 s61, s61, 0x800000
	s_add_u32 s54, s48, s61
	s_addc_u32 s55, s49, 0
	s_mov_b32 s67, 0x400
	s_mov_b32 s78, 0x44000000
	s_branch .Lcv102_d9_ld

.Lcv102_d9_ld:
	s_lshl_b32 s60, s63, 3
	v_mul_lo_u32 v0, v96, s60
	v_lshl_add_u32 v0, v97, 4, v0
	v_add_u32_e32 v4, s63, v0
	v_add_u32_e32 v10, s63, v4
	v_add_u32_e32 v11, s63, v10
	v_add_u32_e32 v12, s63, v11
	v_add_u32_e32 v19, s63, v12
	v_add_u32_e32 v24, s63, v19
	v_add_u32_e32 v25, s63, v24
	global_load_dwordx4 v[110:113], v0, s[2:3] nt
	global_load_dwordx4 v[114:117], v4, s[2:3] nt
	global_load_dwordx4 v[118:121], v10, s[2:3] nt
	global_load_dwordx4 v[122:125], v11, s[2:3] nt
	global_load_dwordx4 v[126:129], v12, s[2:3] nt
	global_load_dwordx4 v[130:133], v19, s[2:3] nt
	global_load_dwordx4 v[134:137], v24, s[2:3] nt
	global_load_dwordx4 v[138:141], v25, s[2:3] nt
	s_cmp_lt_u32 s32, 0x6a80
	s_cbranch_scc0 .Lcv102_drain3
	s_waitcnt vmcnt(24)
	s_lshl_b32 s60, s69, 2
	v_mul_lo_u32 v27, v97, s60
	s_cmp_eq_u32 s79, 0
	s_cbranch_scc1 .Lcv102_p10_bf
	v_lshl_add_u32 v27, v96, 3, v27
	v_add_u32_e32 v32, s69, v27
	v_add_u32_e32 v92, s69, v32
	v_add_u32_e32 v94, s69, v92
	v_mul_f32_e32 v142, s79, v142
	v_mul_f32_e32 v143, s79, v143
	v_mul_f32_e32 v144, s79, v144
	v_mul_f32_e32 v145, s79, v145
	v_mul_f32_e32 v172, s79, v172
	v_mul_f32_e32 v173, s79, v173
	v_mul_f32_e32 v174, s79, v174
	v_mul_f32_e32 v175, s79, v175
	v_mul_f32_e32 v176, s79, v176
	v_mul_f32_e32 v177, s79, v177
	v_mul_f32_e32 v178, s79, v178
	v_mul_f32_e32 v179, s79, v179
	v_mul_f32_e32 v180, s79, v180
	v_mul_f32_e32 v181, s79, v181
	v_mul_f32_e32 v182, s79, v182
	v_mul_f32_e32 v183, s79, v183
	v_mul_f32_e32 v184, s79, v184
	v_mul_f32_e32 v185, s79, v185
	v_mul_f32_e32 v186, s79, v186
	v_mul_f32_e32 v187, s79, v187
	v_mul_f32_e32 v188, s79, v188
	v_mul_f32_e32 v189, s79, v189
	v_mul_f32_e32 v190, s79, v190
	v_mul_f32_e32 v191, s79, v191
	v_mul_f32_e32 v162, s79, v162
	v_mul_f32_e32 v163, s79, v163
	v_mul_f32_e32 v164, s79, v164
	v_mul_f32_e32 v165, s79, v165
	v_mul_f32_e32 v6, s79, v6
	v_mul_f32_e32 v7, s79, v7
	v_mul_f32_e32 v8, s79, v8
	v_mul_f32_e32 v9, s79, v9
	v_med3_f32 v142, v142, s64, v98
	v_med3_f32 v143, v143, s64, v98
	v_med3_f32 v144, v144, s64, v98
	v_med3_f32 v145, v145, s64, v98
	v_med3_f32 v172, v172, s64, v98
	v_med3_f32 v173, v173, s64, v98
	v_med3_f32 v174, v174, s64, v98
	v_med3_f32 v175, v175, s64, v98
	v_med3_f32 v176, v176, s64, v98
	v_med3_f32 v177, v177, s64, v98
	v_med3_f32 v178, v178, s64, v98
	v_med3_f32 v179, v179, s64, v98
	v_med3_f32 v180, v180, s64, v98
	v_med3_f32 v181, v181, s64, v98
	v_med3_f32 v182, v182, s64, v98
	v_med3_f32 v183, v183, s64, v98
	v_med3_f32 v184, v184, s64, v98
	v_med3_f32 v185, v185, s64, v98
	v_med3_f32 v186, v186, s64, v98
	v_med3_f32 v187, v187, s64, v98
	v_med3_f32 v188, v188, s64, v98
	v_med3_f32 v189, v189, s64, v98
	v_med3_f32 v190, v190, s64, v98
	v_med3_f32 v191, v191, s64, v98
	v_med3_f32 v162, v162, s64, v98
	v_med3_f32 v163, v163, s64, v98
	v_med3_f32 v164, v164, s64, v98
	v_med3_f32 v165, v165, s64, v98
	v_med3_f32 v6, v6, s64, v98
	v_med3_f32 v7, v7, s64, v98
	v_med3_f32 v8, v8, s64, v98
	v_med3_f32 v9, v9, s64, v98
	v_cvt_pk_fp8_f32 v148, v142, v172
	v_cvt_pk_fp8_f32 v149, v184, v188
	v_cvt_pk_fp8_f32 v152, v143, v173
	v_cvt_pk_fp8_f32 v153, v185, v189
	v_cvt_pk_fp8_f32 v158, v144, v174
	v_cvt_pk_fp8_f32 v159, v186, v190
	v_cvt_pk_fp8_f32 v196, v145, v175
	v_cvt_pk_fp8_f32 v197, v187, v191
	v_cvt_pk_fp8_f32 v148, v176, v180 op_sel:[0,0,1]
	v_cvt_pk_fp8_f32 v149, v162, v6 op_sel:[0,0,1]
	v_cvt_pk_fp8_f32 v152, v177, v181 op_sel:[0,0,1]
	v_cvt_pk_fp8_f32 v153, v163, v7 op_sel:[0,0,1]
	v_cvt_pk_fp8_f32 v158, v178, v182 op_sel:[0,0,1]
	v_cvt_pk_fp8_f32 v159, v164, v8 op_sel:[0,0,1]
	v_cvt_pk_fp8_f32 v196, v179, v183 op_sel:[0,0,1]
	v_cvt_pk_fp8_f32 v197, v165, v9 op_sel:[0,0,1]
	s_nop 1
	global_store_dwordx2 v27, v[148:149], s[56:57]
	global_store_dwordx2 v32, v[152:153], s[56:57]
	global_store_dwordx2 v92, v[158:159], s[56:57]
	global_store_dwordx2 v94, v[196:197], s[56:57]
	s_branch .Lcv102_p10_end
.Lcv102_p10_bf:
	v_lshl_add_u32 v27, v96, 4, v27
	v_add_u32_e32 v32, s69, v27
	v_add_u32_e32 v92, s69, v32
	v_add_u32_e32 v94, s69, v92
	v_cvt_pk_bf16_f32 v148, v142, v172
	v_cvt_pk_bf16_f32 v149, v176, v180
	v_cvt_pk_bf16_f32 v202, v184, v188
	v_cvt_pk_bf16_f32 v203, v162, v6
	v_cvt_pk_bf16_f32 v152, v143, v173
	v_cvt_pk_bf16_f32 v153, v177, v181
	v_cvt_pk_bf16_f32 v208, v185, v189
	v_cvt_pk_bf16_f32 v209, v163, v7
	v_cvt_pk_bf16_f32 v158, v144, v174
	v_cvt_pk_bf16_f32 v159, v178, v182
	v_cvt_pk_bf16_f32 v220, v186, v190
	v_cvt_pk_bf16_f32 v221, v164, v8
	v_cvt_pk_bf16_f32 v196, v145, v175
	v_cvt_pk_bf16_f32 v197, v179, v183
	v_cvt_pk_bf16_f32 v226, v187, v191
	v_cvt_pk_bf16_f32 v227, v165, v9
	s_nop 1
	global_store_dwordx2 v27, v[148:149], s[56:57]
	global_store_dwordx2 v27, v[202:203], s[56:57] offset:8
	global_store_dwordx2 v32, v[152:153], s[56:57]
	global_store_dwordx2 v32, v[208:209], s[56:57] offset:8
	global_store_dwordx2 v92, v[158:159], s[56:57]
	global_store_dwordx2 v92, v[220:221], s[56:57] offset:8
	global_store_dwordx2 v94, v[196:197], s[56:57]
	global_store_dwordx2 v94, v[226:227], s[56:57] offset:8
.Lcv102_p10_end:
	s_add_u32 s43, s32, 3
	s_cmp_lt_u32 s43, 0x600
	s_cbranch_scc0 .Lcv102_d11_b
	s_mul_i32 s58, s43, 0xaaab
	s_lshr_b32 s58, s58, 22
	s_mul_i32 s59, s58, 96
	s_sub_u32 s59, s43, s59
	s_mul_i32 s60, s58, 0xc0000
	s_mul_i32 s81, s59, 0x80
	s_add_u32 s60, s60, s81
	s_add_u32 s2, s10, s60
	s_addc_u32 s3, s11, 0
	s_mov_b32 s63, 0x3000
	s_mul_i32 s61, s59, 0x8000
	s_mul_i32 s81, s58, 0x40
	s_add_u32 s61, s61, s81
	s_add_u32 s61, s61, 0x800000
	s_add_u32 s56, s48, s61
	s_addc_u32 s57, s49, 0
	s_mov_b32 s69, 0x400
	s_mov_b32 s79, 0x44000000
	s_branch .Lcv102_d11_ld

.Lcv102_d11_ld:
	s_lshl_b32 s60, s63, 3
	v_mul_lo_u32 v0, v96, s60
	v_lshl_add_u32 v0, v97, 4, v0
	v_add_u32_e32 v4, s63, v0
	v_add_u32_e32 v10, s63, v4
	v_add_u32_e32 v11, s63, v10
	v_add_u32_e32 v12, s63, v11
	v_add_u32_e32 v19, s63, v12
	v_add_u32_e32 v24, s63, v19
	v_add_u32_e32 v25, s63, v24
	global_load_dwordx4 v[142:145], v0, s[2:3] nt
	global_load_dwordx4 v[172:175], v4, s[2:3] nt
	global_load_dwordx4 v[176:179], v10, s[2:3] nt
	global_load_dwordx4 v[180:183], v11, s[2:3] nt
	global_load_dwordx4 v[184:187], v12, s[2:3] nt
	global_load_dwordx4 v[188:191], v19, s[2:3] nt
	global_load_dwordx4 v[162:165], v24, s[2:3] nt
	global_load_dwordx4 v[6:9], v25, s[2:3] nt
	s_add_u32 s32, s32, s20
	s_branch .Lcv102_loop
.Lcv102_drain0:
	s_waitcnt vmcnt(0)
	s_cmp_gt_u32 s41, 0
	s_cbranch_scc0 .Lcv102_done
	s_lshl_b32 s60, s65, 2
	v_mul_lo_u32 v27, v97, s60
	s_cmp_eq_u32 s71, 0
	s_cbranch_scc1 .Lcv102_p12_bf
	v_lshl_add_u32 v27, v96, 3, v27
	v_add_u32_e32 v32, s65, v27
	v_add_u32_e32 v92, s65, v32
	v_add_u32_e32 v94, s65, v92
	v_mul_f32_e32 v34, s71, v34
	v_mul_f32_e32 v35, s71, v35
	v_mul_f32_e32 v36, s71, v36
	v_mul_f32_e32 v37, s71, v37
	v_mul_f32_e32 v38, s71, v38
	v_mul_f32_e32 v39, s71, v39
	v_mul_f32_e32 v40, s71, v40
	v_mul_f32_e32 v41, s71, v41
	v_mul_f32_e32 v42, s71, v42
	v_mul_f32_e32 v43, s71, v43
	v_mul_f32_e32 v44, s71, v44
	v_mul_f32_e32 v45, s71, v45
	v_mul_f32_e32 v46, s71, v46
	v_mul_f32_e32 v47, s71, v47
	v_mul_f32_e32 v48, s71, v48
	v_mul_f32_e32 v49, s71, v49
	v_mul_f32_e32 v50, s71, v50
	v_mul_f32_e32 v51, s71, v51
	v_mul_f32_e32 v52, s71, v52
	v_mul_f32_e32 v53, s71, v53
	v_mul_f32_e32 v54, s71, v54
	v_mul_f32_e32 v55, s71, v55
	v_mul_f32_e32 v56, s71, v56
	v_mul_f32_e32 v57, s71, v57
	v_mul_f32_e32 v58, s71, v58
	v_mul_f32_e32 v59, s71, v59
	v_mul_f32_e32 v60, s71, v60
	v_mul_f32_e32 v61, s71, v61
	v_mul_f32_e32 v62, s71, v62
	v_mul_f32_e32 v63, s71, v63
	v_mul_f32_e32 v64, s71, v64
	v_mul_f32_e32 v65, s71, v65
	v_med3_f32 v34, v34, s64, v98
	v_med3_f32 v35, v35, s64, v98
	v_med3_f32 v36, v36, s64, v98
	v_med3_f32 v37, v37, s64, v98
	v_med3_f32 v38, v38, s64, v98
	v_med3_f32 v39, v39, s64, v98
	v_med3_f32 v40, v40, s64, v98
	v_med3_f32 v41, v41, s64, v98
	v_med3_f32 v42, v42, s64, v98
	v_med3_f32 v43, v43, s64, v98
	v_med3_f32 v44, v44, s64, v98
	v_med3_f32 v45, v45, s64, v98
	v_med3_f32 v46, v46, s64, v98
	v_med3_f32 v47, v47, s64, v98
	v_med3_f32 v48, v48, s64, v98
	v_med3_f32 v49, v49, s64, v98
	v_med3_f32 v50, v50, s64, v98
	v_med3_f32 v51, v51, s64, v98
	v_med3_f32 v52, v52, s64, v98
	v_med3_f32 v53, v53, s64, v98
	v_med3_f32 v54, v54, s64, v98
	v_med3_f32 v55, v55, s64, v98
	v_med3_f32 v56, v56, s64, v98
	v_med3_f32 v57, v57, s64, v98
	v_med3_f32 v58, v58, s64, v98
	v_med3_f32 v59, v59, s64, v98
	v_med3_f32 v60, v60, s64, v98
	v_med3_f32 v61, v61, s64, v98
	v_med3_f32 v62, v62, s64, v98
	v_med3_f32 v63, v63, s64, v98
	v_med3_f32 v64, v64, s64, v98
	v_med3_f32 v65, v65, s64, v98
	v_cvt_pk_fp8_f32 v148, v34, v38
	v_cvt_pk_fp8_f32 v149, v50, v54
	v_cvt_pk_fp8_f32 v152, v35, v39
	v_cvt_pk_fp8_f32 v153, v51, v55
	v_cvt_pk_fp8_f32 v158, v36, v40
	v_cvt_pk_fp8_f32 v159, v52, v56
	v_cvt_pk_fp8_f32 v196, v37, v41
	v_cvt_pk_fp8_f32 v197, v53, v57
	v_cvt_pk_fp8_f32 v148, v42, v46 op_sel:[0,0,1]
	v_cvt_pk_fp8_f32 v149, v58, v62 op_sel:[0,0,1]
	v_cvt_pk_fp8_f32 v152, v43, v47 op_sel:[0,0,1]
	v_cvt_pk_fp8_f32 v153, v59, v63 op_sel:[0,0,1]
	v_cvt_pk_fp8_f32 v158, v44, v48 op_sel:[0,0,1]
	v_cvt_pk_fp8_f32 v159, v60, v64 op_sel:[0,0,1]
	v_cvt_pk_fp8_f32 v196, v45, v49 op_sel:[0,0,1]
	v_cvt_pk_fp8_f32 v197, v61, v65 op_sel:[0,0,1]
	s_nop 1
	global_store_dwordx2 v27, v[148:149], s[50:51]
	global_store_dwordx2 v32, v[152:153], s[50:51]
	global_store_dwordx2 v92, v[158:159], s[50:51]
	global_store_dwordx2 v94, v[196:197], s[50:51]
	s_branch .Lcv102_p12_end

.Lcv102_p12_end:
	s_cmp_gt_u32 s41, 1
	s_cbranch_scc0 .Lcv102_done
	s_lshl_b32 s60, s66, 2
	v_mul_lo_u32 v27, v97, s60
	s_cmp_eq_u32 s75, 0
	s_cbranch_scc1 .Lcv102_p13_bf
	v_lshl_add_u32 v27, v96, 3, v27
	v_add_u32_e32 v32, s66, v27
	v_add_u32_e32 v92, s66, v32
	v_add_u32_e32 v94, s66, v92
	v_mul_f32_e32 v66, s75, v66
	v_mul_f32_e32 v67, s75, v67
	v_mul_f32_e32 v68, s75, v68
	v_mul_f32_e32 v69, s75, v69
	v_mul_f32_e32 v70, s75, v70
	v_mul_f32_e32 v71, s75, v71
	v_mul_f32_e32 v72, s75, v72
	v_mul_f32_e32 v73, s75, v73
	v_mul_f32_e32 v74, s75, v74
	v_mul_f32_e32 v75, s75, v75
	v_mul_f32_e32 v76, s75, v76
	v_mul_f32_e32 v77, s75, v77
	v_mul_f32_e32 v78, s75, v78
	v_mul_f32_e32 v79, s75, v79
	v_mul_f32_e32 v80, s75, v80
	v_mul_f32_e32 v81, s75, v81
	v_mul_f32_e32 v82, s75, v82
	v_mul_f32_e32 v83, s75, v83
	v_mul_f32_e32 v84, s75, v84
	v_mul_f32_e32 v85, s75, v85
	v_mul_f32_e32 v86, s75, v86
	v_mul_f32_e32 v87, s75, v87
	v_mul_f32_e32 v88, s75, v88
	v_mul_f32_e32 v89, s75, v89
	v_mul_f32_e32 v102, s75, v102
	v_mul_f32_e32 v103, s75, v103
	v_mul_f32_e32 v104, s75, v104
	v_mul_f32_e32 v105, s75, v105
	v_mul_f32_e32 v106, s75, v106
	v_mul_f32_e32 v107, s75, v107
	v_mul_f32_e32 v108, s75, v108
	v_mul_f32_e32 v109, s75, v109
	v_med3_f32 v66, v66, s64, v98
	v_med3_f32 v67, v67, s64, v98
	v_med3_f32 v68, v68, s64, v98
	v_med3_f32 v69, v69, s64, v98
	v_med3_f32 v70, v70, s64, v98
	v_med3_f32 v71, v71, s64, v98
	v_med3_f32 v72, v72, s64, v98
	v_med3_f32 v73, v73, s64, v98
	v_med3_f32 v74, v74, s64, v98
	v_med3_f32 v75, v75, s64, v98
	v_med3_f32 v76, v76, s64, v98
	v_med3_f32 v77, v77, s64, v98
	v_med3_f32 v78, v78, s64, v98
	v_med3_f32 v79, v79, s64, v98
	v_med3_f32 v80, v80, s64, v98
	v_med3_f32 v81, v81, s64, v98
	v_med3_f32 v82, v82, s64, v98
	v_med3_f32 v83, v83, s64, v98
	v_med3_f32 v84, v84, s64, v98
	v_med3_f32 v85, v85, s64, v98
	v_med3_f32 v86, v86, s64, v98
	v_med3_f32 v87, v87, s64, v98
	v_med3_f32 v88, v88, s64, v98
	v_med3_f32 v89, v89, s64, v98
	v_med3_f32 v102, v102, s64, v98
	v_med3_f32 v103, v103, s64, v98
	v_med3_f32 v104, v104, s64, v98
	v_med3_f32 v105, v105, s64, v98
	v_med3_f32 v106, v106, s64, v98
	v_med3_f32 v107, v107, s64, v98
	v_med3_f32 v108, v108, s64, v98
	v_med3_f32 v109, v109, s64, v98
	v_cvt_pk_fp8_f32 v148, v66, v70
	v_cvt_pk_fp8_f32 v149, v82, v86
	v_cvt_pk_fp8_f32 v152, v67, v71
	v_cvt_pk_fp8_f32 v153, v83, v87
	v_cvt_pk_fp8_f32 v158, v68, v72
	v_cvt_pk_fp8_f32 v159, v84, v88
	v_cvt_pk_fp8_f32 v196, v69, v73
	v_cvt_pk_fp8_f32 v197, v85, v89
	v_cvt_pk_fp8_f32 v148, v74, v78 op_sel:[0,0,1]
	v_cvt_pk_fp8_f32 v149, v102, v106 op_sel:[0,0,1]
	v_cvt_pk_fp8_f32 v152, v75, v79 op_sel:[0,0,1]
	v_cvt_pk_fp8_f32 v153, v103, v107 op_sel:[0,0,1]
	v_cvt_pk_fp8_f32 v158, v76, v80 op_sel:[0,0,1]
	v_cvt_pk_fp8_f32 v159, v104, v108 op_sel:[0,0,1]
	v_cvt_pk_fp8_f32 v196, v77, v81 op_sel:[0,0,1]
	v_cvt_pk_fp8_f32 v197, v105, v109 op_sel:[0,0,1]
	s_nop 1
	global_store_dwordx2 v27, v[148:149], s[52:53]
	global_store_dwordx2 v32, v[152:153], s[52:53]
	global_store_dwordx2 v92, v[158:159], s[52:53]
	global_store_dwordx2 v94, v[196:197], s[52:53]
	s_branch .Lcv102_p13_end

.Lcv102_p13_end:
	s_cmp_gt_u32 s41, 2
	s_cbranch_scc0 .Lcv102_done
	s_lshl_b32 s60, s67, 2
	v_mul_lo_u32 v27, v97, s60
	s_cmp_eq_u32 s78, 0
	s_cbranch_scc1 .Lcv102_p14_bf
	v_lshl_add_u32 v27, v96, 3, v27
	v_add_u32_e32 v32, s67, v27
	v_add_u32_e32 v92, s67, v32
	v_add_u32_e32 v94, s67, v92
	v_mul_f32_e32 v110, s78, v110
	v_mul_f32_e32 v111, s78, v111
	v_mul_f32_e32 v112, s78, v112
	v_mul_f32_e32 v113, s78, v113
	v_mul_f32_e32 v114, s78, v114
	v_mul_f32_e32 v115, s78, v115
	v_mul_f32_e32 v116, s78, v116
	v_mul_f32_e32 v117, s78, v117
	v_mul_f32_e32 v118, s78, v118
	v_mul_f32_e32 v119, s78, v119
	v_mul_f32_e32 v120, s78, v120
	v_mul_f32_e32 v121, s78, v121
	v_mul_f32_e32 v122, s78, v122
	v_mul_f32_e32 v123, s78, v123
	v_mul_f32_e32 v124, s78, v124
	v_mul_f32_e32 v125, s78, v125
	v_mul_f32_e32 v126, s78, v126
	v_mul_f32_e32 v127, s78, v127
	v_mul_f32_e32 v128, s78, v128
	v_mul_f32_e32 v129, s78, v129
	v_mul_f32_e32 v130, s78, v130
	v_mul_f32_e32 v131, s78, v131
	v_mul_f32_e32 v132, s78, v132
	v_mul_f32_e32 v133, s78, v133
	v_mul_f32_e32 v134, s78, v134
	v_mul_f32_e32 v135, s78, v135
	v_mul_f32_e32 v136, s78, v136
	v_mul_f32_e32 v137, s78, v137
	v_mul_f32_e32 v138, s78, v138
	v_mul_f32_e32 v139, s78, v139
	v_mul_f32_e32 v140, s78, v140
	v_mul_f32_e32 v141, s78, v141
	v_med3_f32 v110, v110, s64, v98
	v_med3_f32 v111, v111, s64, v98
	v_med3_f32 v112, v112, s64, v98
	v_med3_f32 v113, v113, s64, v98
	v_med3_f32 v114, v114, s64, v98
	v_med3_f32 v115, v115, s64, v98
	v_med3_f32 v116, v116, s64, v98
	v_med3_f32 v117, v117, s64, v98
	v_med3_f32 v118, v118, s64, v98
	v_med3_f32 v119, v119, s64, v98
	v_med3_f32 v120, v120, s64, v98
	v_med3_f32 v121, v121, s64, v98
	v_med3_f32 v122, v122, s64, v98
	v_med3_f32 v123, v123, s64, v98
	v_med3_f32 v124, v124, s64, v98
	v_med3_f32 v125, v125, s64, v98
	v_med3_f32 v126, v126, s64, v98
	v_med3_f32 v127, v127, s64, v98
	v_med3_f32 v128, v128, s64, v98
	v_med3_f32 v129, v129, s64, v98
	v_med3_f32 v130, v130, s64, v98
	v_med3_f32 v131, v131, s64, v98
	v_med3_f32 v132, v132, s64, v98
	v_med3_f32 v133, v133, s64, v98
	v_med3_f32 v134, v134, s64, v98
	v_med3_f32 v135, v135, s64, v98
	v_med3_f32 v136, v136, s64, v98
	v_med3_f32 v137, v137, s64, v98
	v_med3_f32 v138, v138, s64, v98
	v_med3_f32 v139, v139, s64, v98
	v_med3_f32 v140, v140, s64, v98
	v_med3_f32 v141, v141, s64, v98
	v_cvt_pk_fp8_f32 v148, v110, v114
	v_cvt_pk_fp8_f32 v149, v126, v130
	v_cvt_pk_fp8_f32 v152, v111, v115
	v_cvt_pk_fp8_f32 v153, v127, v131
	v_cvt_pk_fp8_f32 v158, v112, v116
	v_cvt_pk_fp8_f32 v159, v128, v132
	v_cvt_pk_fp8_f32 v196, v113, v117
	v_cvt_pk_fp8_f32 v197, v129, v133
	v_cvt_pk_fp8_f32 v148, v118, v122 op_sel:[0,0,1]
	v_cvt_pk_fp8_f32 v149, v134, v138 op_sel:[0,0,1]
	v_cvt_pk_fp8_f32 v152, v119, v123 op_sel:[0,0,1]
	v_cvt_pk_fp8_f32 v153, v135, v139 op_sel:[0,0,1]
	v_cvt_pk_fp8_f32 v158, v120, v124 op_sel:[0,0,1]
	v_cvt_pk_fp8_f32 v159, v136, v140 op_sel:[0,0,1]
	v_cvt_pk_fp8_f32 v196, v121, v125 op_sel:[0,0,1]
	v_cvt_pk_fp8_f32 v197, v137, v141 op_sel:[0,0,1]
	s_nop 1
	global_store_dwordx2 v27, v[148:149], s[54:55]
	global_store_dwordx2 v32, v[152:153], s[54:55]
	global_store_dwordx2 v92, v[158:159], s[54:55]
	global_store_dwordx2 v94, v[196:197], s[54:55]
	s_branch .Lcv102_p14_end

.Lcv102_p14_end:
	s_cmp_gt_u32 s41, 3
	s_cbranch_scc0 .Lcv102_done
	s_lshl_b32 s60, s69, 2
	v_mul_lo_u32 v27, v97, s60
	s_cmp_eq_u32 s79, 0
	s_cbranch_scc1 .Lcv102_p15_bf
	v_lshl_add_u32 v27, v96, 3, v27
	v_add_u32_e32 v32, s69, v27
	v_add_u32_e32 v92, s69, v32
	v_add_u32_e32 v94, s69, v92
	v_mul_f32_e32 v142, s79, v142
	v_mul_f32_e32 v143, s79, v143
	v_mul_f32_e32 v144, s79, v144
	v_mul_f32_e32 v145, s79, v145
	v_mul_f32_e32 v172, s79, v172
	v_mul_f32_e32 v173, s79, v173
	v_mul_f32_e32 v174, s79, v174
	v_mul_f32_e32 v175, s79, v175
	v_mul_f32_e32 v176, s79, v176
	v_mul_f32_e32 v177, s79, v177
	v_mul_f32_e32 v178, s79, v178
	v_mul_f32_e32 v179, s79, v179
	v_mul_f32_e32 v180, s79, v180
	v_mul_f32_e32 v181, s79, v181
	v_mul_f32_e32 v182, s79, v182
	v_mul_f32_e32 v183, s79, v183
	v_mul_f32_e32 v184, s79, v184
	v_mul_f32_e32 v185, s79, v185
	v_mul_f32_e32 v186, s79, v186
	v_mul_f32_e32 v187, s79, v187
	v_mul_f32_e32 v188, s79, v188
	v_mul_f32_e32 v189, s79, v189
	v_mul_f32_e32 v190, s79, v190
	v_mul_f32_e32 v191, s79, v191
	v_mul_f32_e32 v162, s79, v162
	v_mul_f32_e32 v163, s79, v163
	v_mul_f32_e32 v164, s79, v164
	v_mul_f32_e32 v165, s79, v165
	v_mul_f32_e32 v6, s79, v6
	v_mul_f32_e32 v7, s79, v7
	v_mul_f32_e32 v8, s79, v8
	v_mul_f32_e32 v9, s79, v9
	v_med3_f32 v142, v142, s64, v98
	v_med3_f32 v143, v143, s64, v98
	v_med3_f32 v144, v144, s64, v98
	v_med3_f32 v145, v145, s64, v98
	v_med3_f32 v172, v172, s64, v98
	v_med3_f32 v173, v173, s64, v98
	v_med3_f32 v174, v174, s64, v98
	v_med3_f32 v175, v175, s64, v98
	v_med3_f32 v176, v176, s64, v98
	v_med3_f32 v177, v177, s64, v98
	v_med3_f32 v178, v178, s64, v98
	v_med3_f32 v179, v179, s64, v98
	v_med3_f32 v180, v180, s64, v98
	v_med3_f32 v181, v181, s64, v98
	v_med3_f32 v182, v182, s64, v98
	v_med3_f32 v183, v183, s64, v98
	v_med3_f32 v184, v184, s64, v98
	v_med3_f32 v185, v185, s64, v98
	v_med3_f32 v186, v186, s64, v98
	v_med3_f32 v187, v187, s64, v98
	v_med3_f32 v188, v188, s64, v98
	v_med3_f32 v189, v189, s64, v98
	v_med3_f32 v190, v190, s64, v98
	v_med3_f32 v191, v191, s64, v98
	v_med3_f32 v162, v162, s64, v98
	v_med3_f32 v163, v163, s64, v98
	v_med3_f32 v164, v164, s64, v98
	v_med3_f32 v165, v165, s64, v98
	v_med3_f32 v6, v6, s64, v98
	v_med3_f32 v7, v7, s64, v98
	v_med3_f32 v8, v8, s64, v98
	v_med3_f32 v9, v9, s64, v98
	v_cvt_pk_fp8_f32 v148, v142, v172
	v_cvt_pk_fp8_f32 v149, v184, v188
	v_cvt_pk_fp8_f32 v152, v143, v173
	v_cvt_pk_fp8_f32 v153, v185, v189
	v_cvt_pk_fp8_f32 v158, v144, v174
	v_cvt_pk_fp8_f32 v159, v186, v190
	v_cvt_pk_fp8_f32 v196, v145, v175
	v_cvt_pk_fp8_f32 v197, v187, v191
	v_cvt_pk_fp8_f32 v148, v176, v180 op_sel:[0,0,1]
	v_cvt_pk_fp8_f32 v149, v162, v6 op_sel:[0,0,1]
	v_cvt_pk_fp8_f32 v152, v177, v181 op_sel:[0,0,1]
	v_cvt_pk_fp8_f32 v153, v163, v7 op_sel:[0,0,1]
	v_cvt_pk_fp8_f32 v158, v178, v182 op_sel:[0,0,1]
	v_cvt_pk_fp8_f32 v159, v164, v8 op_sel:[0,0,1]
	v_cvt_pk_fp8_f32 v196, v179, v183 op_sel:[0,0,1]
	v_cvt_pk_fp8_f32 v197, v165, v9 op_sel:[0,0,1]
	s_nop 1
	global_store_dwordx2 v27, v[148:149], s[56:57]
	global_store_dwordx2 v32, v[152:153], s[56:57]
	global_store_dwordx2 v92, v[158:159], s[56:57]
	global_store_dwordx2 v94, v[196:197], s[56:57]
	s_branch .Lcv102_p15_end

.Lcv102_drain1:
	s_waitcnt vmcnt(0)
	s_cmp_gt_u32 s41, 0
	s_cbranch_scc0 .Lcv102_done
	s_lshl_b32 s60, s66, 2
	v_mul_lo_u32 v27, v97, s60
	s_cmp_eq_u32 s75, 0
	s_cbranch_scc1 .Lcv102_p16_bf
	v_lshl_add_u32 v27, v96, 3, v27
	v_add_u32_e32 v32, s66, v27
	v_add_u32_e32 v92, s66, v32
	v_add_u32_e32 v94, s66, v92
	v_mul_f32_e32 v66, s75, v66
	v_mul_f32_e32 v67, s75, v67
	v_mul_f32_e32 v68, s75, v68
	v_mul_f32_e32 v69, s75, v69
	v_mul_f32_e32 v70, s75, v70
	v_mul_f32_e32 v71, s75, v71
	v_mul_f32_e32 v72, s75, v72
	v_mul_f32_e32 v73, s75, v73
	v_mul_f32_e32 v74, s75, v74
	v_mul_f32_e32 v75, s75, v75
	v_mul_f32_e32 v76, s75, v76
	v_mul_f32_e32 v77, s75, v77
	v_mul_f32_e32 v78, s75, v78
	v_mul_f32_e32 v79, s75, v79
	v_mul_f32_e32 v80, s75, v80
	v_mul_f32_e32 v81, s75, v81
	v_mul_f32_e32 v82, s75, v82
	v_mul_f32_e32 v83, s75, v83
	v_mul_f32_e32 v84, s75, v84
	v_mul_f32_e32 v85, s75, v85
	v_mul_f32_e32 v86, s75, v86
	v_mul_f32_e32 v87, s75, v87
	v_mul_f32_e32 v88, s75, v88
	v_mul_f32_e32 v89, s75, v89
	v_mul_f32_e32 v102, s75, v102
	v_mul_f32_e32 v103, s75, v103
	v_mul_f32_e32 v104, s75, v104
	v_mul_f32_e32 v105, s75, v105
	v_mul_f32_e32 v106, s75, v106
	v_mul_f32_e32 v107, s75, v107
	v_mul_f32_e32 v108, s75, v108
	v_mul_f32_e32 v109, s75, v109
	v_med3_f32 v66, v66, s64, v98
	v_med3_f32 v67, v67, s64, v98
	v_med3_f32 v68, v68, s64, v98
	v_med3_f32 v69, v69, s64, v98
	v_med3_f32 v70, v70, s64, v98
	v_med3_f32 v71, v71, s64, v98
	v_med3_f32 v72, v72, s64, v98
	v_med3_f32 v73, v73, s64, v98
	v_med3_f32 v74, v74, s64, v98
	v_med3_f32 v75, v75, s64, v98
	v_med3_f32 v76, v76, s64, v98
	v_med3_f32 v77, v77, s64, v98
	v_med3_f32 v78, v78, s64, v98
	v_med3_f32 v79, v79, s64, v98
	v_med3_f32 v80, v80, s64, v98
	v_med3_f32 v81, v81, s64, v98
	v_med3_f32 v82, v82, s64, v98
	v_med3_f32 v83, v83, s64, v98
	v_med3_f32 v84, v84, s64, v98
	v_med3_f32 v85, v85, s64, v98
	v_med3_f32 v86, v86, s64, v98
	v_med3_f32 v87, v87, s64, v98
	v_med3_f32 v88, v88, s64, v98
	v_med3_f32 v89, v89, s64, v98
	v_med3_f32 v102, v102, s64, v98
	v_med3_f32 v103, v103, s64, v98
	v_med3_f32 v104, v104, s64, v98
	v_med3_f32 v105, v105, s64, v98
	v_med3_f32 v106, v106, s64, v98
	v_med3_f32 v107, v107, s64, v98
	v_med3_f32 v108, v108, s64, v98
	v_med3_f32 v109, v109, s64, v98
	v_cvt_pk_fp8_f32 v148, v66, v70
	v_cvt_pk_fp8_f32 v149, v82, v86
	v_cvt_pk_fp8_f32 v152, v67, v71
	v_cvt_pk_fp8_f32 v153, v83, v87
	v_cvt_pk_fp8_f32 v158, v68, v72
	v_cvt_pk_fp8_f32 v159, v84, v88
	v_cvt_pk_fp8_f32 v196, v69, v73
	v_cvt_pk_fp8_f32 v197, v85, v89
	v_cvt_pk_fp8_f32 v148, v74, v78 op_sel:[0,0,1]
	v_cvt_pk_fp8_f32 v149, v102, v106 op_sel:[0,0,1]
	v_cvt_pk_fp8_f32 v152, v75, v79 op_sel:[0,0,1]
	v_cvt_pk_fp8_f32 v153, v103, v107 op_sel:[0,0,1]
	v_cvt_pk_fp8_f32 v158, v76, v80 op_sel:[0,0,1]
	v_cvt_pk_fp8_f32 v159, v104, v108 op_sel:[0,0,1]
	v_cvt_pk_fp8_f32 v196, v77, v81 op_sel:[0,0,1]
	v_cvt_pk_fp8_f32 v197, v105, v109 op_sel:[0,0,1]
	s_nop 1
	global_store_dwordx2 v27, v[148:149], s[52:53]
	global_store_dwordx2 v32, v[152:153], s[52:53]
	global_store_dwordx2 v92, v[158:159], s[52:53]
	global_store_dwordx2 v94, v[196:197], s[52:53]
	s_branch .Lcv102_p16_end

.Lcv102_p16_end:
	s_cmp_gt_u32 s41, 1
	s_cbranch_scc0 .Lcv102_done
	s_lshl_b32 s60, s67, 2
	v_mul_lo_u32 v27, v97, s60
	s_cmp_eq_u32 s78, 0
	s_cbranch_scc1 .Lcv102_p17_bf
	v_lshl_add_u32 v27, v96, 3, v27
	v_add_u32_e32 v32, s67, v27
	v_add_u32_e32 v92, s67, v32
	v_add_u32_e32 v94, s67, v92
	v_mul_f32_e32 v110, s78, v110
	v_mul_f32_e32 v111, s78, v111
	v_mul_f32_e32 v112, s78, v112
	v_mul_f32_e32 v113, s78, v113
	v_mul_f32_e32 v114, s78, v114
	v_mul_f32_e32 v115, s78, v115
	v_mul_f32_e32 v116, s78, v116
	v_mul_f32_e32 v117, s78, v117
	v_mul_f32_e32 v118, s78, v118
	v_mul_f32_e32 v119, s78, v119
	v_mul_f32_e32 v120, s78, v120
	v_mul_f32_e32 v121, s78, v121
	v_mul_f32_e32 v122, s78, v122
	v_mul_f32_e32 v123, s78, v123
	v_mul_f32_e32 v124, s78, v124
	v_mul_f32_e32 v125, s78, v125
	v_mul_f32_e32 v126, s78, v126
	v_mul_f32_e32 v127, s78, v127
	v_mul_f32_e32 v128, s78, v128
	v_mul_f32_e32 v129, s78, v129
	v_mul_f32_e32 v130, s78, v130
	v_mul_f32_e32 v131, s78, v131
	v_mul_f32_e32 v132, s78, v132
	v_mul_f32_e32 v133, s78, v133
	v_mul_f32_e32 v134, s78, v134
	v_mul_f32_e32 v135, s78, v135
	v_mul_f32_e32 v136, s78, v136
	v_mul_f32_e32 v137, s78, v137
	v_mul_f32_e32 v138, s78, v138
	v_mul_f32_e32 v139, s78, v139
	v_mul_f32_e32 v140, s78, v140
	v_mul_f32_e32 v141, s78, v141
	v_med3_f32 v110, v110, s64, v98
	v_med3_f32 v111, v111, s64, v98
	v_med3_f32 v112, v112, s64, v98
	v_med3_f32 v113, v113, s64, v98
	v_med3_f32 v114, v114, s64, v98
	v_med3_f32 v115, v115, s64, v98
	v_med3_f32 v116, v116, s64, v98
	v_med3_f32 v117, v117, s64, v98
	v_med3_f32 v118, v118, s64, v98
	v_med3_f32 v119, v119, s64, v98
	v_med3_f32 v120, v120, s64, v98
	v_med3_f32 v121, v121, s64, v98
	v_med3_f32 v122, v122, s64, v98
	v_med3_f32 v123, v123, s64, v98
	v_med3_f32 v124, v124, s64, v98
	v_med3_f32 v125, v125, s64, v98
	v_med3_f32 v126, v126, s64, v98
	v_med3_f32 v127, v127, s64, v98
	v_med3_f32 v128, v128, s64, v98
	v_med3_f32 v129, v129, s64, v98
	v_med3_f32 v130, v130, s64, v98
	v_med3_f32 v131, v131, s64, v98
	v_med3_f32 v132, v132, s64, v98
	v_med3_f32 v133, v133, s64, v98
	v_med3_f32 v134, v134, s64, v98
	v_med3_f32 v135, v135, s64, v98
	v_med3_f32 v136, v136, s64, v98
	v_med3_f32 v137, v137, s64, v98
	v_med3_f32 v138, v138, s64, v98
	v_med3_f32 v139, v139, s64, v98
	v_med3_f32 v140, v140, s64, v98
	v_med3_f32 v141, v141, s64, v98
	v_cvt_pk_fp8_f32 v148, v110, v114
	v_cvt_pk_fp8_f32 v149, v126, v130
	v_cvt_pk_fp8_f32 v152, v111, v115
	v_cvt_pk_fp8_f32 v153, v127, v131
	v_cvt_pk_fp8_f32 v158, v112, v116
	v_cvt_pk_fp8_f32 v159, v128, v132
	v_cvt_pk_fp8_f32 v196, v113, v117
	v_cvt_pk_fp8_f32 v197, v129, v133
	v_cvt_pk_fp8_f32 v148, v118, v122 op_sel:[0,0,1]
	v_cvt_pk_fp8_f32 v149, v134, v138 op_sel:[0,0,1]
	v_cvt_pk_fp8_f32 v152, v119, v123 op_sel:[0,0,1]
	v_cvt_pk_fp8_f32 v153, v135, v139 op_sel:[0,0,1]
	v_cvt_pk_fp8_f32 v158, v120, v124 op_sel:[0,0,1]
	v_cvt_pk_fp8_f32 v159, v136, v140 op_sel:[0,0,1]
	v_cvt_pk_fp8_f32 v196, v121, v125 op_sel:[0,0,1]
	v_cvt_pk_fp8_f32 v197, v137, v141 op_sel:[0,0,1]
	s_nop 1
	global_store_dwordx2 v27, v[148:149], s[54:55]
	global_store_dwordx2 v32, v[152:153], s[54:55]
	global_store_dwordx2 v92, v[158:159], s[54:55]
	global_store_dwordx2 v94, v[196:197], s[54:55]
	s_branch .Lcv102_p17_end

.Lcv102_p17_end:
	s_cmp_gt_u32 s41, 2
	s_cbranch_scc0 .Lcv102_done
	s_lshl_b32 s60, s69, 2
	v_mul_lo_u32 v27, v97, s60
	s_cmp_eq_u32 s79, 0
	s_cbranch_scc1 .Lcv102_p18_bf
	v_lshl_add_u32 v27, v96, 3, v27
	v_add_u32_e32 v32, s69, v27
	v_add_u32_e32 v92, s69, v32
	v_add_u32_e32 v94, s69, v92
	v_mul_f32_e32 v142, s79, v142
	v_mul_f32_e32 v143, s79, v143
	v_mul_f32_e32 v144, s79, v144
	v_mul_f32_e32 v145, s79, v145
	v_mul_f32_e32 v172, s79, v172
	v_mul_f32_e32 v173, s79, v173
	v_mul_f32_e32 v174, s79, v174
	v_mul_f32_e32 v175, s79, v175
	v_mul_f32_e32 v176, s79, v176
	v_mul_f32_e32 v177, s79, v177
	v_mul_f32_e32 v178, s79, v178
	v_mul_f32_e32 v179, s79, v179
	v_mul_f32_e32 v180, s79, v180
	v_mul_f32_e32 v181, s79, v181
	v_mul_f32_e32 v182, s79, v182
	v_mul_f32_e32 v183, s79, v183
	v_mul_f32_e32 v184, s79, v184
	v_mul_f32_e32 v185, s79, v185
	v_mul_f32_e32 v186, s79, v186
	v_mul_f32_e32 v187, s79, v187
	v_mul_f32_e32 v188, s79, v188
	v_mul_f32_e32 v189, s79, v189
	v_mul_f32_e32 v190, s79, v190
	v_mul_f32_e32 v191, s79, v191
	v_mul_f32_e32 v162, s79, v162
	v_mul_f32_e32 v163, s79, v163
	v_mul_f32_e32 v164, s79, v164
	v_mul_f32_e32 v165, s79, v165
	v_mul_f32_e32 v6, s79, v6
	v_mul_f32_e32 v7, s79, v7
	v_mul_f32_e32 v8, s79, v8
	v_mul_f32_e32 v9, s79, v9
	v_med3_f32 v142, v142, s64, v98
	v_med3_f32 v143, v143, s64, v98
	v_med3_f32 v144, v144, s64, v98
	v_med3_f32 v145, v145, s64, v98
	v_med3_f32 v172, v172, s64, v98
	v_med3_f32 v173, v173, s64, v98
	v_med3_f32 v174, v174, s64, v98
	v_med3_f32 v175, v175, s64, v98
	v_med3_f32 v176, v176, s64, v98
	v_med3_f32 v177, v177, s64, v98
	v_med3_f32 v178, v178, s64, v98
	v_med3_f32 v179, v179, s64, v98
	v_med3_f32 v180, v180, s64, v98
	v_med3_f32 v181, v181, s64, v98
	v_med3_f32 v182, v182, s64, v98
	v_med3_f32 v183, v183, s64, v98
	v_med3_f32 v184, v184, s64, v98
	v_med3_f32 v185, v185, s64, v98
	v_med3_f32 v186, v186, s64, v98
	v_med3_f32 v187, v187, s64, v98
	v_med3_f32 v188, v188, s64, v98
	v_med3_f32 v189, v189, s64, v98
	v_med3_f32 v190, v190, s64, v98
	v_med3_f32 v191, v191, s64, v98
	v_med3_f32 v162, v162, s64, v98
	v_med3_f32 v163, v163, s64, v98
	v_med3_f32 v164, v164, s64, v98
	v_med3_f32 v165, v165, s64, v98
	v_med3_f32 v6, v6, s64, v98
	v_med3_f32 v7, v7, s64, v98
	v_med3_f32 v8, v8, s64, v98
	v_med3_f32 v9, v9, s64, v98
	v_cvt_pk_fp8_f32 v148, v142, v172
	v_cvt_pk_fp8_f32 v149, v184, v188
	v_cvt_pk_fp8_f32 v152, v143, v173
	v_cvt_pk_fp8_f32 v153, v185, v189
	v_cvt_pk_fp8_f32 v158, v144, v174
	v_cvt_pk_fp8_f32 v159, v186, v190
	v_cvt_pk_fp8_f32 v196, v145, v175
	v_cvt_pk_fp8_f32 v197, v187, v191
	v_cvt_pk_fp8_f32 v148, v176, v180 op_sel:[0,0,1]
	v_cvt_pk_fp8_f32 v149, v162, v6 op_sel:[0,0,1]
	v_cvt_pk_fp8_f32 v152, v177, v181 op_sel:[0,0,1]
	v_cvt_pk_fp8_f32 v153, v163, v7 op_sel:[0,0,1]
	v_cvt_pk_fp8_f32 v158, v178, v182 op_sel:[0,0,1]
	v_cvt_pk_fp8_f32 v159, v164, v8 op_sel:[0,0,1]
	v_cvt_pk_fp8_f32 v196, v179, v183 op_sel:[0,0,1]
	v_cvt_pk_fp8_f32 v197, v165, v9 op_sel:[0,0,1]
	s_nop 1
	global_store_dwordx2 v27, v[148:149], s[56:57]
	global_store_dwordx2 v32, v[152:153], s[56:57]
	global_store_dwordx2 v92, v[158:159], s[56:57]
	global_store_dwordx2 v94, v[196:197], s[56:57]
	s_branch .Lcv102_p18_end

.Lcv102_p18_end:
	s_cmp_gt_u32 s41, 3
	s_cbranch_scc0 .Lcv102_done
	s_lshl_b32 s60, s65, 2
	v_mul_lo_u32 v27, v97, s60
	s_cmp_eq_u32 s71, 0
	s_cbranch_scc1 .Lcv102_p19_bf
	v_lshl_add_u32 v27, v96, 3, v27
	v_add_u32_e32 v32, s65, v27
	v_add_u32_e32 v92, s65, v32
	v_add_u32_e32 v94, s65, v92
	v_mul_f32_e32 v34, s71, v34
	v_mul_f32_e32 v35, s71, v35
	v_mul_f32_e32 v36, s71, v36
	v_mul_f32_e32 v37, s71, v37
	v_mul_f32_e32 v38, s71, v38
	v_mul_f32_e32 v39, s71, v39
	v_mul_f32_e32 v40, s71, v40
	v_mul_f32_e32 v41, s71, v41
	v_mul_f32_e32 v42, s71, v42
	v_mul_f32_e32 v43, s71, v43
	v_mul_f32_e32 v44, s71, v44
	v_mul_f32_e32 v45, s71, v45
	v_mul_f32_e32 v46, s71, v46
	v_mul_f32_e32 v47, s71, v47
	v_mul_f32_e32 v48, s71, v48
	v_mul_f32_e32 v49, s71, v49
	v_mul_f32_e32 v50, s71, v50
	v_mul_f32_e32 v51, s71, v51
	v_mul_f32_e32 v52, s71, v52
	v_mul_f32_e32 v53, s71, v53
	v_mul_f32_e32 v54, s71, v54
	v_mul_f32_e32 v55, s71, v55
	v_mul_f32_e32 v56, s71, v56
	v_mul_f32_e32 v57, s71, v57
	v_mul_f32_e32 v58, s71, v58
	v_mul_f32_e32 v59, s71, v59
	v_mul_f32_e32 v60, s71, v60
	v_mul_f32_e32 v61, s71, v61
	v_mul_f32_e32 v62, s71, v62
	v_mul_f32_e32 v63, s71, v63
	v_mul_f32_e32 v64, s71, v64
	v_mul_f32_e32 v65, s71, v65
	v_med3_f32 v34, v34, s64, v98
	v_med3_f32 v35, v35, s64, v98
	v_med3_f32 v36, v36, s64, v98
	v_med3_f32 v37, v37, s64, v98
	v_med3_f32 v38, v38, s64, v98
	v_med3_f32 v39, v39, s64, v98
	v_med3_f32 v40, v40, s64, v98
	v_med3_f32 v41, v41, s64, v98
	v_med3_f32 v42, v42, s64, v98
	v_med3_f32 v43, v43, s64, v98
	v_med3_f32 v44, v44, s64, v98
	v_med3_f32 v45, v45, s64, v98
	v_med3_f32 v46, v46, s64, v98
	v_med3_f32 v47, v47, s64, v98
	v_med3_f32 v48, v48, s64, v98
	v_med3_f32 v49, v49, s64, v98
	v_med3_f32 v50, v50, s64, v98
	v_med3_f32 v51, v51, s64, v98
	v_med3_f32 v52, v52, s64, v98
	v_med3_f32 v53, v53, s64, v98
	v_med3_f32 v54, v54, s64, v98
	v_med3_f32 v55, v55, s64, v98
	v_med3_f32 v56, v56, s64, v98
	v_med3_f32 v57, v57, s64, v98
	v_med3_f32 v58, v58, s64, v98
	v_med3_f32 v59, v59, s64, v98
	v_med3_f32 v60, v60, s64, v98
	v_med3_f32 v61, v61, s64, v98
	v_med3_f32 v62, v62, s64, v98
	v_med3_f32 v63, v63, s64, v98
	v_med3_f32 v64, v64, s64, v98
	v_med3_f32 v65, v65, s64, v98
	v_cvt_pk_fp8_f32 v148, v34, v38
	v_cvt_pk_fp8_f32 v149, v50, v54
	v_cvt_pk_fp8_f32 v152, v35, v39
	v_cvt_pk_fp8_f32 v153, v51, v55
	v_cvt_pk_fp8_f32 v158, v36, v40
	v_cvt_pk_fp8_f32 v159, v52, v56
	v_cvt_pk_fp8_f32 v196, v37, v41
	v_cvt_pk_fp8_f32 v197, v53, v57
	v_cvt_pk_fp8_f32 v148, v42, v46 op_sel:[0,0,1]
	v_cvt_pk_fp8_f32 v149, v58, v62 op_sel:[0,0,1]
	v_cvt_pk_fp8_f32 v152, v43, v47 op_sel:[0,0,1]
	v_cvt_pk_fp8_f32 v153, v59, v63 op_sel:[0,0,1]
	v_cvt_pk_fp8_f32 v158, v44, v48 op_sel:[0,0,1]
	v_cvt_pk_fp8_f32 v159, v60, v64 op_sel:[0,0,1]
	v_cvt_pk_fp8_f32 v196, v45, v49 op_sel:[0,0,1]
	v_cvt_pk_fp8_f32 v197, v61, v65 op_sel:[0,0,1]
	s_nop 1
	global_store_dwordx2 v27, v[148:149], s[50:51]
	global_store_dwordx2 v32, v[152:153], s[50:51]
	global_store_dwordx2 v92, v[158:159], s[50:51]
	global_store_dwordx2 v94, v[196:197], s[50:51]
	s_branch .Lcv102_p19_end

.Lcv102_drain2:
	s_waitcnt vmcnt(0)
	s_cmp_gt_u32 s41, 0
	s_cbranch_scc0 .Lcv102_done
	s_lshl_b32 s60, s67, 2
	v_mul_lo_u32 v27, v97, s60
	s_cmp_eq_u32 s78, 0
	s_cbranch_scc1 .Lcv102_p20_bf
	v_lshl_add_u32 v27, v96, 3, v27
	v_add_u32_e32 v32, s67, v27
	v_add_u32_e32 v92, s67, v32
	v_add_u32_e32 v94, s67, v92
	v_mul_f32_e32 v110, s78, v110
	v_mul_f32_e32 v111, s78, v111
	v_mul_f32_e32 v112, s78, v112
	v_mul_f32_e32 v113, s78, v113
	v_mul_f32_e32 v114, s78, v114
	v_mul_f32_e32 v115, s78, v115
	v_mul_f32_e32 v116, s78, v116
	v_mul_f32_e32 v117, s78, v117
	v_mul_f32_e32 v118, s78, v118
	v_mul_f32_e32 v119, s78, v119
	v_mul_f32_e32 v120, s78, v120
	v_mul_f32_e32 v121, s78, v121
	v_mul_f32_e32 v122, s78, v122
	v_mul_f32_e32 v123, s78, v123
	v_mul_f32_e32 v124, s78, v124
	v_mul_f32_e32 v125, s78, v125
	v_mul_f32_e32 v126, s78, v126
	v_mul_f32_e32 v127, s78, v127
	v_mul_f32_e32 v128, s78, v128
	v_mul_f32_e32 v129, s78, v129
	v_mul_f32_e32 v130, s78, v130
	v_mul_f32_e32 v131, s78, v131
	v_mul_f32_e32 v132, s78, v132
	v_mul_f32_e32 v133, s78, v133
	v_mul_f32_e32 v134, s78, v134
	v_mul_f32_e32 v135, s78, v135
	v_mul_f32_e32 v136, s78, v136
	v_mul_f32_e32 v137, s78, v137
	v_mul_f32_e32 v138, s78, v138
	v_mul_f32_e32 v139, s78, v139
	v_mul_f32_e32 v140, s78, v140
	v_mul_f32_e32 v141, s78, v141
	v_med3_f32 v110, v110, s64, v98
	v_med3_f32 v111, v111, s64, v98
	v_med3_f32 v112, v112, s64, v98
	v_med3_f32 v113, v113, s64, v98
	v_med3_f32 v114, v114, s64, v98
	v_med3_f32 v115, v115, s64, v98
	v_med3_f32 v116, v116, s64, v98
	v_med3_f32 v117, v117, s64, v98
	v_med3_f32 v118, v118, s64, v98
	v_med3_f32 v119, v119, s64, v98
	v_med3_f32 v120, v120, s64, v98
	v_med3_f32 v121, v121, s64, v98
	v_med3_f32 v122, v122, s64, v98
	v_med3_f32 v123, v123, s64, v98
	v_med3_f32 v124, v124, s64, v98
	v_med3_f32 v125, v125, s64, v98
	v_med3_f32 v126, v126, s64, v98
	v_med3_f32 v127, v127, s64, v98
	v_med3_f32 v128, v128, s64, v98
	v_med3_f32 v129, v129, s64, v98
	v_med3_f32 v130, v130, s64, v98
	v_med3_f32 v131, v131, s64, v98
	v_med3_f32 v132, v132, s64, v98
	v_med3_f32 v133, v133, s64, v98
	v_med3_f32 v134, v134, s64, v98
	v_med3_f32 v135, v135, s64, v98
	v_med3_f32 v136, v136, s64, v98
	v_med3_f32 v137, v137, s64, v98
	v_med3_f32 v138, v138, s64, v98
	v_med3_f32 v139, v139, s64, v98
	v_med3_f32 v140, v140, s64, v98
	v_med3_f32 v141, v141, s64, v98
	v_cvt_pk_fp8_f32 v148, v110, v114
	v_cvt_pk_fp8_f32 v149, v126, v130
	v_cvt_pk_fp8_f32 v152, v111, v115
	v_cvt_pk_fp8_f32 v153, v127, v131
	v_cvt_pk_fp8_f32 v158, v112, v116
	v_cvt_pk_fp8_f32 v159, v128, v132
	v_cvt_pk_fp8_f32 v196, v113, v117
	v_cvt_pk_fp8_f32 v197, v129, v133
	v_cvt_pk_fp8_f32 v148, v118, v122 op_sel:[0,0,1]
	v_cvt_pk_fp8_f32 v149, v134, v138 op_sel:[0,0,1]
	v_cvt_pk_fp8_f32 v152, v119, v123 op_sel:[0,0,1]
	v_cvt_pk_fp8_f32 v153, v135, v139 op_sel:[0,0,1]
	v_cvt_pk_fp8_f32 v158, v120, v124 op_sel:[0,0,1]
	v_cvt_pk_fp8_f32 v159, v136, v140 op_sel:[0,0,1]
	v_cvt_pk_fp8_f32 v196, v121, v125 op_sel:[0,0,1]
	v_cvt_pk_fp8_f32 v197, v137, v141 op_sel:[0,0,1]
	s_nop 1
	global_store_dwordx2 v27, v[148:149], s[54:55]
	global_store_dwordx2 v32, v[152:153], s[54:55]
	global_store_dwordx2 v92, v[158:159], s[54:55]
	global_store_dwordx2 v94, v[196:197], s[54:55]
	s_branch .Lcv102_p20_end

.Lcv102_p20_end:
	s_cmp_gt_u32 s41, 1
	s_cbranch_scc0 .Lcv102_done
	s_lshl_b32 s60, s69, 2
	v_mul_lo_u32 v27, v97, s60
	s_cmp_eq_u32 s79, 0
	s_cbranch_scc1 .Lcv102_p21_bf
	v_lshl_add_u32 v27, v96, 3, v27
	v_add_u32_e32 v32, s69, v27
	v_add_u32_e32 v92, s69, v32
	v_add_u32_e32 v94, s69, v92
	v_mul_f32_e32 v142, s79, v142
	v_mul_f32_e32 v143, s79, v143
	v_mul_f32_e32 v144, s79, v144
	v_mul_f32_e32 v145, s79, v145
	v_mul_f32_e32 v172, s79, v172
	v_mul_f32_e32 v173, s79, v173
	v_mul_f32_e32 v174, s79, v174
	v_mul_f32_e32 v175, s79, v175
	v_mul_f32_e32 v176, s79, v176
	v_mul_f32_e32 v177, s79, v177
	v_mul_f32_e32 v178, s79, v178
	v_mul_f32_e32 v179, s79, v179
	v_mul_f32_e32 v180, s79, v180
	v_mul_f32_e32 v181, s79, v181
	v_mul_f32_e32 v182, s79, v182
	v_mul_f32_e32 v183, s79, v183
	v_mul_f32_e32 v184, s79, v184
	v_mul_f32_e32 v185, s79, v185
	v_mul_f32_e32 v186, s79, v186
	v_mul_f32_e32 v187, s79, v187
	v_mul_f32_e32 v188, s79, v188
	v_mul_f32_e32 v189, s79, v189
	v_mul_f32_e32 v190, s79, v190
	v_mul_f32_e32 v191, s79, v191
	v_mul_f32_e32 v162, s79, v162
	v_mul_f32_e32 v163, s79, v163
	v_mul_f32_e32 v164, s79, v164
	v_mul_f32_e32 v165, s79, v165
	v_mul_f32_e32 v6, s79, v6
	v_mul_f32_e32 v7, s79, v7
	v_mul_f32_e32 v8, s79, v8
	v_mul_f32_e32 v9, s79, v9
	v_med3_f32 v142, v142, s64, v98
	v_med3_f32 v143, v143, s64, v98
	v_med3_f32 v144, v144, s64, v98
	v_med3_f32 v145, v145, s64, v98
	v_med3_f32 v172, v172, s64, v98
	v_med3_f32 v173, v173, s64, v98
	v_med3_f32 v174, v174, s64, v98
	v_med3_f32 v175, v175, s64, v98
	v_med3_f32 v176, v176, s64, v98
	v_med3_f32 v177, v177, s64, v98
	v_med3_f32 v178, v178, s64, v98
	v_med3_f32 v179, v179, s64, v98
	v_med3_f32 v180, v180, s64, v98
	v_med3_f32 v181, v181, s64, v98
	v_med3_f32 v182, v182, s64, v98
	v_med3_f32 v183, v183, s64, v98
	v_med3_f32 v184, v184, s64, v98
	v_med3_f32 v185, v185, s64, v98
	v_med3_f32 v186, v186, s64, v98
	v_med3_f32 v187, v187, s64, v98
	v_med3_f32 v188, v188, s64, v98
	v_med3_f32 v189, v189, s64, v98
	v_med3_f32 v190, v190, s64, v98
	v_med3_f32 v191, v191, s64, v98
	v_med3_f32 v162, v162, s64, v98
	v_med3_f32 v163, v163, s64, v98
	v_med3_f32 v164, v164, s64, v98
	v_med3_f32 v165, v165, s64, v98
	v_med3_f32 v6, v6, s64, v98
	v_med3_f32 v7, v7, s64, v98
	v_med3_f32 v8, v8, s64, v98
	v_med3_f32 v9, v9, s64, v98
	v_cvt_pk_fp8_f32 v148, v142, v172
	v_cvt_pk_fp8_f32 v149, v184, v188
	v_cvt_pk_fp8_f32 v152, v143, v173
	v_cvt_pk_fp8_f32 v153, v185, v189
	v_cvt_pk_fp8_f32 v158, v144, v174
	v_cvt_pk_fp8_f32 v159, v186, v190
	v_cvt_pk_fp8_f32 v196, v145, v175
	v_cvt_pk_fp8_f32 v197, v187, v191
	v_cvt_pk_fp8_f32 v148, v176, v180 op_sel:[0,0,1]
	v_cvt_pk_fp8_f32 v149, v162, v6 op_sel:[0,0,1]
	v_cvt_pk_fp8_f32 v152, v177, v181 op_sel:[0,0,1]
	v_cvt_pk_fp8_f32 v153, v163, v7 op_sel:[0,0,1]
	v_cvt_pk_fp8_f32 v158, v178, v182 op_sel:[0,0,1]
	v_cvt_pk_fp8_f32 v159, v164, v8 op_sel:[0,0,1]
	v_cvt_pk_fp8_f32 v196, v179, v183 op_sel:[0,0,1]
	v_cvt_pk_fp8_f32 v197, v165, v9 op_sel:[0,0,1]
	s_nop 1
	global_store_dwordx2 v27, v[148:149], s[56:57]
	global_store_dwordx2 v32, v[152:153], s[56:57]
	global_store_dwordx2 v92, v[158:159], s[56:57]
	global_store_dwordx2 v94, v[196:197], s[56:57]
	s_branch .Lcv102_p21_end

.Lcv102_p21_end:
	s_cmp_gt_u32 s41, 2
	s_cbranch_scc0 .Lcv102_done
	s_lshl_b32 s60, s65, 2
	v_mul_lo_u32 v27, v97, s60
	s_cmp_eq_u32 s71, 0
	s_cbranch_scc1 .Lcv102_p22_bf
	v_lshl_add_u32 v27, v96, 3, v27
	v_add_u32_e32 v32, s65, v27
	v_add_u32_e32 v92, s65, v32
	v_add_u32_e32 v94, s65, v92
	v_mul_f32_e32 v34, s71, v34
	v_mul_f32_e32 v35, s71, v35
	v_mul_f32_e32 v36, s71, v36
	v_mul_f32_e32 v37, s71, v37
	v_mul_f32_e32 v38, s71, v38
	v_mul_f32_e32 v39, s71, v39
	v_mul_f32_e32 v40, s71, v40
	v_mul_f32_e32 v41, s71, v41
	v_mul_f32_e32 v42, s71, v42
	v_mul_f32_e32 v43, s71, v43
	v_mul_f32_e32 v44, s71, v44
	v_mul_f32_e32 v45, s71, v45
	v_mul_f32_e32 v46, s71, v46
	v_mul_f32_e32 v47, s71, v47
	v_mul_f32_e32 v48, s71, v48
	v_mul_f32_e32 v49, s71, v49
	v_mul_f32_e32 v50, s71, v50
	v_mul_f32_e32 v51, s71, v51
	v_mul_f32_e32 v52, s71, v52
	v_mul_f32_e32 v53, s71, v53
	v_mul_f32_e32 v54, s71, v54
	v_mul_f32_e32 v55, s71, v55
	v_mul_f32_e32 v56, s71, v56
	v_mul_f32_e32 v57, s71, v57
	v_mul_f32_e32 v58, s71, v58
	v_mul_f32_e32 v59, s71, v59
	v_mul_f32_e32 v60, s71, v60
	v_mul_f32_e32 v61, s71, v61
	v_mul_f32_e32 v62, s71, v62
	v_mul_f32_e32 v63, s71, v63
	v_mul_f32_e32 v64, s71, v64
	v_mul_f32_e32 v65, s71, v65
	v_med3_f32 v34, v34, s64, v98
	v_med3_f32 v35, v35, s64, v98
	v_med3_f32 v36, v36, s64, v98
	v_med3_f32 v37, v37, s64, v98
	v_med3_f32 v38, v38, s64, v98
	v_med3_f32 v39, v39, s64, v98
	v_med3_f32 v40, v40, s64, v98
	v_med3_f32 v41, v41, s64, v98
	v_med3_f32 v42, v42, s64, v98
	v_med3_f32 v43, v43, s64, v98
	v_med3_f32 v44, v44, s64, v98
	v_med3_f32 v45, v45, s64, v98
	v_med3_f32 v46, v46, s64, v98
	v_med3_f32 v47, v47, s64, v98
	v_med3_f32 v48, v48, s64, v98
	v_med3_f32 v49, v49, s64, v98
	v_med3_f32 v50, v50, s64, v98
	v_med3_f32 v51, v51, s64, v98
	v_med3_f32 v52, v52, s64, v98
	v_med3_f32 v53, v53, s64, v98
	v_med3_f32 v54, v54, s64, v98
	v_med3_f32 v55, v55, s64, v98
	v_med3_f32 v56, v56, s64, v98
	v_med3_f32 v57, v57, s64, v98
	v_med3_f32 v58, v58, s64, v98
	v_med3_f32 v59, v59, s64, v98
	v_med3_f32 v60, v60, s64, v98
	v_med3_f32 v61, v61, s64, v98
	v_med3_f32 v62, v62, s64, v98
	v_med3_f32 v63, v63, s64, v98
	v_med3_f32 v64, v64, s64, v98
	v_med3_f32 v65, v65, s64, v98
	v_cvt_pk_fp8_f32 v148, v34, v38
	v_cvt_pk_fp8_f32 v149, v50, v54
	v_cvt_pk_fp8_f32 v152, v35, v39
	v_cvt_pk_fp8_f32 v153, v51, v55
	v_cvt_pk_fp8_f32 v158, v36, v40
	v_cvt_pk_fp8_f32 v159, v52, v56
	v_cvt_pk_fp8_f32 v196, v37, v41
	v_cvt_pk_fp8_f32 v197, v53, v57
	v_cvt_pk_fp8_f32 v148, v42, v46 op_sel:[0,0,1]
	v_cvt_pk_fp8_f32 v149, v58, v62 op_sel:[0,0,1]
	v_cvt_pk_fp8_f32 v152, v43, v47 op_sel:[0,0,1]
	v_cvt_pk_fp8_f32 v153, v59, v63 op_sel:[0,0,1]
	v_cvt_pk_fp8_f32 v158, v44, v48 op_sel:[0,0,1]
	v_cvt_pk_fp8_f32 v159, v60, v64 op_sel:[0,0,1]
	v_cvt_pk_fp8_f32 v196, v45, v49 op_sel:[0,0,1]
	v_cvt_pk_fp8_f32 v197, v61, v65 op_sel:[0,0,1]
	s_nop 1
	global_store_dwordx2 v27, v[148:149], s[50:51]
	global_store_dwordx2 v32, v[152:153], s[50:51]
	global_store_dwordx2 v92, v[158:159], s[50:51]
	global_store_dwordx2 v94, v[196:197], s[50:51]
	s_branch .Lcv102_p22_end

.Lcv102_p22_end:
	s_cmp_gt_u32 s41, 3
	s_cbranch_scc0 .Lcv102_done
	s_lshl_b32 s60, s66, 2
	v_mul_lo_u32 v27, v97, s60
	s_cmp_eq_u32 s75, 0
	s_cbranch_scc1 .Lcv102_p23_bf
	v_lshl_add_u32 v27, v96, 3, v27
	v_add_u32_e32 v32, s66, v27
	v_add_u32_e32 v92, s66, v32
	v_add_u32_e32 v94, s66, v92
	v_mul_f32_e32 v66, s75, v66
	v_mul_f32_e32 v67, s75, v67
	v_mul_f32_e32 v68, s75, v68
	v_mul_f32_e32 v69, s75, v69
	v_mul_f32_e32 v70, s75, v70
	v_mul_f32_e32 v71, s75, v71
	v_mul_f32_e32 v72, s75, v72
	v_mul_f32_e32 v73, s75, v73
	v_mul_f32_e32 v74, s75, v74
	v_mul_f32_e32 v75, s75, v75
	v_mul_f32_e32 v76, s75, v76
	v_mul_f32_e32 v77, s75, v77
	v_mul_f32_e32 v78, s75, v78
	v_mul_f32_e32 v79, s75, v79
	v_mul_f32_e32 v80, s75, v80
	v_mul_f32_e32 v81, s75, v81
	v_mul_f32_e32 v82, s75, v82
	v_mul_f32_e32 v83, s75, v83
	v_mul_f32_e32 v84, s75, v84
	v_mul_f32_e32 v85, s75, v85
	v_mul_f32_e32 v86, s75, v86
	v_mul_f32_e32 v87, s75, v87
	v_mul_f32_e32 v88, s75, v88
	v_mul_f32_e32 v89, s75, v89
	v_mul_f32_e32 v102, s75, v102
	v_mul_f32_e32 v103, s75, v103
	v_mul_f32_e32 v104, s75, v104
	v_mul_f32_e32 v105, s75, v105
	v_mul_f32_e32 v106, s75, v106
	v_mul_f32_e32 v107, s75, v107
	v_mul_f32_e32 v108, s75, v108
	v_mul_f32_e32 v109, s75, v109
	v_med3_f32 v66, v66, s64, v98
	v_med3_f32 v67, v67, s64, v98
	v_med3_f32 v68, v68, s64, v98
	v_med3_f32 v69, v69, s64, v98
	v_med3_f32 v70, v70, s64, v98
	v_med3_f32 v71, v71, s64, v98
	v_med3_f32 v72, v72, s64, v98
	v_med3_f32 v73, v73, s64, v98
	v_med3_f32 v74, v74, s64, v98
	v_med3_f32 v75, v75, s64, v98
	v_med3_f32 v76, v76, s64, v98
	v_med3_f32 v77, v77, s64, v98
	v_med3_f32 v78, v78, s64, v98
	v_med3_f32 v79, v79, s64, v98
	v_med3_f32 v80, v80, s64, v98
	v_med3_f32 v81, v81, s64, v98
	v_med3_f32 v82, v82, s64, v98
	v_med3_f32 v83, v83, s64, v98
	v_med3_f32 v84, v84, s64, v98
	v_med3_f32 v85, v85, s64, v98
	v_med3_f32 v86, v86, s64, v98
	v_med3_f32 v87, v87, s64, v98
	v_med3_f32 v88, v88, s64, v98
	v_med3_f32 v89, v89, s64, v98
	v_med3_f32 v102, v102, s64, v98
	v_med3_f32 v103, v103, s64, v98
	v_med3_f32 v104, v104, s64, v98
	v_med3_f32 v105, v105, s64, v98
	v_med3_f32 v106, v106, s64, v98
	v_med3_f32 v107, v107, s64, v98
	v_med3_f32 v108, v108, s64, v98
	v_med3_f32 v109, v109, s64, v98
	v_cvt_pk_fp8_f32 v148, v66, v70
	v_cvt_pk_fp8_f32 v149, v82, v86
	v_cvt_pk_fp8_f32 v152, v67, v71
	v_cvt_pk_fp8_f32 v153, v83, v87
	v_cvt_pk_fp8_f32 v158, v68, v72
	v_cvt_pk_fp8_f32 v159, v84, v88
	v_cvt_pk_fp8_f32 v196, v69, v73
	v_cvt_pk_fp8_f32 v197, v85, v89
	v_cvt_pk_fp8_f32 v148, v74, v78 op_sel:[0,0,1]
	v_cvt_pk_fp8_f32 v149, v102, v106 op_sel:[0,0,1]
	v_cvt_pk_fp8_f32 v152, v75, v79 op_sel:[0,0,1]
	v_cvt_pk_fp8_f32 v153, v103, v107 op_sel:[0,0,1]
	v_cvt_pk_fp8_f32 v158, v76, v80 op_sel:[0,0,1]
	v_cvt_pk_fp8_f32 v159, v104, v108 op_sel:[0,0,1]
	v_cvt_pk_fp8_f32 v196, v77, v81 op_sel:[0,0,1]
	v_cvt_pk_fp8_f32 v197, v105, v109 op_sel:[0,0,1]
	s_nop 1
	global_store_dwordx2 v27, v[148:149], s[52:53]
	global_store_dwordx2 v32, v[152:153], s[52:53]
	global_store_dwordx2 v92, v[158:159], s[52:53]
	global_store_dwordx2 v94, v[196:197], s[52:53]
	s_branch .Lcv102_p23_end

.Lcv102_drain3:
	s_waitcnt vmcnt(0)
	s_cmp_gt_u32 s41, 0
	s_cbranch_scc0 .Lcv102_done
	s_lshl_b32 s60, s69, 2
	v_mul_lo_u32 v27, v97, s60
	s_cmp_eq_u32 s79, 0
	s_cbranch_scc1 .Lcv102_p24_bf
	v_lshl_add_u32 v27, v96, 3, v27
	v_add_u32_e32 v32, s69, v27
	v_add_u32_e32 v92, s69, v32
	v_add_u32_e32 v94, s69, v92
	v_mul_f32_e32 v142, s79, v142
	v_mul_f32_e32 v143, s79, v143
	v_mul_f32_e32 v144, s79, v144
	v_mul_f32_e32 v145, s79, v145
	v_mul_f32_e32 v172, s79, v172
	v_mul_f32_e32 v173, s79, v173
	v_mul_f32_e32 v174, s79, v174
	v_mul_f32_e32 v175, s79, v175
	v_mul_f32_e32 v176, s79, v176
	v_mul_f32_e32 v177, s79, v177
	v_mul_f32_e32 v178, s79, v178
	v_mul_f32_e32 v179, s79, v179
	v_mul_f32_e32 v180, s79, v180
	v_mul_f32_e32 v181, s79, v181
	v_mul_f32_e32 v182, s79, v182
	v_mul_f32_e32 v183, s79, v183
	v_mul_f32_e32 v184, s79, v184
	v_mul_f32_e32 v185, s79, v185
	v_mul_f32_e32 v186, s79, v186
	v_mul_f32_e32 v187, s79, v187
	v_mul_f32_e32 v188, s79, v188
	v_mul_f32_e32 v189, s79, v189
	v_mul_f32_e32 v190, s79, v190
	v_mul_f32_e32 v191, s79, v191
	v_mul_f32_e32 v162, s79, v162
	v_mul_f32_e32 v163, s79, v163
	v_mul_f32_e32 v164, s79, v164
	v_mul_f32_e32 v165, s79, v165
	v_mul_f32_e32 v6, s79, v6
	v_mul_f32_e32 v7, s79, v7
	v_mul_f32_e32 v8, s79, v8
	v_mul_f32_e32 v9, s79, v9
	v_med3_f32 v142, v142, s64, v98
	v_med3_f32 v143, v143, s64, v98
	v_med3_f32 v144, v144, s64, v98
	v_med3_f32 v145, v145, s64, v98
	v_med3_f32 v172, v172, s64, v98
	v_med3_f32 v173, v173, s64, v98
	v_med3_f32 v174, v174, s64, v98
	v_med3_f32 v175, v175, s64, v98
	v_med3_f32 v176, v176, s64, v98
	v_med3_f32 v177, v177, s64, v98
	v_med3_f32 v178, v178, s64, v98
	v_med3_f32 v179, v179, s64, v98
	v_med3_f32 v180, v180, s64, v98
	v_med3_f32 v181, v181, s64, v98
	v_med3_f32 v182, v182, s64, v98
	v_med3_f32 v183, v183, s64, v98
	v_med3_f32 v184, v184, s64, v98
	v_med3_f32 v185, v185, s64, v98
	v_med3_f32 v186, v186, s64, v98
	v_med3_f32 v187, v187, s64, v98
	v_med3_f32 v188, v188, s64, v98
	v_med3_f32 v189, v189, s64, v98
	v_med3_f32 v190, v190, s64, v98
	v_med3_f32 v191, v191, s64, v98
	v_med3_f32 v162, v162, s64, v98
	v_med3_f32 v163, v163, s64, v98
	v_med3_f32 v164, v164, s64, v98
	v_med3_f32 v165, v165, s64, v98
	v_med3_f32 v6, v6, s64, v98
	v_med3_f32 v7, v7, s64, v98
	v_med3_f32 v8, v8, s64, v98
	v_med3_f32 v9, v9, s64, v98
	v_cvt_pk_fp8_f32 v148, v142, v172
	v_cvt_pk_fp8_f32 v149, v184, v188
	v_cvt_pk_fp8_f32 v152, v143, v173
	v_cvt_pk_fp8_f32 v153, v185, v189
	v_cvt_pk_fp8_f32 v158, v144, v174
	v_cvt_pk_fp8_f32 v159, v186, v190
	v_cvt_pk_fp8_f32 v196, v145, v175
	v_cvt_pk_fp8_f32 v197, v187, v191
	v_cvt_pk_fp8_f32 v148, v176, v180 op_sel:[0,0,1]
	v_cvt_pk_fp8_f32 v149, v162, v6 op_sel:[0,0,1]
	v_cvt_pk_fp8_f32 v152, v177, v181 op_sel:[0,0,1]
	v_cvt_pk_fp8_f32 v153, v163, v7 op_sel:[0,0,1]
	v_cvt_pk_fp8_f32 v158, v178, v182 op_sel:[0,0,1]
	v_cvt_pk_fp8_f32 v159, v164, v8 op_sel:[0,0,1]
	v_cvt_pk_fp8_f32 v196, v179, v183 op_sel:[0,0,1]
	v_cvt_pk_fp8_f32 v197, v165, v9 op_sel:[0,0,1]
	s_nop 1
	global_store_dwordx2 v27, v[148:149], s[56:57]
	global_store_dwordx2 v32, v[152:153], s[56:57]
	global_store_dwordx2 v92, v[158:159], s[56:57]
	global_store_dwordx2 v94, v[196:197], s[56:57]
	s_branch .Lcv102_p24_end

.Lcv102_p24_end:
	s_cmp_gt_u32 s41, 1
	s_cbranch_scc0 .Lcv102_done
	s_lshl_b32 s60, s65, 2
	v_mul_lo_u32 v27, v97, s60
	s_cmp_eq_u32 s71, 0
	s_cbranch_scc1 .Lcv102_p25_bf
	v_lshl_add_u32 v27, v96, 3, v27
	v_add_u32_e32 v32, s65, v27
	v_add_u32_e32 v92, s65, v32
	v_add_u32_e32 v94, s65, v92
	v_mul_f32_e32 v34, s71, v34
	v_mul_f32_e32 v35, s71, v35
	v_mul_f32_e32 v36, s71, v36
	v_mul_f32_e32 v37, s71, v37
	v_mul_f32_e32 v38, s71, v38
	v_mul_f32_e32 v39, s71, v39
	v_mul_f32_e32 v40, s71, v40
	v_mul_f32_e32 v41, s71, v41
	v_mul_f32_e32 v42, s71, v42
	v_mul_f32_e32 v43, s71, v43
	v_mul_f32_e32 v44, s71, v44
	v_mul_f32_e32 v45, s71, v45
	v_mul_f32_e32 v46, s71, v46
	v_mul_f32_e32 v47, s71, v47
	v_mul_f32_e32 v48, s71, v48
	v_mul_f32_e32 v49, s71, v49
	v_mul_f32_e32 v50, s71, v50
	v_mul_f32_e32 v51, s71, v51
	v_mul_f32_e32 v52, s71, v52
	v_mul_f32_e32 v53, s71, v53
	v_mul_f32_e32 v54, s71, v54
	v_mul_f32_e32 v55, s71, v55
	v_mul_f32_e32 v56, s71, v56
	v_mul_f32_e32 v57, s71, v57
	v_mul_f32_e32 v58, s71, v58
	v_mul_f32_e32 v59, s71, v59
	v_mul_f32_e32 v60, s71, v60
	v_mul_f32_e32 v61, s71, v61
	v_mul_f32_e32 v62, s71, v62
	v_mul_f32_e32 v63, s71, v63
	v_mul_f32_e32 v64, s71, v64
	v_mul_f32_e32 v65, s71, v65
	v_med3_f32 v34, v34, s64, v98
	v_med3_f32 v35, v35, s64, v98
	v_med3_f32 v36, v36, s64, v98
	v_med3_f32 v37, v37, s64, v98
	v_med3_f32 v38, v38, s64, v98
	v_med3_f32 v39, v39, s64, v98
	v_med3_f32 v40, v40, s64, v98
	v_med3_f32 v41, v41, s64, v98
	v_med3_f32 v42, v42, s64, v98
	v_med3_f32 v43, v43, s64, v98
	v_med3_f32 v44, v44, s64, v98
	v_med3_f32 v45, v45, s64, v98
	v_med3_f32 v46, v46, s64, v98
	v_med3_f32 v47, v47, s64, v98
	v_med3_f32 v48, v48, s64, v98
	v_med3_f32 v49, v49, s64, v98
	v_med3_f32 v50, v50, s64, v98
	v_med3_f32 v51, v51, s64, v98
	v_med3_f32 v52, v52, s64, v98
	v_med3_f32 v53, v53, s64, v98
	v_med3_f32 v54, v54, s64, v98
	v_med3_f32 v55, v55, s64, v98
	v_med3_f32 v56, v56, s64, v98
	v_med3_f32 v57, v57, s64, v98
	v_med3_f32 v58, v58, s64, v98
	v_med3_f32 v59, v59, s64, v98
	v_med3_f32 v60, v60, s64, v98
	v_med3_f32 v61, v61, s64, v98
	v_med3_f32 v62, v62, s64, v98
	v_med3_f32 v63, v63, s64, v98
	v_med3_f32 v64, v64, s64, v98
	v_med3_f32 v65, v65, s64, v98
	v_cvt_pk_fp8_f32 v148, v34, v38
	v_cvt_pk_fp8_f32 v149, v50, v54
	v_cvt_pk_fp8_f32 v152, v35, v39
	v_cvt_pk_fp8_f32 v153, v51, v55
	v_cvt_pk_fp8_f32 v158, v36, v40
	v_cvt_pk_fp8_f32 v159, v52, v56
	v_cvt_pk_fp8_f32 v196, v37, v41
	v_cvt_pk_fp8_f32 v197, v53, v57
	v_cvt_pk_fp8_f32 v148, v42, v46 op_sel:[0,0,1]
	v_cvt_pk_fp8_f32 v149, v58, v62 op_sel:[0,0,1]
	v_cvt_pk_fp8_f32 v152, v43, v47 op_sel:[0,0,1]
	v_cvt_pk_fp8_f32 v153, v59, v63 op_sel:[0,0,1]
	v_cvt_pk_fp8_f32 v158, v44, v48 op_sel:[0,0,1]
	v_cvt_pk_fp8_f32 v159, v60, v64 op_sel:[0,0,1]
	v_cvt_pk_fp8_f32 v196, v45, v49 op_sel:[0,0,1]
	v_cvt_pk_fp8_f32 v197, v61, v65 op_sel:[0,0,1]
	s_nop 1
	global_store_dwordx2 v27, v[148:149], s[50:51]
	global_store_dwordx2 v32, v[152:153], s[50:51]
	global_store_dwordx2 v92, v[158:159], s[50:51]
	global_store_dwordx2 v94, v[196:197], s[50:51]
	s_branch .Lcv102_p25_end

.Lcv102_p25_end:
	s_cmp_gt_u32 s41, 2
	s_cbranch_scc0 .Lcv102_done
	s_lshl_b32 s60, s66, 2
	v_mul_lo_u32 v27, v97, s60
	s_cmp_eq_u32 s75, 0
	s_cbranch_scc1 .Lcv102_p26_bf
	v_lshl_add_u32 v27, v96, 3, v27
	v_add_u32_e32 v32, s66, v27
	v_add_u32_e32 v92, s66, v32
	v_add_u32_e32 v94, s66, v92
	v_mul_f32_e32 v66, s75, v66
	v_mul_f32_e32 v67, s75, v67
	v_mul_f32_e32 v68, s75, v68
	v_mul_f32_e32 v69, s75, v69
	v_mul_f32_e32 v70, s75, v70
	v_mul_f32_e32 v71, s75, v71
	v_mul_f32_e32 v72, s75, v72
	v_mul_f32_e32 v73, s75, v73
	v_mul_f32_e32 v74, s75, v74
	v_mul_f32_e32 v75, s75, v75
	v_mul_f32_e32 v76, s75, v76
	v_mul_f32_e32 v77, s75, v77
	v_mul_f32_e32 v78, s75, v78
	v_mul_f32_e32 v79, s75, v79
	v_mul_f32_e32 v80, s75, v80
	v_mul_f32_e32 v81, s75, v81
	v_mul_f32_e32 v82, s75, v82
	v_mul_f32_e32 v83, s75, v83
	v_mul_f32_e32 v84, s75, v84
	v_mul_f32_e32 v85, s75, v85
	v_mul_f32_e32 v86, s75, v86
	v_mul_f32_e32 v87, s75, v87
	v_mul_f32_e32 v88, s75, v88
	v_mul_f32_e32 v89, s75, v89
	v_mul_f32_e32 v102, s75, v102
	v_mul_f32_e32 v103, s75, v103
	v_mul_f32_e32 v104, s75, v104
	v_mul_f32_e32 v105, s75, v105
	v_mul_f32_e32 v106, s75, v106
	v_mul_f32_e32 v107, s75, v107
	v_mul_f32_e32 v108, s75, v108
	v_mul_f32_e32 v109, s75, v109
	v_med3_f32 v66, v66, s64, v98
	v_med3_f32 v67, v67, s64, v98
	v_med3_f32 v68, v68, s64, v98
	v_med3_f32 v69, v69, s64, v98
	v_med3_f32 v70, v70, s64, v98
	v_med3_f32 v71, v71, s64, v98
	v_med3_f32 v72, v72, s64, v98
	v_med3_f32 v73, v73, s64, v98
	v_med3_f32 v74, v74, s64, v98
	v_med3_f32 v75, v75, s64, v98
	v_med3_f32 v76, v76, s64, v98
	v_med3_f32 v77, v77, s64, v98
	v_med3_f32 v78, v78, s64, v98
	v_med3_f32 v79, v79, s64, v98
	v_med3_f32 v80, v80, s64, v98
	v_med3_f32 v81, v81, s64, v98
	v_med3_f32 v82, v82, s64, v98
	v_med3_f32 v83, v83, s64, v98
	v_med3_f32 v84, v84, s64, v98
	v_med3_f32 v85, v85, s64, v98
	v_med3_f32 v86, v86, s64, v98
	v_med3_f32 v87, v87, s64, v98
	v_med3_f32 v88, v88, s64, v98
	v_med3_f32 v89, v89, s64, v98
	v_med3_f32 v102, v102, s64, v98
	v_med3_f32 v103, v103, s64, v98
	v_med3_f32 v104, v104, s64, v98
	v_med3_f32 v105, v105, s64, v98
	v_med3_f32 v106, v106, s64, v98
	v_med3_f32 v107, v107, s64, v98
	v_med3_f32 v108, v108, s64, v98
	v_med3_f32 v109, v109, s64, v98
	v_cvt_pk_fp8_f32 v148, v66, v70
	v_cvt_pk_fp8_f32 v149, v82, v86
	v_cvt_pk_fp8_f32 v152, v67, v71
	v_cvt_pk_fp8_f32 v153, v83, v87
	v_cvt_pk_fp8_f32 v158, v68, v72
	v_cvt_pk_fp8_f32 v159, v84, v88
	v_cvt_pk_fp8_f32 v196, v69, v73
	v_cvt_pk_fp8_f32 v197, v85, v89
	v_cvt_pk_fp8_f32 v148, v74, v78 op_sel:[0,0,1]
	v_cvt_pk_fp8_f32 v149, v102, v106 op_sel:[0,0,1]
	v_cvt_pk_fp8_f32 v152, v75, v79 op_sel:[0,0,1]
	v_cvt_pk_fp8_f32 v153, v103, v107 op_sel:[0,0,1]
	v_cvt_pk_fp8_f32 v158, v76, v80 op_sel:[0,0,1]
	v_cvt_pk_fp8_f32 v159, v104, v108 op_sel:[0,0,1]
	v_cvt_pk_fp8_f32 v196, v77, v81 op_sel:[0,0,1]
	v_cvt_pk_fp8_f32 v197, v105, v109 op_sel:[0,0,1]
	s_nop 1
	global_store_dwordx2 v27, v[148:149], s[52:53]
	global_store_dwordx2 v32, v[152:153], s[52:53]
	global_store_dwordx2 v92, v[158:159], s[52:53]
	global_store_dwordx2 v94, v[196:197], s[52:53]
	s_branch .Lcv102_p26_end

.Lcv102_p26_end:
	s_cmp_gt_u32 s41, 3
	s_cbranch_scc0 .Lcv102_done
	s_lshl_b32 s60, s67, 2
	v_mul_lo_u32 v27, v97, s60
	s_cmp_eq_u32 s78, 0
	s_cbranch_scc1 .Lcv102_p27_bf
	v_lshl_add_u32 v27, v96, 3, v27
	v_add_u32_e32 v32, s67, v27
	v_add_u32_e32 v92, s67, v32
	v_add_u32_e32 v94, s67, v92
	v_mul_f32_e32 v110, s78, v110
	v_mul_f32_e32 v111, s78, v111
	v_mul_f32_e32 v112, s78, v112
	v_mul_f32_e32 v113, s78, v113
	v_mul_f32_e32 v114, s78, v114
	v_mul_f32_e32 v115, s78, v115
	v_mul_f32_e32 v116, s78, v116
	v_mul_f32_e32 v117, s78, v117
	v_mul_f32_e32 v118, s78, v118
	v_mul_f32_e32 v119, s78, v119
	v_mul_f32_e32 v120, s78, v120
	v_mul_f32_e32 v121, s78, v121
	v_mul_f32_e32 v122, s78, v122
	v_mul_f32_e32 v123, s78, v123
	v_mul_f32_e32 v124, s78, v124
	v_mul_f32_e32 v125, s78, v125
	v_mul_f32_e32 v126, s78, v126
	v_mul_f32_e32 v127, s78, v127
	v_mul_f32_e32 v128, s78, v128
	v_mul_f32_e32 v129, s78, v129
	v_mul_f32_e32 v130, s78, v130
	v_mul_f32_e32 v131, s78, v131
	v_mul_f32_e32 v132, s78, v132
	v_mul_f32_e32 v133, s78, v133
	v_mul_f32_e32 v134, s78, v134
	v_mul_f32_e32 v135, s78, v135
	v_mul_f32_e32 v136, s78, v136
	v_mul_f32_e32 v137, s78, v137
	v_mul_f32_e32 v138, s78, v138
	v_mul_f32_e32 v139, s78, v139
	v_mul_f32_e32 v140, s78, v140
	v_mul_f32_e32 v141, s78, v141
	v_med3_f32 v110, v110, s64, v98
	v_med3_f32 v111, v111, s64, v98
	v_med3_f32 v112, v112, s64, v98
	v_med3_f32 v113, v113, s64, v98
	v_med3_f32 v114, v114, s64, v98
	v_med3_f32 v115, v115, s64, v98
	v_med3_f32 v116, v116, s64, v98
	v_med3_f32 v117, v117, s64, v98
	v_med3_f32 v118, v118, s64, v98
	v_med3_f32 v119, v119, s64, v98
	v_med3_f32 v120, v120, s64, v98
	v_med3_f32 v121, v121, s64, v98
	v_med3_f32 v122, v122, s64, v98
	v_med3_f32 v123, v123, s64, v98
	v_med3_f32 v124, v124, s64, v98
	v_med3_f32 v125, v125, s64, v98
	v_med3_f32 v126, v126, s64, v98
	v_med3_f32 v127, v127, s64, v98
	v_med3_f32 v128, v128, s64, v98
	v_med3_f32 v129, v129, s64, v98
	v_med3_f32 v130, v130, s64, v98
	v_med3_f32 v131, v131, s64, v98
	v_med3_f32 v132, v132, s64, v98
	v_med3_f32 v133, v133, s64, v98
	v_med3_f32 v134, v134, s64, v98
	v_med3_f32 v135, v135, s64, v98
	v_med3_f32 v136, v136, s64, v98
	v_med3_f32 v137, v137, s64, v98
	v_med3_f32 v138, v138, s64, v98
	v_med3_f32 v139, v139, s64, v98
	v_med3_f32 v140, v140, s64, v98
	v_med3_f32 v141, v141, s64, v98
	v_cvt_pk_fp8_f32 v148, v110, v114
	v_cvt_pk_fp8_f32 v149, v126, v130
	v_cvt_pk_fp8_f32 v152, v111, v115
	v_cvt_pk_fp8_f32 v153, v127, v131
	v_cvt_pk_fp8_f32 v158, v112, v116
	v_cvt_pk_fp8_f32 v159, v128, v132
	v_cvt_pk_fp8_f32 v196, v113, v117
	v_cvt_pk_fp8_f32 v197, v129, v133
	v_cvt_pk_fp8_f32 v148, v118, v122 op_sel:[0,0,1]
	v_cvt_pk_fp8_f32 v149, v134, v138 op_sel:[0,0,1]
	v_cvt_pk_fp8_f32 v152, v119, v123 op_sel:[0,0,1]
	v_cvt_pk_fp8_f32 v153, v135, v139 op_sel:[0,0,1]
	v_cvt_pk_fp8_f32 v158, v120, v124 op_sel:[0,0,1]
	v_cvt_pk_fp8_f32 v159, v136, v140 op_sel:[0,0,1]
	v_cvt_pk_fp8_f32 v196, v121, v125 op_sel:[0,0,1]
	v_cvt_pk_fp8_f32 v197, v137, v141 op_sel:[0,0,1]
	s_nop 1
	global_store_dwordx2 v27, v[148:149], s[54:55]
	global_store_dwordx2 v32, v[152:153], s[54:55]
	global_store_dwordx2 v92, v[158:159], s[54:55]
	global_store_dwordx2 v94, v[196:197], s[54:55]
	s_branch .Lcv102_p27_end

.Lcv102_done:
.LBB0_102:
	v_lshl_add_u32 v10, s6, 6, v14
	s_movk_i32 s0, 0x1800
	v_cmp_gt_i32_e32 vcc, s0, v10
	s_and_saveexec_b64 s[0:1], vcc
	s_cbranch_execz .LBB0_153
	s_add_u32 s4, s90, 0x8300000
	s_addc_u32 s5, s91, 0
	s_lshl_b32 s7, s74, 9
	v_and_b32_e32 v11, 15, v14
	v_lshlrev_b32_e32 v12, 3, v10
	s_lshl_b32 s14, s74, 12
	s_mov_b64 s[8:9], 0
	s_mov_b32 s15, 0x55555556
	v_mov_b32_e32 v1, 0
	s_movk_i32 s16, 0x17ff
	s_branch .LBB0_105

.LBB0_301:
	s_cmp_lt_i32 s12, 4
	s_cselect_b64 s[0:1], -1, 0
	s_cmp_gt_i32 s13, 3
	s_cselect_b64 s[2:3], -1, 0
	s_and_b64 s[0:1], s[0:1], s[2:3]
	s_andn2_b64 vcc, exec, s[0:1]
	s_mov_b32 s0, s62
	v_writelane_b32 v254, s0, 59
	s_nop 1
	v_writelane_b32 v254, s1, 60
	s_cbranch_vccnz .LBB0_571
	v_readlane_b32 s0, v254, 0
	s_waitcnt vmcnt(0)
	v_mbcnt_lo_u32_b32 v0, -1, 0
	s_cmp_gt_i32 s0, 63
	v_mbcnt_hi_u32_b32 v26, -1, v0
	s_cbranch_scc1 .LBB0_459
	v_readlane_b32 s0, v254, 0
	s_lshl_b32 s0, s0, 3
	v_readlane_b32 s1, v254, 41
	s_min_i32 s7, s74, 64
	s_add_i32 s8, s1, s0
	s_lshl_b32 s6, s7, 3
	s_waitcnt lgkmcnt(9)
	v_mov_b32_e32 v14, v26
	s_cmpk_gt_i32 s8, 0x677f
	s_branch .Lcvt_site_398
.Lcvt_site_398:
	s_waitcnt vmcnt(0) lgkmcnt(0)
	v_readlane_b32 s0, v254, 42
	v_readlane_b32 s1, v254, 43
	v_readlane_b32 s60, v254, 0
	v_readlane_b32 s61, v254, 41
	s_nop 3
	s_sub_u32 s0, s0, 0xd0
	s_subb_u32 s1, s1, 0
	s_lshl_b32 s9, s60, 3
	s_add_u32 s9, s9, s61
	s_min_u32 s20, s74, 0x40
	s_lshl_b32 s20, s20, 3
	s_load_dwordx2 s[10:11], s[0:1], 0x20
	s_load_dwordx2 s[12:13], s[0:1], 0x28
	s_load_dwordx2 s[14:15], s[0:1], 0x88
	s_load_dwordx2 s[28:29], s[0:1], 0x90
	s_load_dwordx2 s[38:39], s[0:1], 0x98
	s_load_dwordx2 s[44:45], s[0:1], 0xa0
	s_load_dwordx2 s[46:47], s[0:1], 0xa8
	s_load_dwordx2 s[48:49], s[0:1], 0xb8
	v_mbcnt_lo_u32_b32 v100, -1, 0
	v_mbcnt_hi_u32_b32 v100, -1, v100
	v_and_b32_e32 v96, 7, v100
	v_lshrrev_b32_e32 v97, 3, v100
	v_mov_b32_e32 v98, 0x43e00000
	s_mov_b32 s64, 0xc3e00000
	s_waitcnt lgkmcnt(0)
	s_add_u32 s14, s14, 0x4000000
	s_addc_u32 s15, s15, 0
	s_add_u32 s28, s28, 0x4000000
	s_addc_u32 s29, s29, 0
	s_add_u32 s38, s38, 0x4000000
	s_addc_u32 s39, s39, 0
	s_add_u32 s44, s44, 0x400000
	s_addc_u32 s45, s45, 0
	s_add_u32 s46, s46, 0x100000
	s_addc_u32 s47, s47, 0
	s_add_u32 s48, s48, 0x2bd00000
	s_addc_u32 s49, s49, 0
	s_lshl_b32 s32, s9, 2
	s_lshl_b32 s20, s20, 2
	s_mov_b32 s41, 0
	s_cmp_lt_u32 s32, 0x6780
	s_cbranch_scc0 .Lcv398_drain0
	s_add_u32 s43, s32, 0
	s_cmp_lt_u32 s43, 0x300
	s_cbranch_scc0 .Lcv398_d0_b
	s_mul_i32 s58, s43, 0xaaab
	s_lshr_b32 s58, s58, 21
	s_mul_i32 s59, s58, 48
	s_sub_u32 s59, s43, s59
	s_mul_i32 s60, s58, 0x60000
	s_mul_i32 s81, s59, 0x80
	s_add_u32 s60, s60, s81
	s_add_u32 s2, s10, s60
	s_addc_u32 s3, s11, 0
	s_mov_b32 s63, 0x1800
	s_mul_i32 s61, s59, 0x8000
	s_mul_i32 s81, s58, 0x40
	s_add_u32 s61, s61, s81
	s_add_u32 s61, s61, 0x800000
	s_add_u32 s50, s48, s61
	s_addc_u32 s51, s49, 0
	s_mov_b32 s65, 0x400
	s_mov_b32 s71, 0x44000000
	s_branch .Lcv398_d0_ld
.Lcv398_d0_b:
	s_sub_u32 s43, s43, 0x300
	s_cmp_lt_u32 s43, 0x200
	s_cbranch_scc0 .Lcv398_d0_c
	s_lshr_b32 s58, s43, 5
	s_and_b32 s59, s43, 31
	s_mul_i32 s60, s58, 0x40000
	s_mul_i32 s81, s59, 0x80
	s_add_u32 s60, s60, s81
	s_add_u32 s2, s12, s60
	s_addc_u32 s3, s13, 0
	s_mov_b32 s63, 0x1000
	s_mul_i32 s61, s59, 0x8000
	s_mul_i32 s81, s58, 0x40
	s_add_u32 s61, s61, s81
	s_add_u32 s61, s61, 0xe00000
	s_add_u32 s50, s48, s61
	s_addc_u32 s51, s49, 0
	s_mov_b32 s65, 0x400
	s_mov_b32 s71, 0x44800000
	s_branch .Lcv398_d0_ld

.Lcv398_d0_ld:
	s_lshl_b32 s60, s63, 3
	v_mul_lo_u32 v0, v96, s60
	v_lshl_add_u32 v0, v97, 4, v0
	v_add_u32_e32 v4, s63, v0
	v_add_u32_e32 v10, s63, v4
	v_add_u32_e32 v11, s63, v10
	v_add_u32_e32 v12, s63, v11
	v_add_u32_e32 v19, s63, v12
	v_add_u32_e32 v24, s63, v19
	v_add_u32_e32 v25, s63, v24
	global_load_dwordx4 v[34:37], v0, s[2:3] nt
	global_load_dwordx4 v[38:41], v4, s[2:3] nt
	global_load_dwordx4 v[42:45], v10, s[2:3] nt
	global_load_dwordx4 v[46:49], v11, s[2:3] nt
	global_load_dwordx4 v[50:53], v12, s[2:3] nt
	global_load_dwordx4 v[54:57], v19, s[2:3] nt
	global_load_dwordx4 v[58:61], v24, s[2:3] nt
	global_load_dwordx4 v[62:65], v25, s[2:3] nt
	s_mov_b32 s41, 1
	s_cmp_lt_u32 s32, 0x6780
	s_cbranch_scc0 .Lcv398_drain0
	s_add_u32 s43, s32, 1
	s_cmp_lt_u32 s43, 0x300
	s_cbranch_scc0 .Lcv398_d1_b
	s_mul_i32 s58, s43, 0xaaab
	s_lshr_b32 s58, s58, 21
	s_mul_i32 s59, s58, 48
	s_sub_u32 s59, s43, s59
	s_mul_i32 s60, s58, 0x60000
	s_mul_i32 s81, s59, 0x80
	s_add_u32 s60, s60, s81
	s_add_u32 s2, s10, s60
	s_addc_u32 s3, s11, 0
	s_mov_b32 s63, 0x1800
	s_mul_i32 s61, s59, 0x8000
	s_mul_i32 s81, s58, 0x40
	s_add_u32 s61, s61, s81
	s_add_u32 s61, s61, 0x800000
	s_add_u32 s52, s48, s61
	s_addc_u32 s53, s49, 0
	s_mov_b32 s66, 0x400
	s_mov_b32 s75, 0x44000000
	s_branch .Lcv398_d1_ld
.Lcv398_d1_b:
	s_sub_u32 s43, s43, 0x300
	s_cmp_lt_u32 s43, 0x200
	s_cbranch_scc0 .Lcv398_d1_c
	s_lshr_b32 s58, s43, 5
	s_and_b32 s59, s43, 31
	s_mul_i32 s60, s58, 0x40000
	s_mul_i32 s81, s59, 0x80
	s_add_u32 s60, s60, s81
	s_add_u32 s2, s12, s60
	s_addc_u32 s3, s13, 0
	s_mov_b32 s63, 0x1000
	s_mul_i32 s61, s59, 0x8000
	s_mul_i32 s81, s58, 0x40
	s_add_u32 s61, s61, s81
	s_add_u32 s61, s61, 0xe00000
	s_add_u32 s52, s48, s61
	s_addc_u32 s53, s49, 0
	s_mov_b32 s66, 0x400
	s_mov_b32 s75, 0x44800000
	s_branch .Lcv398_d1_ld

.Lcv398_d1_ld:
	s_lshl_b32 s60, s63, 3
	v_mul_lo_u32 v0, v96, s60
	v_lshl_add_u32 v0, v97, 4, v0
	v_add_u32_e32 v4, s63, v0
	v_add_u32_e32 v10, s63, v4
	v_add_u32_e32 v11, s63, v10
	v_add_u32_e32 v12, s63, v11
	v_add_u32_e32 v19, s63, v12
	v_add_u32_e32 v24, s63, v19
	v_add_u32_e32 v25, s63, v24
	global_load_dwordx4 v[66:69], v0, s[2:3] nt
	global_load_dwordx4 v[70:73], v4, s[2:3] nt
	global_load_dwordx4 v[74:77], v10, s[2:3] nt
	global_load_dwordx4 v[78:81], v11, s[2:3] nt
	global_load_dwordx4 v[82:85], v12, s[2:3] nt
	global_load_dwordx4 v[86:89], v19, s[2:3] nt
	global_load_dwordx4 v[102:105], v24, s[2:3] nt
	global_load_dwordx4 v[106:109], v25, s[2:3] nt
	s_mov_b32 s41, 2
	s_cmp_lt_u32 s32, 0x6780
	s_cbranch_scc0 .Lcv398_drain0
	s_add_u32 s43, s32, 2
	s_cmp_lt_u32 s43, 0x300
	s_cbranch_scc0 .Lcv398_d2_b
	s_mul_i32 s58, s43, 0xaaab
	s_lshr_b32 s58, s58, 21
	s_mul_i32 s59, s58, 48
	s_sub_u32 s59, s43, s59
	s_mul_i32 s60, s58, 0x60000
	s_mul_i32 s81, s59, 0x80
	s_add_u32 s60, s60, s81
	s_add_u32 s2, s10, s60
	s_addc_u32 s3, s11, 0
	s_mov_b32 s63, 0x1800
	s_mul_i32 s61, s59, 0x8000
	s_mul_i32 s81, s58, 0x40
	s_add_u32 s61, s61, s81
	s_add_u32 s61, s61, 0x800000
	s_add_u32 s54, s48, s61
	s_addc_u32 s55, s49, 0
	s_mov_b32 s67, 0x400
	s_mov_b32 s78, 0x44000000
	s_branch .Lcv398_d2_ld
.Lcv398_d2_b:
	s_sub_u32 s43, s43, 0x300
	s_cmp_lt_u32 s43, 0x200
	s_cbranch_scc0 .Lcv398_d2_c
	s_lshr_b32 s58, s43, 5
	s_and_b32 s59, s43, 31
	s_mul_i32 s60, s58, 0x40000
	s_mul_i32 s81, s59, 0x80
	s_add_u32 s60, s60, s81
	s_add_u32 s2, s12, s60
	s_addc_u32 s3, s13, 0
	s_mov_b32 s63, 0x1000
	s_mul_i32 s61, s59, 0x8000
	s_mul_i32 s81, s58, 0x40
	s_add_u32 s61, s61, s81
	s_add_u32 s61, s61, 0xe00000
	s_add_u32 s54, s48, s61
	s_addc_u32 s55, s49, 0
	s_mov_b32 s67, 0x400
	s_mov_b32 s78, 0x44800000
	s_branch .Lcv398_d2_ld

.Lcv398_d2_ld:
	s_lshl_b32 s60, s63, 3
	v_mul_lo_u32 v0, v96, s60
	v_lshl_add_u32 v0, v97, 4, v0
	v_add_u32_e32 v4, s63, v0
	v_add_u32_e32 v10, s63, v4
	v_add_u32_e32 v11, s63, v10
	v_add_u32_e32 v12, s63, v11
	v_add_u32_e32 v19, s63, v12
	v_add_u32_e32 v24, s63, v19
	v_add_u32_e32 v25, s63, v24
	global_load_dwordx4 v[110:113], v0, s[2:3] nt
	global_load_dwordx4 v[114:117], v4, s[2:3] nt
	global_load_dwordx4 v[118:121], v10, s[2:3] nt
	global_load_dwordx4 v[122:125], v11, s[2:3] nt
	global_load_dwordx4 v[126:129], v12, s[2:3] nt
	global_load_dwordx4 v[130:133], v19, s[2:3] nt
	global_load_dwordx4 v[134:137], v24, s[2:3] nt
	global_load_dwordx4 v[138:141], v25, s[2:3] nt
	s_mov_b32 s41, 3
	s_cmp_lt_u32 s32, 0x6780
	s_cbranch_scc0 .Lcv398_drain0
	s_add_u32 s43, s32, 3
	s_cmp_lt_u32 s43, 0x300
	s_cbranch_scc0 .Lcv398_d3_b
	s_mul_i32 s58, s43, 0xaaab
	s_lshr_b32 s58, s58, 21
	s_mul_i32 s59, s58, 48
	s_sub_u32 s59, s43, s59
	s_mul_i32 s60, s58, 0x60000
	s_mul_i32 s81, s59, 0x80
	s_add_u32 s60, s60, s81
	s_add_u32 s2, s10, s60
	s_addc_u32 s3, s11, 0
	s_mov_b32 s63, 0x1800
	s_mul_i32 s61, s59, 0x8000
	s_mul_i32 s81, s58, 0x40
	s_add_u32 s61, s61, s81
	s_add_u32 s61, s61, 0x800000
	s_add_u32 s56, s48, s61
	s_addc_u32 s57, s49, 0
	s_mov_b32 s69, 0x400
	s_mov_b32 s79, 0x44000000
	s_branch .Lcv398_d3_ld
.Lcv398_d3_b:
	s_sub_u32 s43, s43, 0x300
	s_cmp_lt_u32 s43, 0x200
	s_cbranch_scc0 .Lcv398_d3_c
	s_lshr_b32 s58, s43, 5
	s_and_b32 s59, s43, 31
	s_mul_i32 s60, s58, 0x40000
	s_mul_i32 s81, s59, 0x80
	s_add_u32 s60, s60, s81
	s_add_u32 s2, s12, s60
	s_addc_u32 s3, s13, 0
	s_mov_b32 s63, 0x1000
	s_mul_i32 s61, s59, 0x8000
	s_mul_i32 s81, s58, 0x40
	s_add_u32 s61, s61, s81
	s_add_u32 s61, s61, 0xe00000
	s_add_u32 s56, s48, s61
	s_addc_u32 s57, s49, 0
	s_mov_b32 s69, 0x400
	s_mov_b32 s79, 0x44800000
	s_branch .Lcv398_d3_ld

.Lcv398_loop:
	s_cmp_lt_u32 s32, 0x6780
	s_cbranch_scc0 .Lcv398_drain0
	s_waitcnt vmcnt(24)
	s_lshl_b32 s60, s65, 2
	v_mul_lo_u32 v27, v97, s60
	s_cmp_eq_u32 s71, 0
	s_cbranch_scc1 .Lcv398_p4_bf
	v_lshl_add_u32 v27, v96, 3, v27
	v_add_u32_e32 v32, s65, v27
	v_add_u32_e32 v92, s65, v32
	v_add_u32_e32 v94, s65, v92
	v_mul_f32_e32 v34, s71, v34
	v_mul_f32_e32 v35, s71, v35
	v_mul_f32_e32 v36, s71, v36
	v_mul_f32_e32 v37, s71, v37
	v_mul_f32_e32 v38, s71, v38
	v_mul_f32_e32 v39, s71, v39
	v_mul_f32_e32 v40, s71, v40
	v_mul_f32_e32 v41, s71, v41
	v_mul_f32_e32 v42, s71, v42
	v_mul_f32_e32 v43, s71, v43
	v_mul_f32_e32 v44, s71, v44
	v_mul_f32_e32 v45, s71, v45
	v_mul_f32_e32 v46, s71, v46
	v_mul_f32_e32 v47, s71, v47
	v_mul_f32_e32 v48, s71, v48
	v_mul_f32_e32 v49, s71, v49
	v_mul_f32_e32 v50, s71, v50
	v_mul_f32_e32 v51, s71, v51
	v_mul_f32_e32 v52, s71, v52
	v_mul_f32_e32 v53, s71, v53
	v_mul_f32_e32 v54, s71, v54
	v_mul_f32_e32 v55, s71, v55
	v_mul_f32_e32 v56, s71, v56
	v_mul_f32_e32 v57, s71, v57
	v_mul_f32_e32 v58, s71, v58
	v_mul_f32_e32 v59, s71, v59
	v_mul_f32_e32 v60, s71, v60
	v_mul_f32_e32 v61, s71, v61
	v_mul_f32_e32 v62, s71, v62
	v_mul_f32_e32 v63, s71, v63
	v_mul_f32_e32 v64, s71, v64
	v_mul_f32_e32 v65, s71, v65
	v_med3_f32 v34, v34, s64, v98
	v_med3_f32 v35, v35, s64, v98
	v_med3_f32 v36, v36, s64, v98
	v_med3_f32 v37, v37, s64, v98
	v_med3_f32 v38, v38, s64, v98
	v_med3_f32 v39, v39, s64, v98
	v_med3_f32 v40, v40, s64, v98
	v_med3_f32 v41, v41, s64, v98
	v_med3_f32 v42, v42, s64, v98
	v_med3_f32 v43, v43, s64, v98
	v_med3_f32 v44, v44, s64, v98
	v_med3_f32 v45, v45, s64, v98
	v_med3_f32 v46, v46, s64, v98
	v_med3_f32 v47, v47, s64, v98
	v_med3_f32 v48, v48, s64, v98
	v_med3_f32 v49, v49, s64, v98
	v_med3_f32 v50, v50, s64, v98
	v_med3_f32 v51, v51, s64, v98
	v_med3_f32 v52, v52, s64, v98
	v_med3_f32 v53, v53, s64, v98
	v_med3_f32 v54, v54, s64, v98
	v_med3_f32 v55, v55, s64, v98
	v_med3_f32 v56, v56, s64, v98
	v_med3_f32 v57, v57, s64, v98
	v_med3_f32 v58, v58, s64, v98
	v_med3_f32 v59, v59, s64, v98
	v_med3_f32 v60, v60, s64, v98
	v_med3_f32 v61, v61, s64, v98
	v_med3_f32 v62, v62, s64, v98
	v_med3_f32 v63, v63, s64, v98
	v_med3_f32 v64, v64, s64, v98
	v_med3_f32 v65, v65, s64, v98
	v_cvt_pk_fp8_f32 v148, v34, v38
	v_cvt_pk_fp8_f32 v149, v50, v54
	v_cvt_pk_fp8_f32 v152, v35, v39
	v_cvt_pk_fp8_f32 v153, v51, v55
	v_cvt_pk_fp8_f32 v158, v36, v40
	v_cvt_pk_fp8_f32 v159, v52, v56
	v_cvt_pk_fp8_f32 v196, v37, v41
	v_cvt_pk_fp8_f32 v197, v53, v57
	v_cvt_pk_fp8_f32 v148, v42, v46 op_sel:[0,0,1]
	v_cvt_pk_fp8_f32 v149, v58, v62 op_sel:[0,0,1]
	v_cvt_pk_fp8_f32 v152, v43, v47 op_sel:[0,0,1]
	v_cvt_pk_fp8_f32 v153, v59, v63 op_sel:[0,0,1]
	v_cvt_pk_fp8_f32 v158, v44, v48 op_sel:[0,0,1]
	v_cvt_pk_fp8_f32 v159, v60, v64 op_sel:[0,0,1]
	v_cvt_pk_fp8_f32 v196, v45, v49 op_sel:[0,0,1]
	v_cvt_pk_fp8_f32 v197, v61, v65 op_sel:[0,0,1]
	s_nop 1
	global_store_dwordx2 v27, v[148:149], s[50:51]
	global_store_dwordx2 v32, v[152:153], s[50:51]
	global_store_dwordx2 v92, v[158:159], s[50:51]
	global_store_dwordx2 v94, v[196:197], s[50:51]
	s_branch .Lcv398_p4_end

.Lcv398_p4_end:
	s_add_u32 s43, s32, 0
	s_cmp_lt_u32 s43, 0x300
	s_cbranch_scc0 .Lcv398_d5_b
	s_mul_i32 s58, s43, 0xaaab
	s_lshr_b32 s58, s58, 21
	s_mul_i32 s59, s58, 48
	s_sub_u32 s59, s43, s59
	s_mul_i32 s60, s58, 0x60000
	s_mul_i32 s81, s59, 0x80
	s_add_u32 s60, s60, s81
	s_add_u32 s2, s10, s60
	s_addc_u32 s3, s11, 0
	s_mov_b32 s63, 0x1800
	s_mul_i32 s61, s59, 0x8000
	s_mul_i32 s81, s58, 0x40
	s_add_u32 s61, s61, s81
	s_add_u32 s61, s61, 0x800000
	s_add_u32 s50, s48, s61
	s_addc_u32 s51, s49, 0
	s_mov_b32 s65, 0x400
	s_mov_b32 s71, 0x44000000
	s_branch .Lcv398_d5_ld

.Lcv398_d5_ld:
	s_lshl_b32 s60, s63, 3
	v_mul_lo_u32 v0, v96, s60
	v_lshl_add_u32 v0, v97, 4, v0
	v_add_u32_e32 v4, s63, v0
	v_add_u32_e32 v10, s63, v4
	v_add_u32_e32 v11, s63, v10
	v_add_u32_e32 v12, s63, v11
	v_add_u32_e32 v19, s63, v12
	v_add_u32_e32 v24, s63, v19
	v_add_u32_e32 v25, s63, v24
	global_load_dwordx4 v[34:37], v0, s[2:3] nt
	global_load_dwordx4 v[38:41], v4, s[2:3] nt
	global_load_dwordx4 v[42:45], v10, s[2:3] nt
	global_load_dwordx4 v[46:49], v11, s[2:3] nt
	global_load_dwordx4 v[50:53], v12, s[2:3] nt
	global_load_dwordx4 v[54:57], v19, s[2:3] nt
	global_load_dwordx4 v[58:61], v24, s[2:3] nt
	global_load_dwordx4 v[62:65], v25, s[2:3] nt
	s_cmp_lt_u32 s32, 0x6780
	s_cbranch_scc0 .Lcv398_drain1
	s_waitcnt vmcnt(24)
	s_lshl_b32 s60, s66, 2
	v_mul_lo_u32 v27, v97, s60
	s_cmp_eq_u32 s75, 0
	s_cbranch_scc1 .Lcv398_p6_bf
	v_lshl_add_u32 v27, v96, 3, v27
	v_add_u32_e32 v32, s66, v27
	v_add_u32_e32 v92, s66, v32
	v_add_u32_e32 v94, s66, v92
	v_mul_f32_e32 v66, s75, v66
	v_mul_f32_e32 v67, s75, v67
	v_mul_f32_e32 v68, s75, v68
	v_mul_f32_e32 v69, s75, v69
	v_mul_f32_e32 v70, s75, v70
	v_mul_f32_e32 v71, s75, v71
	v_mul_f32_e32 v72, s75, v72
	v_mul_f32_e32 v73, s75, v73
	v_mul_f32_e32 v74, s75, v74
	v_mul_f32_e32 v75, s75, v75
	v_mul_f32_e32 v76, s75, v76
	v_mul_f32_e32 v77, s75, v77
	v_mul_f32_e32 v78, s75, v78
	v_mul_f32_e32 v79, s75, v79
	v_mul_f32_e32 v80, s75, v80
	v_mul_f32_e32 v81, s75, v81
	v_mul_f32_e32 v82, s75, v82
	v_mul_f32_e32 v83, s75, v83
	v_mul_f32_e32 v84, s75, v84
	v_mul_f32_e32 v85, s75, v85
	v_mul_f32_e32 v86, s75, v86
	v_mul_f32_e32 v87, s75, v87
	v_mul_f32_e32 v88, s75, v88
	v_mul_f32_e32 v89, s75, v89
	v_mul_f32_e32 v102, s75, v102
	v_mul_f32_e32 v103, s75, v103
	v_mul_f32_e32 v104, s75, v104
	v_mul_f32_e32 v105, s75, v105
	v_mul_f32_e32 v106, s75, v106
	v_mul_f32_e32 v107, s75, v107
	v_mul_f32_e32 v108, s75, v108
	v_mul_f32_e32 v109, s75, v109
	v_med3_f32 v66, v66, s64, v98
	v_med3_f32 v67, v67, s64, v98
	v_med3_f32 v68, v68, s64, v98
	v_med3_f32 v69, v69, s64, v98
	v_med3_f32 v70, v70, s64, v98
	v_med3_f32 v71, v71, s64, v98
	v_med3_f32 v72, v72, s64, v98
	v_med3_f32 v73, v73, s64, v98
	v_med3_f32 v74, v74, s64, v98
	v_med3_f32 v75, v75, s64, v98
	v_med3_f32 v76, v76, s64, v98
	v_med3_f32 v77, v77, s64, v98
	v_med3_f32 v78, v78, s64, v98
	v_med3_f32 v79, v79, s64, v98
	v_med3_f32 v80, v80, s64, v98
	v_med3_f32 v81, v81, s64, v98
	v_med3_f32 v82, v82, s64, v98
	v_med3_f32 v83, v83, s64, v98
	v_med3_f32 v84, v84, s64, v98
	v_med3_f32 v85, v85, s64, v98
	v_med3_f32 v86, v86, s64, v98
	v_med3_f32 v87, v87, s64, v98
	v_med3_f32 v88, v88, s64, v98
	v_med3_f32 v89, v89, s64, v98
	v_med3_f32 v102, v102, s64, v98
	v_med3_f32 v103, v103, s64, v98
	v_med3_f32 v104, v104, s64, v98
	v_med3_f32 v105, v105, s64, v98
	v_med3_f32 v106, v106, s64, v98
	v_med3_f32 v107, v107, s64, v98
	v_med3_f32 v108, v108, s64, v98
	v_med3_f32 v109, v109, s64, v98
	v_cvt_pk_fp8_f32 v148, v66, v70
	v_cvt_pk_fp8_f32 v149, v82, v86
	v_cvt_pk_fp8_f32 v152, v67, v71
	v_cvt_pk_fp8_f32 v153, v83, v87
	v_cvt_pk_fp8_f32 v158, v68, v72
	v_cvt_pk_fp8_f32 v159, v84, v88
	v_cvt_pk_fp8_f32 v196, v69, v73
	v_cvt_pk_fp8_f32 v197, v85, v89
	v_cvt_pk_fp8_f32 v148, v74, v78 op_sel:[0,0,1]
	v_cvt_pk_fp8_f32 v149, v102, v106 op_sel:[0,0,1]
	v_cvt_pk_fp8_f32 v152, v75, v79 op_sel:[0,0,1]
	v_cvt_pk_fp8_f32 v153, v103, v107 op_sel:[0,0,1]
	v_cvt_pk_fp8_f32 v158, v76, v80 op_sel:[0,0,1]
	v_cvt_pk_fp8_f32 v159, v104, v108 op_sel:[0,0,1]
	v_cvt_pk_fp8_f32 v196, v77, v81 op_sel:[0,0,1]
	v_cvt_pk_fp8_f32 v197, v105, v109 op_sel:[0,0,1]
	s_nop 1
	global_store_dwordx2 v27, v[148:149], s[52:53]
	global_store_dwordx2 v32, v[152:153], s[52:53]
	global_store_dwordx2 v92, v[158:159], s[52:53]
	global_store_dwordx2 v94, v[196:197], s[52:53]
	s_branch .Lcv398_p6_end

.Lcv398_p6_end:
	s_add_u32 s43, s32, 1
	s_cmp_lt_u32 s43, 0x300
	s_cbranch_scc0 .Lcv398_d7_b
	s_mul_i32 s58, s43, 0xaaab
	s_lshr_b32 s58, s58, 21
	s_mul_i32 s59, s58, 48
	s_sub_u32 s59, s43, s59
	s_mul_i32 s60, s58, 0x60000
	s_mul_i32 s81, s59, 0x80
	s_add_u32 s60, s60, s81
	s_add_u32 s2, s10, s60
	s_addc_u32 s3, s11, 0
	s_mov_b32 s63, 0x1800
	s_mul_i32 s61, s59, 0x8000
	s_mul_i32 s81, s58, 0x40
	s_add_u32 s61, s61, s81
	s_add_u32 s61, s61, 0x800000
	s_add_u32 s52, s48, s61
	s_addc_u32 s53, s49, 0
	s_mov_b32 s66, 0x400
	s_mov_b32 s75, 0x44000000
	s_branch .Lcv398_d7_ld

.Lcv398_d7_ld:
	s_lshl_b32 s60, s63, 3
	v_mul_lo_u32 v0, v96, s60
	v_lshl_add_u32 v0, v97, 4, v0
	v_add_u32_e32 v4, s63, v0
	v_add_u32_e32 v10, s63, v4
	v_add_u32_e32 v11, s63, v10
	v_add_u32_e32 v12, s63, v11
	v_add_u32_e32 v19, s63, v12
	v_add_u32_e32 v24, s63, v19
	v_add_u32_e32 v25, s63, v24
	global_load_dwordx4 v[66:69], v0, s[2:3] nt
	global_load_dwordx4 v[70:73], v4, s[2:3] nt
	global_load_dwordx4 v[74:77], v10, s[2:3] nt
	global_load_dwordx4 v[78:81], v11, s[2:3] nt
	global_load_dwordx4 v[82:85], v12, s[2:3] nt
	global_load_dwordx4 v[86:89], v19, s[2:3] nt
	global_load_dwordx4 v[102:105], v24, s[2:3] nt
	global_load_dwordx4 v[106:109], v25, s[2:3] nt
	s_cmp_lt_u32 s32, 0x6780
	s_cbranch_scc0 .Lcv398_drain2
	s_waitcnt vmcnt(24)
	s_lshl_b32 s60, s67, 2
	v_mul_lo_u32 v27, v97, s60
	s_cmp_eq_u32 s78, 0
	s_cbranch_scc1 .Lcv398_p8_bf
	v_lshl_add_u32 v27, v96, 3, v27
	v_add_u32_e32 v32, s67, v27
	v_add_u32_e32 v92, s67, v32
	v_add_u32_e32 v94, s67, v92
	v_mul_f32_e32 v110, s78, v110
	v_mul_f32_e32 v111, s78, v111
	v_mul_f32_e32 v112, s78, v112
	v_mul_f32_e32 v113, s78, v113
	v_mul_f32_e32 v114, s78, v114
	v_mul_f32_e32 v115, s78, v115
	v_mul_f32_e32 v116, s78, v116
	v_mul_f32_e32 v117, s78, v117
	v_mul_f32_e32 v118, s78, v118
	v_mul_f32_e32 v119, s78, v119
	v_mul_f32_e32 v120, s78, v120
	v_mul_f32_e32 v121, s78, v121
	v_mul_f32_e32 v122, s78, v122
	v_mul_f32_e32 v123, s78, v123
	v_mul_f32_e32 v124, s78, v124
	v_mul_f32_e32 v125, s78, v125
	v_mul_f32_e32 v126, s78, v126
	v_mul_f32_e32 v127, s78, v127
	v_mul_f32_e32 v128, s78, v128
	v_mul_f32_e32 v129, s78, v129
	v_mul_f32_e32 v130, s78, v130
	v_mul_f32_e32 v131, s78, v131
	v_mul_f32_e32 v132, s78, v132
	v_mul_f32_e32 v133, s78, v133
	v_mul_f32_e32 v134, s78, v134
	v_mul_f32_e32 v135, s78, v135
	v_mul_f32_e32 v136, s78, v136
	v_mul_f32_e32 v137, s78, v137
	v_mul_f32_e32 v138, s78, v138
	v_mul_f32_e32 v139, s78, v139
	v_mul_f32_e32 v140, s78, v140
	v_mul_f32_e32 v141, s78, v141
	v_med3_f32 v110, v110, s64, v98
	v_med3_f32 v111, v111, s64, v98
	v_med3_f32 v112, v112, s64, v98
	v_med3_f32 v113, v113, s64, v98
	v_med3_f32 v114, v114, s64, v98
	v_med3_f32 v115, v115, s64, v98
	v_med3_f32 v116, v116, s64, v98
	v_med3_f32 v117, v117, s64, v98
	v_med3_f32 v118, v118, s64, v98
	v_med3_f32 v119, v119, s64, v98
	v_med3_f32 v120, v120, s64, v98
	v_med3_f32 v121, v121, s64, v98
	v_med3_f32 v122, v122, s64, v98
	v_med3_f32 v123, v123, s64, v98
	v_med3_f32 v124, v124, s64, v98
	v_med3_f32 v125, v125, s64, v98
	v_med3_f32 v126, v126, s64, v98
	v_med3_f32 v127, v127, s64, v98
	v_med3_f32 v128, v128, s64, v98
	v_med3_f32 v129, v129, s64, v98
	v_med3_f32 v130, v130, s64, v98
	v_med3_f32 v131, v131, s64, v98
	v_med3_f32 v132, v132, s64, v98
	v_med3_f32 v133, v133, s64, v98
	v_med3_f32 v134, v134, s64, v98
	v_med3_f32 v135, v135, s64, v98
	v_med3_f32 v136, v136, s64, v98
	v_med3_f32 v137, v137, s64, v98
	v_med3_f32 v138, v138, s64, v98
	v_med3_f32 v139, v139, s64, v98
	v_med3_f32 v140, v140, s64, v98
	v_med3_f32 v141, v141, s64, v98
	v_cvt_pk_fp8_f32 v148, v110, v114
	v_cvt_pk_fp8_f32 v149, v126, v130
	v_cvt_pk_fp8_f32 v152, v111, v115
	v_cvt_pk_fp8_f32 v153, v127, v131
	v_cvt_pk_fp8_f32 v158, v112, v116
	v_cvt_pk_fp8_f32 v159, v128, v132
	v_cvt_pk_fp8_f32 v196, v113, v117
	v_cvt_pk_fp8_f32 v197, v129, v133
	v_cvt_pk_fp8_f32 v148, v118, v122 op_sel:[0,0,1]
	v_cvt_pk_fp8_f32 v149, v134, v138 op_sel:[0,0,1]
	v_cvt_pk_fp8_f32 v152, v119, v123 op_sel:[0,0,1]
	v_cvt_pk_fp8_f32 v153, v135, v139 op_sel:[0,0,1]
	v_cvt_pk_fp8_f32 v158, v120, v124 op_sel:[0,0,1]
	v_cvt_pk_fp8_f32 v159, v136, v140 op_sel:[0,0,1]
	v_cvt_pk_fp8_f32 v196, v121, v125 op_sel:[0,0,1]
	v_cvt_pk_fp8_f32 v197, v137, v141 op_sel:[0,0,1]
	s_nop 1
	global_store_dwordx2 v27, v[148:149], s[54:55]
	global_store_dwordx2 v32, v[152:153], s[54:55]
	global_store_dwordx2 v92, v[158:159], s[54:55]
	global_store_dwordx2 v94, v[196:197], s[54:55]
	s_branch .Lcv398_p8_end

.Lcv398_p8_end:
	s_add_u32 s43, s32, 2
	s_cmp_lt_u32 s43, 0x300
	s_cbranch_scc0 .Lcv398_d9_b
	s_mul_i32 s58, s43, 0xaaab
	s_lshr_b32 s58, s58, 21
	s_mul_i32 s59, s58, 48
	s_sub_u32 s59, s43, s59
	s_mul_i32 s60, s58, 0x60000
	s_mul_i32 s81, s59, 0x80
	s_add_u32 s60, s60, s81
	s_add_u32 s2, s10, s60
	s_addc_u32 s3, s11, 0
	s_mov_b32 s63, 0x1800
	s_mul_i32 s61, s59, 0x8000
	s_mul_i32 s81, s58, 0x40
	s_add_u32 s61, s61, s81
	s_add_u32 s61, s61, 0x800000
	s_add_u32 s54, s48, s61
	s_addc_u32 s55, s49, 0
	s_mov_b32 s67, 0x400
	s_mov_b32 s78, 0x44000000
	s_branch .Lcv398_d9_ld

.Lcv398_d9_ld:
	s_lshl_b32 s60, s63, 3
	v_mul_lo_u32 v0, v96, s60
	v_lshl_add_u32 v0, v97, 4, v0
	v_add_u32_e32 v4, s63, v0
	v_add_u32_e32 v10, s63, v4
	v_add_u32_e32 v11, s63, v10
	v_add_u32_e32 v12, s63, v11
	v_add_u32_e32 v19, s63, v12
	v_add_u32_e32 v24, s63, v19
	v_add_u32_e32 v25, s63, v24
	global_load_dwordx4 v[110:113], v0, s[2:3] nt
	global_load_dwordx4 v[114:117], v4, s[2:3] nt
	global_load_dwordx4 v[118:121], v10, s[2:3] nt
	global_load_dwordx4 v[122:125], v11, s[2:3] nt
	global_load_dwordx4 v[126:129], v12, s[2:3] nt
	global_load_dwordx4 v[130:133], v19, s[2:3] nt
	global_load_dwordx4 v[134:137], v24, s[2:3] nt
	global_load_dwordx4 v[138:141], v25, s[2:3] nt
	s_cmp_lt_u32 s32, 0x6780
	s_cbranch_scc0 .Lcv398_drain3
	s_waitcnt vmcnt(24)
	s_lshl_b32 s60, s69, 2
	v_mul_lo_u32 v27, v97, s60
	s_cmp_eq_u32 s79, 0
	s_cbranch_scc1 .Lcv398_p10_bf
	v_lshl_add_u32 v27, v96, 3, v27
	v_add_u32_e32 v32, s69, v27
	v_add_u32_e32 v92, s69, v32
	v_add_u32_e32 v94, s69, v92
	v_mul_f32_e32 v142, s79, v142
	v_mul_f32_e32 v143, s79, v143
	v_mul_f32_e32 v144, s79, v144
	v_mul_f32_e32 v145, s79, v145
	v_mul_f32_e32 v172, s79, v172
	v_mul_f32_e32 v173, s79, v173
	v_mul_f32_e32 v174, s79, v174
	v_mul_f32_e32 v175, s79, v175
	v_mul_f32_e32 v176, s79, v176
	v_mul_f32_e32 v177, s79, v177
	v_mul_f32_e32 v178, s79, v178
	v_mul_f32_e32 v179, s79, v179
	v_mul_f32_e32 v180, s79, v180
	v_mul_f32_e32 v181, s79, v181
	v_mul_f32_e32 v182, s79, v182
	v_mul_f32_e32 v183, s79, v183
	v_mul_f32_e32 v184, s79, v184
	v_mul_f32_e32 v185, s79, v185
	v_mul_f32_e32 v186, s79, v186
	v_mul_f32_e32 v187, s79, v187
	v_mul_f32_e32 v188, s79, v188
	v_mul_f32_e32 v189, s79, v189
	v_mul_f32_e32 v190, s79, v190
	v_mul_f32_e32 v191, s79, v191
	v_mul_f32_e32 v162, s79, v162
	v_mul_f32_e32 v163, s79, v163
	v_mul_f32_e32 v164, s79, v164
	v_mul_f32_e32 v165, s79, v165
	v_mul_f32_e32 v6, s79, v6
	v_mul_f32_e32 v7, s79, v7
	v_mul_f32_e32 v8, s79, v8
	v_mul_f32_e32 v9, s79, v9
	v_med3_f32 v142, v142, s64, v98
	v_med3_f32 v143, v143, s64, v98
	v_med3_f32 v144, v144, s64, v98
	v_med3_f32 v145, v145, s64, v98
	v_med3_f32 v172, v172, s64, v98
	v_med3_f32 v173, v173, s64, v98
	v_med3_f32 v174, v174, s64, v98
	v_med3_f32 v175, v175, s64, v98
	v_med3_f32 v176, v176, s64, v98
	v_med3_f32 v177, v177, s64, v98
	v_med3_f32 v178, v178, s64, v98
	v_med3_f32 v179, v179, s64, v98
	v_med3_f32 v180, v180, s64, v98
	v_med3_f32 v181, v181, s64, v98
	v_med3_f32 v182, v182, s64, v98
	v_med3_f32 v183, v183, s64, v98
	v_med3_f32 v184, v184, s64, v98
	v_med3_f32 v185, v185, s64, v98
	v_med3_f32 v186, v186, s64, v98
	v_med3_f32 v187, v187, s64, v98
	v_med3_f32 v188, v188, s64, v98
	v_med3_f32 v189, v189, s64, v98
	v_med3_f32 v190, v190, s64, v98
	v_med3_f32 v191, v191, s64, v98
	v_med3_f32 v162, v162, s64, v98
	v_med3_f32 v163, v163, s64, v98
	v_med3_f32 v164, v164, s64, v98
	v_med3_f32 v165, v165, s64, v98
	v_med3_f32 v6, v6, s64, v98
	v_med3_f32 v7, v7, s64, v98
	v_med3_f32 v8, v8, s64, v98
	v_med3_f32 v9, v9, s64, v98
	v_cvt_pk_fp8_f32 v148, v142, v172
	v_cvt_pk_fp8_f32 v149, v184, v188
	v_cvt_pk_fp8_f32 v152, v143, v173
	v_cvt_pk_fp8_f32 v153, v185, v189
	v_cvt_pk_fp8_f32 v158, v144, v174
	v_cvt_pk_fp8_f32 v159, v186, v190
	v_cvt_pk_fp8_f32 v196, v145, v175
	v_cvt_pk_fp8_f32 v197, v187, v191
	v_cvt_pk_fp8_f32 v148, v176, v180 op_sel:[0,0,1]
	v_cvt_pk_fp8_f32 v149, v162, v6 op_sel:[0,0,1]
	v_cvt_pk_fp8_f32 v152, v177, v181 op_sel:[0,0,1]
	v_cvt_pk_fp8_f32 v153, v163, v7 op_sel:[0,0,1]
	v_cvt_pk_fp8_f32 v158, v178, v182 op_sel:[0,0,1]
	v_cvt_pk_fp8_f32 v159, v164, v8 op_sel:[0,0,1]
	v_cvt_pk_fp8_f32 v196, v179, v183 op_sel:[0,0,1]
	v_cvt_pk_fp8_f32 v197, v165, v9 op_sel:[0,0,1]
	s_nop 1
	global_store_dwordx2 v27, v[148:149], s[56:57]
	global_store_dwordx2 v32, v[152:153], s[56:57]
	global_store_dwordx2 v92, v[158:159], s[56:57]
	global_store_dwordx2 v94, v[196:197], s[56:57]
	s_branch .Lcv398_p10_end

.Lcv398_p10_end:
	s_add_u32 s43, s32, 3
	s_cmp_lt_u32 s43, 0x300
	s_cbranch_scc0 .Lcv398_d11_b
	s_mul_i32 s58, s43, 0xaaab
	s_lshr_b32 s58, s58, 21
	s_mul_i32 s59, s58, 48
	s_sub_u32 s59, s43, s59
	s_mul_i32 s60, s58, 0x60000
	s_mul_i32 s81, s59, 0x80
	s_add_u32 s60, s60, s81
	s_add_u32 s2, s10, s60
	s_addc_u32 s3, s11, 0
	s_mov_b32 s63, 0x1800
	s_mul_i32 s61, s59, 0x8000
	s_mul_i32 s81, s58, 0x40
	s_add_u32 s61, s61, s81
	s_add_u32 s61, s61, 0x800000
	s_add_u32 s56, s48, s61
	s_addc_u32 s57, s49, 0
	s_mov_b32 s69, 0x400
	s_mov_b32 s79, 0x44000000
	s_branch .Lcv398_d11_ld

.Lcv398_done:
.LBB0_398:
	v_lshl_add_u32 v10, s8, 6, v14
	s_movk_i32 s0, 0x1800
	v_cmp_gt_i32_e32 vcc, s0, v10
	s_and_saveexec_b64 s[0:1], vcc
	s_cbranch_execz .LBB0_449
	v_readlane_b32 s12, v254, 22
	v_readlane_b32 s22, v254, 32
	v_readlane_b32 s23, v254, 33
	s_add_u32 s10, s22, 0x4000
	v_readlane_b32 s26, v254, 36
	s_addc_u32 s11, s23, 0
	v_readlane_b32 s13, v254, 23
	v_readlane_b32 s27, v254, 37
	s_add_u32 s12, s26, 0x20000
	v_readlane_b32 s14, v254, 24
	s_addc_u32 s13, s27, 0
	v_readlane_b32 s15, v254, 25
	v_readlane_b32 s16, v254, 26
	v_readlane_b32 s17, v254, 27
	v_readlane_b32 s24, v254, 34
	v_readlane_b32 s25, v254, 35
	s_add_u32 s14, s90, 0x34000000
	s_addc_u32 s15, s91, 0
	s_lshl_b32 s9, s7, 9
	v_and_b32_e32 v11, 15, v14
	v_lshlrev_b32_e32 v12, 3, v10
	s_lshl_b32 s7, s7, 12
	s_mov_b64 s[24:25], 0
	s_mov_b32 s16, 0x55555556
	v_mov_b32_e32 v1, 0
	s_movk_i32 s17, 0x17ff
	v_readlane_b32 s18, v254, 28
	v_readlane_b32 s19, v254, 29
	v_readlane_b32 s20, v254, 30
	v_readlane_b32 s21, v254, 31
	s_branch .LBB0_401

.LBB0_1236:
	s_cmp_lt_i32 s12, 14
	s_cselect_b64 s[0:1], -1, 0
	s_cmp_gt_i32 s13, 13
	s_cselect_b64 s[2:3], -1, 0
	s_and_b64 s[0:1], s[0:1], s[2:3]
	s_andn2_b64 vcc, exec, s[0:1]
	s_cbranch_vccnz .LBB0_1483
	v_readlane_b32 s0, v254, 0
	v_mbcnt_lo_u32_b32 v0, -1, 0
	s_cmp_gt_i32 s0, 0x7f
	v_mbcnt_hi_u32_b32 v26, -1, v0
	s_cbranch_scc1 .LBB0_1394
	v_readlane_b32 s0, v254, 0
	s_lshl_b32 s0, s0, 3
	v_readlane_b32 s1, v254, 41
	s_min_i32 s5, s74, 0x80
	s_add_i32 s6, s1, s0
	s_lshl_b32 s4, s5, 3
	s_waitcnt lgkmcnt(0)
	v_mov_b32_e32 v14, v26
	s_cmpk_gt_i32 s6, 0x6a7f
	s_branch .Lcvt_site_1333
.Lcvt_site_1333:
	s_waitcnt vmcnt(0) lgkmcnt(0)
	v_readlane_b32 s0, v254, 42
	v_readlane_b32 s1, v254, 43
	v_readlane_b32 s60, v254, 0
	v_readlane_b32 s61, v254, 41
	s_nop 3
	s_sub_u32 s0, s0, 0xd0
	s_subb_u32 s1, s1, 0
	s_lshl_b32 s9, s60, 3
	s_add_u32 s9, s9, s61
	s_min_u32 s20, s74, 0x80
	s_lshl_b32 s20, s20, 3
	s_load_dwordx2 s[10:11], s[0:1], 0x38
	s_load_dwordx2 s[12:13], s[0:1], 0x40
	s_load_dwordx2 s[14:15], s[0:1], 0x88
	s_load_dwordx2 s[28:29], s[0:1], 0x90
	s_load_dwordx2 s[38:39], s[0:1], 0x98
	s_load_dwordx2 s[44:45], s[0:1], 0xa0
	s_load_dwordx2 s[46:47], s[0:1], 0xa8
	s_load_dwordx2 s[48:49], s[0:1], 0xb8
	v_mbcnt_lo_u32_b32 v100, -1, 0
	v_mbcnt_hi_u32_b32 v100, -1, v100
	v_and_b32_e32 v96, 7, v100
	v_lshrrev_b32_e32 v97, 3, v100
	v_mov_b32_e32 v98, 0x43e00000
	s_mov_b32 s64, 0xc3e00000
	s_waitcnt lgkmcnt(0)
	s_add_u32 s14, s14, 0x8000000
	s_addc_u32 s15, s15, 0
	s_add_u32 s28, s28, 0x8000000
	s_addc_u32 s29, s29, 0
	s_add_u32 s38, s38, 0x8000000
	s_addc_u32 s39, s39, 0
	s_add_u32 s44, s44, 0x800000
	s_addc_u32 s45, s45, 0
	s_add_u32 s46, s46, 0x200000
	s_addc_u32 s47, s47, 0
	s_lshl_b32 s32, s9, 2
	s_lshl_b32 s20, s20, 2
	s_mov_b32 s41, 0
	s_cmp_lt_u32 s32, 0x6a80
	s_cbranch_scc0 .Lcv1333_drain0
	s_add_u32 s43, s32, 0
	s_cmp_lt_u32 s43, 0x600
	s_cbranch_scc0 .Lcv1333_d0_b
	s_mul_i32 s58, s43, 0xaaab
	s_lshr_b32 s58, s58, 22
	s_mul_i32 s59, s58, 96
	s_sub_u32 s59, s43, s59
	s_mul_i32 s60, s58, 0xc0000
	s_mul_i32 s81, s59, 0x80
	s_add_u32 s60, s60, s81
	s_add_u32 s2, s10, s60
	s_addc_u32 s3, s11, 0
	s_mov_b32 s63, 0x3000
	s_mul_i32 s61, s59, 0x8000
	s_mul_i32 s81, s58, 0x40
	s_add_u32 s61, s61, s81
	s_add_u32 s61, s61, 0x800000
	s_add_u32 s50, s48, s61
	s_addc_u32 s51, s49, 0
	s_mov_b32 s65, 0x400
	s_mov_b32 s71, 0x44000000
	s_branch .Lcv1333_d0_ld

.Lcv1333_done:
.LBB0_1333:
	v_lshl_add_u32 v10, s6, 6, v14
	s_movk_i32 s0, 0x1800
	v_cmp_gt_i32_e32 vcc, s0, v10
	s_and_saveexec_b64 s[0:1], vcc
	s_cbranch_execz .LBB0_1384
	v_readlane_b32 s8, v254, 22
	v_readlane_b32 s18, v254, 32
	v_readlane_b32 s9, v254, 23
	v_readlane_b32 s19, v254, 33
	s_add_u32 s8, s18, 0x8000
	v_readlane_b32 s10, v254, 24
	v_readlane_b32 s22, v254, 36
	s_addc_u32 s9, s19, 0
	v_readlane_b32 s11, v254, 25
	v_readlane_b32 s23, v254, 37
	s_add_u32 s10, s22, 0x40000
	v_readlane_b32 s12, v254, 26
	s_addc_u32 s11, s23, 0
	v_readlane_b32 s13, v254, 27
	v_readlane_b32 s14, v254, 28
	v_readlane_b32 s15, v254, 29
	s_add_u32 s12, s90, 0x8300000
	s_addc_u32 s13, s91, 0
	s_lshl_b32 s7, s5, 9
	v_and_b32_e32 v11, 15, v14
	v_lshlrev_b32_e32 v12, 3, v10
	s_lshl_b32 s5, s5, 12
	s_mov_b64 s[14:15], 0
	s_mov_b32 s18, 0x55555556
	v_mov_b32_e32 v1, 0
	s_movk_i32 s19, 0x17ff
	v_readlane_b32 s16, v254, 30
	v_readlane_b32 s17, v254, 31
	v_readlane_b32 s20, v254, 34
	v_readlane_b32 s21, v254, 35
	s_branch .LBB0_1336

.LBB0_2113:
	s_cmp_lt_i32 s12, 24
	s_cselect_b64 s[0:1], -1, 0
	s_cmp_gt_i32 s13, 23
	s_cselect_b64 s[2:3], -1, 0
	s_and_b64 s[0:1], s[0:1], s[2:3]
	s_andn2_b64 vcc, exec, s[0:1]
	s_cbranch_vccnz .LBB0_2362
	v_readlane_b32 s0, v254, 0
	v_mbcnt_lo_u32_b32 v0, -1, 0
	s_cmp_gt_i32 s0, 63
	v_mbcnt_hi_u32_b32 v26, -1, v0
	s_cbranch_scc1 .LBB0_2271
	v_readlane_b32 s0, v254, 0
	s_lshl_b32 s0, s0, 3
	v_readlane_b32 s1, v254, 41
	s_min_i32 s5, s74, 64
	s_add_i32 s6, s1, s0
	s_lshl_b32 s4, s5, 3
	s_waitcnt lgkmcnt(0)
	v_mov_b32_e32 v14, v26
	s_cmpk_gt_i32 s6, 0x6a7f
	s_branch .Lcvt_site_2210
.Lcvt_site_2210:
	s_waitcnt vmcnt(0) lgkmcnt(0)
	v_readlane_b32 s0, v254, 42
	v_readlane_b32 s1, v254, 43
	v_readlane_b32 s60, v254, 0
	v_readlane_b32 s61, v254, 41
	s_nop 3
	s_sub_u32 s0, s0, 0xd0
	s_subb_u32 s1, s1, 0
	s_lshl_b32 s9, s60, 3
	s_add_u32 s9, s9, s61
	s_min_u32 s20, s74, 0x40
	s_lshl_b32 s20, s20, 3
	s_load_dwordx2 s[10:11], s[0:1], 0x10
	s_load_dwordx2 s[12:13], s[0:1], 0x18
	s_load_dwordx2 s[14:15], s[0:1], 0x88
	s_load_dwordx2 s[28:29], s[0:1], 0x90
	s_load_dwordx2 s[38:39], s[0:1], 0x98
	s_load_dwordx2 s[44:45], s[0:1], 0xa0
	s_load_dwordx2 s[46:47], s[0:1], 0xa8
	s_load_dwordx2 s[48:49], s[0:1], 0xb8
	v_mbcnt_lo_u32_b32 v100, -1, 0
	v_mbcnt_hi_u32_b32 v100, -1, v100
	v_and_b32_e32 v96, 7, v100
	v_lshrrev_b32_e32 v97, 3, v100
	v_mov_b32_e32 v98, 0x43e00000
	s_mov_b32 s64, 0xc3e00000
	s_waitcnt lgkmcnt(0)
	s_add_u32 s10, s10, 0xc00000
	s_addc_u32 s11, s11, 0
	s_add_u32 s12, s12, 0x400000
	s_addc_u32 s13, s13, 0
	s_add_u32 s14, s14, 0xc000000
	s_addc_u32 s15, s15, 0
	s_add_u32 s28, s28, 0xc000000
	s_addc_u32 s29, s29, 0
	s_add_u32 s38, s38, 0xc000000
	s_addc_u32 s39, s39, 0
	s_add_u32 s44, s44, 0xc00000
	s_addc_u32 s45, s45, 0
	s_add_u32 s46, s46, 0x300000
	s_addc_u32 s47, s47, 0
	s_add_u32 s48, s48, 0x2bd00000
	s_addc_u32 s49, s49, 0
	s_lshl_b32 s32, s9, 2
	s_lshl_b32 s20, s20, 2
	s_mov_b32 s41, 0
	s_cmp_lt_u32 s32, 0x6a80
	s_cbranch_scc0 .Lcv2210_drain0
	s_add_u32 s43, s32, 0
	s_cmp_lt_u32 s43, 0x600
	s_cbranch_scc0 .Lcv2210_d0_b
	s_mul_i32 s58, s43, 0xaaab
	s_lshr_b32 s58, s58, 22
	s_mul_i32 s59, s58, 96
	s_sub_u32 s59, s43, s59
	s_mul_i32 s60, s58, 0xc0000
	s_mul_i32 s81, s59, 0x80
	s_add_u32 s60, s60, s81
	s_add_u32 s2, s10, s60
	s_addc_u32 s3, s11, 0
	s_mov_b32 s63, 0x3000
	s_mul_i32 s61, s59, 0x8000
	s_mul_i32 s81, s58, 0x40
	s_add_u32 s61, s61, s81
	s_add_u32 s61, s61, 0x800000
	s_add_u32 s50, s48, s61
	s_addc_u32 s51, s49, 0
	s_mov_b32 s65, 0x400
	s_mov_b32 s71, 0x44000000
	s_branch .Lcv2210_d0_ld

.Lcv2210_done:
.LBB0_2210:
	v_lshl_add_u32 v10, s6, 6, v14
	s_movk_i32 s0, 0x1800
	v_cmp_gt_i32_e32 vcc, s0, v10
	s_and_saveexec_b64 s[0:1], vcc
	s_cbranch_execz .LBB0_2261
	v_readlane_b32 s8, v254, 22
	v_readlane_b32 s18, v254, 32
	v_readlane_b32 s9, v254, 23
	v_readlane_b32 s19, v254, 33
	s_add_u32 s8, s18, 0xc000
	v_readlane_b32 s10, v254, 24
	v_readlane_b32 s22, v254, 36
	s_addc_u32 s9, s19, 0
	v_readlane_b32 s11, v254, 25
	v_readlane_b32 s23, v254, 37
	s_add_u32 s10, s22, 0x60000
	v_readlane_b32 s12, v254, 26
	s_addc_u32 s11, s23, 0
	v_readlane_b32 s13, v254, 27
	v_readlane_b32 s14, v254, 28
	v_readlane_b32 s15, v254, 29
	s_add_u32 s12, s90, 0x34000000
	s_addc_u32 s13, s91, 0
	s_lshl_b32 s7, s5, 9
	v_and_b32_e32 v11, 15, v14
	v_lshlrev_b32_e32 v12, 3, v10
	s_lshl_b32 s5, s5, 12
	s_mov_b64 s[14:15], 0
	s_mov_b32 s18, 0x55555556
	v_mov_b32_e32 v1, 0
	s_movk_i32 s19, 0x17ff
	v_readlane_b32 s16, v254, 30
	v_readlane_b32 s17, v254, 31
	v_readlane_b32 s20, v254, 34
	v_readlane_b32 s21, v254, 35
	s_branch .LBB0_2213
